# all 16-byte global stores made write-through (sc1) so the grid barriers' L2 write-back has less dirty data to flush
# baseline (speedup 1.0000x reference)
.LBB0_43:
	s_and_saveexec_b64 s[20:21], s[6:7]
	s_cbranch_execz .LBB0_8
	v_mov_b32_e32 v5, s19
	v_or_b32_e32 v4, s18, v70
	s_ashr_i32 s17, s16, 31
	v_lshl_add_u64 v[80:81], s[16:17], 1, v[74:75]
	v_lshlrev_b64 v[4:5], 12, v[4:5]
	v_lshl_add_u64 v[88:89], v[80:81], 0, v[4:5]
	s_waitcnt vmcnt(0)
	v_cvt_pk_bf16_f32 v80, v6, v10
	v_cvt_pk_bf16_f32 v81, v14, v18
	v_cvt_pk_bf16_f32 v82, v22, v26
	v_cvt_pk_bf16_f32 v83, v30, v34
	v_add_co_u32_e32 v10, vcc, s22, v88
	v_cvt_pk_bf16_f32 v84, v38, v42
	v_cvt_pk_bf16_f32 v85, v46, v50
	v_cvt_pk_bf16_f32 v86, v54, v58
	v_cvt_pk_bf16_f32 v87, v62, v66
	global_store_dwordx4 v[88:89], v[80:83], off sc1
	global_store_dwordx4 v[88:89], v[84:87], off offset:16 sc1
	v_cvt_pk_bf16_f32 v4, v7, v11
	v_addc_co_u32_e32 v11, vcc, 0, v89, vcc
	v_add_co_u32_e32 v14, vcc, s23, v88
	v_cvt_pk_bf16_f32 v5, v15, v19
	v_cvt_pk_bf16_f32 v6, v23, v27
	v_cvt_pk_bf16_f32 v7, v31, v35
	v_cvt_pk_bf16_f32 v80, v39, v43
	s_nop 1
	v_addc_co_u32_e32 v15, vcc, 0, v89, vcc
	v_cvt_pk_bf16_f32 v81, v47, v51
	v_cvt_pk_bf16_f32 v82, v55, v59
	v_cvt_pk_bf16_f32 v83, v63, v67
	global_store_dwordx4 v[14:15], v[4:7], off offset:-4096 sc1
	global_store_dwordx4 v[10:11], v[80:83], off offset:16 sc1
	s_nop 0
	v_cvt_pk_bf16_f32 v4, v8, v12
	v_cvt_pk_bf16_f32 v5, v16, v20
	v_cvt_pk_bf16_f32 v6, v24, v28
	v_cvt_pk_bf16_f32 v7, v32, v36
	v_add_co_u32_e32 v12, vcc, 0x3000, v88
	v_cvt_pk_bf16_f32 v80, v40, v44
	v_cvt_pk_bf16_f32 v81, v48, v52
	v_cvt_pk_bf16_f32 v82, v56, v60
	v_cvt_pk_bf16_f32 v83, v64, v68
	global_store_dwordx4 v[14:15], v[4:7], off sc1
	global_store_dwordx4 v[14:15], v[80:83], off offset:16 sc1
	s_nop 0
	v_cvt_pk_bf16_f32 v4, v9, v13
	v_cvt_pk_bf16_f32 v5, v17, v21
	v_cvt_pk_bf16_f32 v6, v25, v29
	v_cvt_pk_bf16_f32 v7, v33, v37
	v_addc_co_u32_e32 v13, vcc, 0, v89, vcc
	v_cvt_pk_bf16_f32 v8, v41, v45
	v_cvt_pk_bf16_f32 v9, v49, v53
	v_cvt_pk_bf16_f32 v10, v57, v61
	v_cvt_pk_bf16_f32 v11, v65, v69
	global_store_dwordx4 v[12:13], v[4:7], off sc1
	global_store_dwordx4 v[12:13], v[8:11], off offset:16 sc1
	s_branch .LBB0_8

.LBB0_131:
	v_lshl_add_u32 v3, s12, 8, v208
	v_lshl_or_b32 v132, s14, 8, v210
	v_ashrrev_i32_e32 v134, 31, v3
	v_ashrrev_i32_e32 v133, 31, v132
	v_mul_lo_u32 v136, s16, v134
	v_mul_lo_u32 v137, s17, v3
	v_mad_u64_u32 v[134:135], s[2:3], s16, v3, 0
	v_lshl_add_u64 v[132:133], v[132:133], 1, s[18:19]
	v_add3_u32 v135, v135, v136, v137
	v_lshl_add_u64 v[134:135], v[134:135], 1, v[132:133]
	v_cvt_pk_bf16_f32 v128, v128, v129
	v_cvt_pk_bf16_f32 v129, v130, v131
	v_cvt_pk_bf16_f32 v130, v124, v125
	v_cvt_pk_bf16_f32 v131, v126, v127
	global_store_dwordx4 v[134:135], v[128:131], off sc1
	v_cvt_pk_bf16_f32 v116, v116, v117
	v_cvt_pk_bf16_f32 v117, v118, v119
	v_cvt_pk_bf16_f32 v118, v108, v109
	v_or_b32_e32 v108, 16, v3
	v_cvt_pk_bf16_f32 v119, v110, v111
	v_mul_lo_u32 v110, s17, v108
	v_mad_u64_u32 v[108:109], s[2:3], s16, v108, 0
	v_add3_u32 v109, v109, v136, v110
	global_store_dwordx4 v[134:135], v[116:119], off offset:256 sc1
	s_cmp_eq_u32 s12, s43
	s_nop 0
	v_lshl_add_u64 v[116:117], v[108:109], 1, v[132:133]
	v_cvt_pk_bf16_f32 v108, v120, v121
	v_cvt_pk_bf16_f32 v109, v122, v123
	v_cvt_pk_bf16_f32 v110, v112, v113
	v_cvt_pk_bf16_f32 v111, v114, v115
	global_store_dwordx4 v[116:117], v[108:111], off sc1
	v_cvt_pk_bf16_f32 v100, v100, v101
	v_cvt_pk_bf16_f32 v101, v102, v103
	v_cvt_pk_bf16_f32 v102, v92, v93
	v_or_b32_e32 v92, 32, v3
	v_cvt_pk_bf16_f32 v103, v94, v95
	v_mul_lo_u32 v94, s17, v92
	v_mad_u64_u32 v[92:93], s[2:3], s16, v92, 0
	v_add3_u32 v93, v93, v136, v94
	global_store_dwordx4 v[116:117], v[100:103], off offset:256 sc1
	s_nop 1
	v_lshl_add_u64 v[100:101], v[92:93], 1, v[132:133]
	v_cvt_pk_bf16_f32 v92, v104, v105
	v_cvt_pk_bf16_f32 v93, v106, v107
	v_cvt_pk_bf16_f32 v94, v96, v97
	v_cvt_pk_bf16_f32 v95, v98, v99
	global_store_dwordx4 v[100:101], v[92:95], off sc1
	v_cvt_pk_bf16_f32 v84, v84, v85
	v_cvt_pk_bf16_f32 v85, v86, v87
	v_cvt_pk_bf16_f32 v86, v76, v77
	v_or_b32_e32 v76, 48, v3
	v_cvt_pk_bf16_f32 v87, v78, v79
	v_mul_lo_u32 v78, s17, v76
	v_mad_u64_u32 v[76:77], s[2:3], s16, v76, 0
	v_add3_u32 v77, v77, v136, v78
	global_store_dwordx4 v[100:101], v[84:87], off offset:256 sc1
	s_nop 1
	v_lshl_add_u64 v[84:85], v[76:77], 1, v[132:133]
	v_cvt_pk_bf16_f32 v76, v88, v89
	v_cvt_pk_bf16_f32 v77, v90, v91
	v_cvt_pk_bf16_f32 v78, v80, v81
	v_cvt_pk_bf16_f32 v79, v82, v83
	global_store_dwordx4 v[84:85], v[76:79], off sc1
	v_cvt_pk_bf16_f32 v72, v72, v73
	v_cvt_pk_bf16_f32 v73, v74, v75
	v_cvt_pk_bf16_f32 v74, v68, v69
	v_add_u32_e32 v68, 0x80, v3
	v_ashrrev_i32_e32 v69, 31, v68
	v_cvt_pk_bf16_f32 v75, v70, v71
	v_mul_lo_u32 v70, s16, v69
	v_mul_lo_u32 v71, s17, v68
	v_mad_u64_u32 v[68:69], s[2:3], s16, v68, 0
	v_add3_u32 v69, v69, v70, v71
	v_lshl_add_u64 v[68:69], v[68:69], 1, v[132:133]
	global_store_dwordx4 v[84:85], v[72:75], off offset:256 sc1
	v_cvt_pk_bf16_f32 v64, v64, v65
	v_cvt_pk_bf16_f32 v65, v66, v67
	v_cvt_pk_bf16_f32 v66, v60, v61
	v_cvt_pk_bf16_f32 v67, v62, v63
	global_store_dwordx4 v[68:69], v[64:67], off sc1
	v_cvt_pk_bf16_f32 v56, v56, v57
	v_cvt_pk_bf16_f32 v57, v58, v59
	v_cvt_pk_bf16_f32 v58, v48, v49
	v_add_u32_e32 v48, 0x90, v3
	v_ashrrev_i32_e32 v49, 31, v48
	v_cvt_pk_bf16_f32 v59, v50, v51
	v_mul_lo_u32 v50, s16, v49
	v_mul_lo_u32 v51, s17, v48
	v_mad_u64_u32 v[48:49], s[2:3], s16, v48, 0
	v_add3_u32 v49, v49, v50, v51
	global_store_dwordx4 v[68:69], v[56:59], off offset:256 sc1
	s_nop 1
	v_lshl_add_u64 v[56:57], v[48:49], 1, v[132:133]
	v_cvt_pk_bf16_f32 v48, v52, v53
	v_cvt_pk_bf16_f32 v49, v54, v55
	v_cvt_pk_bf16_f32 v50, v44, v45
	v_cvt_pk_bf16_f32 v51, v46, v47
	global_store_dwordx4 v[56:57], v[48:51], off sc1
	v_cvt_pk_bf16_f32 v40, v40, v41
	v_cvt_pk_bf16_f32 v41, v42, v43
	v_cvt_pk_bf16_f32 v42, v32, v33
	v_add_u32_e32 v32, 0xa0, v3
	v_ashrrev_i32_e32 v33, 31, v32
	v_cvt_pk_bf16_f32 v43, v34, v35
	v_mul_lo_u32 v34, s16, v33
	v_mul_lo_u32 v35, s17, v32
	v_mad_u64_u32 v[32:33], s[2:3], s16, v32, 0
	v_add3_u32 v33, v33, v34, v35
	global_store_dwordx4 v[56:57], v[40:43], off offset:256 sc1
	v_add_u32_e32 v3, 0xb0, v3
	s_nop 0
	v_lshl_add_u64 v[40:41], v[32:33], 1, v[132:133]
	v_cvt_pk_bf16_f32 v32, v36, v37
	v_cvt_pk_bf16_f32 v33, v38, v39
	v_cvt_pk_bf16_f32 v34, v28, v29
	v_cvt_pk_bf16_f32 v35, v30, v31
	global_store_dwordx4 v[40:41], v[32:35], off sc1
	v_cvt_pk_bf16_f32 v24, v24, v25
	v_cvt_pk_bf16_f32 v25, v26, v27
	v_cvt_pk_bf16_f32 v26, v16, v17
	v_ashrrev_i32_e32 v16, 31, v3
	v_cvt_pk_bf16_f32 v27, v18, v19
	v_mul_lo_u32 v18, s16, v16
	v_mad_u64_u32 v[16:17], s[2:3], s16, v3, 0
	s_cselect_b64 s[2:3], -1, 0
	s_cmp_eq_u32 s4, s49
	v_mul_lo_u32 v19, s17, v3
	s_cselect_b64 s[4:5], -1, 0
	v_add3_u32 v17, v17, v18, v19
	s_and_b64 s[2:3], s[2:3], s[4:5]
	global_store_dwordx4 v[40:41], v[24:27], off offset:256 sc1
	s_andn2_b64 vcc, exec, s[2:3]
	s_nop 0
	v_lshl_add_u64 v[24:25], v[16:17], 1, v[132:133]
	v_cvt_pk_bf16_f32 v16, v20, v21
	v_cvt_pk_bf16_f32 v17, v22, v23
	v_cvt_pk_bf16_f32 v18, v12, v13
	v_cvt_pk_bf16_f32 v19, v14, v15
	global_store_dwordx4 v[24:25], v[16:19], off sc1
	v_cvt_pk_bf16_f32 v8, v8, v9
	v_cvt_pk_bf16_f32 v9, v10, v11
	v_cvt_pk_bf16_f32 v10, v4, v5
	v_cvt_pk_bf16_f32 v11, v6, v7
	global_store_dwordx4 v[24:25], v[8:11], off offset:256 sc1
	s_cbranch_vccnz .LBB0_324
	v_readlane_b32 s2, v252, 30
	v_readlane_b32 s3, v252, 31
	s_andn2_b64 vcc, exec, s[2:3]
	v_readlane_b32 s2, v252, 13
	s_mov_b32 s59, 1
	s_mov_b32 s61, s94
	s_mov_b32 s4, s2
	v_readlane_b32 s3, v252, 14
	s_cbranch_vccnz .LBB0_136
	v_readlane_b32 s2, v252, 33
	v_readlane_b32 s3, v252, 34
	s_andn2_b64 vcc, exec, s[2:3]
	v_readlane_b32 s61, v252, 29
	s_cbranch_vccnz .LBB0_135
	s_mov_b32 s59, 3
	v_readlane_b32 s61, v252, 35

.LBB0_142:
	s_waitcnt lgkmcnt(0)
	s_ashr_i32 s12, s24, 31
	s_lshr_b32 s12, s12, 27
	s_add_i32 s12, s24, s12
	s_ashr_i32 s14, s12, 5
	s_lshl_b32 s15, s14, 11
	s_sub_i32 s12, s2, s15
	v_add_u32_e32 v3, s12, v172
	v_cmp_gt_i32_e32 vcc, s22, v3
	s_and_saveexec_b64 s[12:13], vcc
	s_cbranch_execz .LBB0_141
	s_load_dwordx2 s[68:69], s[0:1], 0x30
	s_lshl_b32 s14, s14, 6
	v_or_b32_e32 v4, s14, v174
	s_sub_i32 s15, 0, s15
	v_ashrrev_i32_e32 v5, 31, v4
	s_add_i32 s18, s2, s15
	v_lshlrev_b64 v[4:5], 13, v[4:5]
	s_waitcnt lgkmcnt(0)
	v_lshl_add_u64 v[4:5], s[68:69], 0, v[4:5]
	s_ashr_i32 s19, s18, 31
	v_lshl_add_u64 v[4:5], s[18:19], 2, v[4:5]
	s_waitcnt vmcnt(0)
	v_lshlrev_b32_e32 v6, 2, v172
	v_mov_b32_e32 v7, v2
	v_lshl_add_u64 v[60:61], v[4:5], 0, v[6:7]
	v_add_co_u32_e32 v8, vcc, s29, v60
	v_mov_b32_e32 v69, s19
	s_nop 0
	v_addc_co_u32_e32 v9, vcc, 0, v61, vcc
	v_add_co_u32_e32 v12, vcc, s37, v60
	global_load_dwordx4 v[4:7], v[60:61], off
	s_nop 0
	global_load_dwordx4 v[8:11], v[8:9], off
	v_addc_co_u32_e32 v13, vcc, 0, v61, vcc
	v_add_co_u32_e32 v16, vcc, s20, v60
	v_or_b32_e32 v68, s18, v172
	s_nop 0
	v_addc_co_u32_e32 v17, vcc, 0, v61, vcc
	v_add_co_u32_e32 v20, vcc, s31, v60
	global_load_dwordx4 v[12:15], v[12:13], off
	s_nop 0
	global_load_dwordx4 v[16:19], v[16:17], off
	v_addc_co_u32_e32 v21, vcc, 0, v61, vcc
	v_add_co_u32_e32 v24, vcc, s33, v60
	s_ashr_i32 s15, s14, 31
	s_nop 0
	v_addc_co_u32_e32 v25, vcc, 0, v61, vcc
	v_add_co_u32_e32 v28, vcc, s48, v60
	global_load_dwordx4 v[20:23], v[20:21], off
	s_nop 0
	global_load_dwordx4 v[24:27], v[24:25], off
	v_addc_co_u32_e32 v29, vcc, 0, v61, vcc
	v_add_co_u32_e32 v32, vcc, s28, v60
	v_lshl_add_u64 v[70:71], s[14:15], 1, v[188:189]
	s_nop 0
	v_addc_co_u32_e32 v33, vcc, 0, v61, vcc
	v_add_co_u32_e32 v36, vcc, s51, v60
	global_load_dwordx4 v[28:31], v[28:29], off
	s_nop 0
	global_load_dwordx4 v[32:35], v[32:33], off
	v_addc_co_u32_e32 v37, vcc, 0, v61, vcc
	v_add_co_u32_e32 v40, vcc, s34, v60
	v_lshlrev_b64 v[68:69], 12, v[68:69]
	s_nop 0
	v_addc_co_u32_e32 v41, vcc, 0, v61, vcc
	v_add_co_u32_e32 v44, vcc, s35, v60
	global_load_dwordx4 v[36:39], v[36:37], off
	s_nop 0
	global_load_dwordx4 v[40:43], v[40:41], off
	v_addc_co_u32_e32 v45, vcc, 0, v61, vcc
	v_add_co_u32_e32 v48, vcc, s36, v60
	v_lshl_add_u64 v[76:77], v[70:71], 0, v[68:69]
	s_nop 0
	v_addc_co_u32_e32 v49, vcc, 0, v61, vcc
	v_add_co_u32_e32 v52, vcc, s21, v60
	global_load_dwordx4 v[44:47], v[44:45], off
	s_nop 0
	global_load_dwordx4 v[48:51], v[48:49], off
	v_addc_co_u32_e32 v53, vcc, 0, v61, vcc
	v_add_co_u32_e32 v56, vcc, s30, v60
	s_nop 1
	v_addc_co_u32_e32 v57, vcc, 0, v61, vcc
	v_add_co_u32_e32 v62, vcc, s26, v60
	global_load_dwordx4 v[52:55], v[52:53], off
	s_nop 0
	global_load_dwordx4 v[56:59], v[56:57], off
	v_addc_co_u32_e32 v63, vcc, 0, v61, vcc
	v_add_co_u32_e32 v64, vcc, s27, v60
	s_nop 1
	v_addc_co_u32_e32 v65, vcc, 0, v61, vcc
	global_load_dwordx4 v[60:63], v[62:63], off
	s_nop 0
	global_load_dwordx4 v[64:67], v[64:65], off
	s_waitcnt vmcnt(0)
	v_cvt_pk_bf16_f32 v68, v4, v8
	v_cvt_pk_bf16_f32 v69, v12, v16
	v_cvt_pk_bf16_f32 v70, v20, v24
	v_cvt_pk_bf16_f32 v71, v28, v32
	v_add_co_u32_e32 v4, vcc, s23, v76
	v_cvt_pk_bf16_f32 v72, v36, v40
	v_cvt_pk_bf16_f32 v73, v44, v48
	v_cvt_pk_bf16_f32 v74, v52, v56
	v_cvt_pk_bf16_f32 v75, v60, v64
	global_store_dwordx4 v[76:77], v[68:71], off sc1
	global_store_dwordx4 v[76:77], v[72:75], off offset:16 sc1
	s_nop 0
	v_cvt_pk_bf16_f32 v68, v5, v9
	v_addc_co_u32_e32 v5, vcc, 0, v77, vcc
	v_add_co_u32_e32 v8, vcc, s29, v76
	v_cvt_pk_bf16_f32 v69, v13, v17
	v_cvt_pk_bf16_f32 v70, v21, v25
	v_cvt_pk_bf16_f32 v71, v29, v33
	v_cvt_pk_bf16_f32 v72, v37, v41
	s_nop 1
	v_addc_co_u32_e32 v9, vcc, 0, v77, vcc
	v_cvt_pk_bf16_f32 v73, v45, v49
	v_cvt_pk_bf16_f32 v74, v53, v57
	v_cvt_pk_bf16_f32 v75, v61, v65
	global_store_dwordx4 v[8:9], v[68:71], off offset:-4096 sc1
	global_store_dwordx4 v[4:5], v[72:75], off offset:16 sc1
	v_add_co_u32_e32 v12, vcc, 0x3000, v76
	v_cvt_pk_bf16_f32 v68, v6, v10
	v_cvt_pk_bf16_f32 v69, v14, v18
	v_cvt_pk_bf16_f32 v70, v22, v26
	v_cvt_pk_bf16_f32 v71, v30, v34
	s_nop 0
	v_cvt_pk_bf16_f32 v72, v38, v42
	v_cvt_pk_bf16_f32 v73, v46, v50
	v_cvt_pk_bf16_f32 v74, v54, v58
	v_cvt_pk_bf16_f32 v75, v62, v66
	global_store_dwordx4 v[8:9], v[68:71], off sc1
	global_store_dwordx4 v[8:9], v[72:75], off offset:16 sc1
	v_cvt_pk_bf16_f32 v4, v7, v11
	v_cvt_pk_bf16_f32 v5, v15, v19
	v_cvt_pk_bf16_f32 v6, v23, v27
	v_cvt_pk_bf16_f32 v7, v31, v35
	v_addc_co_u32_e32 v13, vcc, 0, v77, vcc
	v_cvt_pk_bf16_f32 v8, v39, v43
	v_cvt_pk_bf16_f32 v9, v47, v51
	v_cvt_pk_bf16_f32 v10, v55, v59
	v_cvt_pk_bf16_f32 v11, v63, v67
	global_store_dwordx4 v[12:13], v[4:7], off sc1
	global_store_dwordx4 v[12:13], v[8:11], off offset:16 sc1
	s_branch .LBB0_141

.LBB0_179:
	s_and_saveexec_b64 s[72:73], s[12:13]
	s_cbranch_execz .LBB0_144
	v_mov_b32_e32 v5, s71
	v_or_b32_e32 v4, s70, v172
	s_ashr_i32 s69, s68, 31
	v_lshl_add_u64 v[72:73], s[68:69], 1, v[190:191]
	v_lshlrev_b64 v[4:5], 12, v[4:5]
	v_lshl_add_u64 v[80:81], v[72:73], 0, v[4:5]
	s_waitcnt vmcnt(0)
	v_cvt_pk_bf16_f32 v72, v6, v10
	v_cvt_pk_bf16_f32 v73, v14, v18
	v_cvt_pk_bf16_f32 v74, v22, v26
	v_cvt_pk_bf16_f32 v75, v30, v34
	v_add_co_u32_e32 v10, vcc, s23, v80
	v_cvt_pk_bf16_f32 v76, v38, v42
	v_cvt_pk_bf16_f32 v77, v46, v50
	v_cvt_pk_bf16_f32 v78, v54, v58
	v_cvt_pk_bf16_f32 v79, v62, v66
	global_store_dwordx4 v[80:81], v[72:75], off sc1
	global_store_dwordx4 v[80:81], v[76:79], off offset:16 sc1
	v_cvt_pk_bf16_f32 v4, v7, v11
	v_addc_co_u32_e32 v11, vcc, 0, v81, vcc
	v_add_co_u32_e32 v14, vcc, s29, v80
	v_cvt_pk_bf16_f32 v5, v15, v19
	v_cvt_pk_bf16_f32 v6, v23, v27
	v_cvt_pk_bf16_f32 v7, v31, v35
	v_cvt_pk_bf16_f32 v72, v39, v43
	s_nop 1
	v_addc_co_u32_e32 v15, vcc, 0, v81, vcc
	v_cvt_pk_bf16_f32 v73, v47, v51
	v_cvt_pk_bf16_f32 v74, v55, v59
	v_cvt_pk_bf16_f32 v75, v63, v67
	global_store_dwordx4 v[14:15], v[4:7], off offset:-4096 sc1
	global_store_dwordx4 v[10:11], v[72:75], off offset:16 sc1
	s_nop 0
	v_cvt_pk_bf16_f32 v4, v8, v12
	v_cvt_pk_bf16_f32 v5, v16, v20
	v_cvt_pk_bf16_f32 v6, v24, v28
	v_cvt_pk_bf16_f32 v7, v32, v36
	v_add_co_u32_e32 v12, vcc, 0x3000, v80
	v_cvt_pk_bf16_f32 v72, v40, v44
	v_cvt_pk_bf16_f32 v73, v48, v52
	v_cvt_pk_bf16_f32 v74, v56, v60
	v_cvt_pk_bf16_f32 v75, v64, v68
	global_store_dwordx4 v[14:15], v[4:7], off sc1
	global_store_dwordx4 v[14:15], v[72:75], off offset:16 sc1
	s_nop 0
	v_cvt_pk_bf16_f32 v4, v9, v13
	v_cvt_pk_bf16_f32 v5, v17, v21
	v_cvt_pk_bf16_f32 v6, v25, v29
	v_cvt_pk_bf16_f32 v7, v33, v37
	v_addc_co_u32_e32 v13, vcc, 0, v81, vcc
	v_cvt_pk_bf16_f32 v8, v41, v45
	v_cvt_pk_bf16_f32 v9, v49, v53
	v_cvt_pk_bf16_f32 v10, v57, v61
	v_cvt_pk_bf16_f32 v11, v65, v69
	global_store_dwordx4 v[12:13], v[4:7], off sc1
	global_store_dwordx4 v[12:13], v[8:11], off offset:16 sc1
	s_branch .LBB0_144

.LBB0_218:
	s_and_saveexec_b64 s[70:71], s[12:13]
	s_cbranch_execz .LBB0_183
	s_add_i32 s2, s68, 0x200
	s_ashr_i32 s12, s2, 31
	v_mov_b32_e32 v5, s12
	v_or_b32_e32 v4, s2, v172
	s_ashr_i32 s19, s18, 31
	v_lshl_add_u64 v[74:75], s[18:19], 1, v[190:191]
	v_lshlrev_b64 v[4:5], 12, v[4:5]
	v_lshl_add_u64 v[82:83], v[74:75], 0, v[4:5]
	s_waitcnt vmcnt(0)
	v_cvt_pk_bf16_f32 v74, v6, v10
	v_cvt_pk_bf16_f32 v75, v14, v18
	v_cvt_pk_bf16_f32 v76, v22, v26
	v_cvt_pk_bf16_f32 v77, v30, v34
	v_add_co_u32_e32 v10, vcc, s23, v82
	v_cvt_pk_bf16_f32 v78, v38, v42
	v_cvt_pk_bf16_f32 v79, v46, v50
	v_cvt_pk_bf16_f32 v80, v54, v58
	v_cvt_pk_bf16_f32 v81, v62, v66
	global_store_dwordx4 v[82:83], v[74:77], off sc1
	global_store_dwordx4 v[82:83], v[78:81], off offset:16 sc1
	v_cvt_pk_bf16_f32 v4, v7, v11
	v_addc_co_u32_e32 v11, vcc, 0, v83, vcc
	v_add_co_u32_e32 v14, vcc, s29, v82
	v_cvt_pk_bf16_f32 v5, v15, v19
	v_cvt_pk_bf16_f32 v6, v23, v27
	v_cvt_pk_bf16_f32 v7, v31, v35
	v_cvt_pk_bf16_f32 v74, v39, v43
	s_nop 1
	v_addc_co_u32_e32 v15, vcc, 0, v83, vcc
	v_cvt_pk_bf16_f32 v75, v47, v51
	v_cvt_pk_bf16_f32 v76, v55, v59
	v_cvt_pk_bf16_f32 v77, v63, v67
	global_store_dwordx4 v[14:15], v[4:7], off offset:-4096 sc1
	global_store_dwordx4 v[10:11], v[74:77], off offset:16 sc1
	s_nop 0
	v_cvt_pk_bf16_f32 v4, v8, v12
	v_cvt_pk_bf16_f32 v5, v16, v20
	v_cvt_pk_bf16_f32 v6, v24, v28
	v_cvt_pk_bf16_f32 v7, v32, v36
	v_add_co_u32_e32 v12, vcc, 0x3000, v82
	v_cvt_pk_bf16_f32 v74, v40, v44
	v_cvt_pk_bf16_f32 v75, v48, v52
	v_cvt_pk_bf16_f32 v76, v56, v60
	v_cvt_pk_bf16_f32 v77, v64, v68
	global_store_dwordx4 v[14:15], v[4:7], off sc1
	global_store_dwordx4 v[14:15], v[74:77], off offset:16 sc1
	s_nop 0
	v_cvt_pk_bf16_f32 v4, v9, v13
	v_cvt_pk_bf16_f32 v5, v17, v21
	v_cvt_pk_bf16_f32 v6, v25, v29
	v_cvt_pk_bf16_f32 v7, v33, v37
	v_addc_co_u32_e32 v13, vcc, 0, v83, vcc
	v_cvt_pk_bf16_f32 v8, v41, v45
	v_cvt_pk_bf16_f32 v9, v49, v53
	v_cvt_pk_bf16_f32 v10, v57, v61
	v_cvt_pk_bf16_f32 v11, v65, v69
	global_store_dwordx4 v[12:13], v[4:7], off sc1
	global_store_dwordx4 v[12:13], v[8:11], off offset:16 sc1
	s_branch .LBB0_183

.LBB0_222:
	s_ashr_i32 s12, s18, 31
	s_lshr_b32 s12, s12, 27
	s_add_i32 s12, s18, s12
	s_ashr_i32 s14, s12, 5
	s_lshl_b32 s15, s14, 11
	s_sub_i32 s12, s2, s15
	v_add_u32_e32 v3, s12, v172
	v_cmp_gt_i32_e32 vcc, s22, v3
	s_and_saveexec_b64 s[12:13], vcc
	s_cbranch_execz .LBB0_221
	s_load_dwordx2 s[68:69], s[0:1], 0x78
	s_lshl_b32 s14, s14, 6
	v_or_b32_e32 v4, s14, v174
	s_sub_i32 s15, 0, s15
	v_ashrrev_i32_e32 v5, 31, v4
	s_add_i32 s16, s2, s15
	v_lshlrev_b64 v[4:5], 13, v[4:5]
	s_waitcnt lgkmcnt(0)
	v_lshl_add_u64 v[4:5], s[68:69], 0, v[4:5]
	s_ashr_i32 s17, s16, 31
	v_lshl_add_u64 v[4:5], s[16:17], 2, v[4:5]
	v_mov_b32_e32 v71, v2
	s_waitcnt vmcnt(0)
	v_lshl_add_u64 v[60:61], v[4:5], 0, v[70:71]
	v_add_co_u32_e32 v8, vcc, s29, v60
	v_mov_b32_e32 v69, s17
	s_nop 0
	v_addc_co_u32_e32 v9, vcc, 0, v61, vcc
	v_add_co_u32_e32 v12, vcc, s37, v60
	global_load_dwordx4 v[4:7], v[60:61], off
	s_nop 0
	global_load_dwordx4 v[8:11], v[8:9], off
	v_addc_co_u32_e32 v13, vcc, 0, v61, vcc
	v_add_co_u32_e32 v16, vcc, s20, v60
	v_or_b32_e32 v68, s16, v172
	s_nop 0
	v_addc_co_u32_e32 v17, vcc, 0, v61, vcc
	v_add_co_u32_e32 v20, vcc, s31, v60
	global_load_dwordx4 v[12:15], v[12:13], off
	s_nop 0
	global_load_dwordx4 v[16:19], v[16:17], off
	v_addc_co_u32_e32 v21, vcc, 0, v61, vcc
	v_add_co_u32_e32 v24, vcc, s33, v60
	s_ashr_i32 s15, s14, 31
	s_nop 0
	v_addc_co_u32_e32 v25, vcc, 0, v61, vcc
	v_add_co_u32_e32 v28, vcc, s48, v60
	global_load_dwordx4 v[20:23], v[20:21], off
	s_nop 0
	global_load_dwordx4 v[24:27], v[24:25], off
	v_addc_co_u32_e32 v29, vcc, 0, v61, vcc
	v_add_co_u32_e32 v32, vcc, s28, v60
	v_lshl_add_u64 v[72:73], s[14:15], 1, v[192:193]
	s_nop 0
	v_addc_co_u32_e32 v33, vcc, 0, v61, vcc
	v_add_co_u32_e32 v36, vcc, s51, v60
	global_load_dwordx4 v[28:31], v[28:29], off
	s_nop 0
	global_load_dwordx4 v[32:35], v[32:33], off
	v_addc_co_u32_e32 v37, vcc, 0, v61, vcc
	v_add_co_u32_e32 v40, vcc, s34, v60
	v_lshlrev_b64 v[68:69], 12, v[68:69]
	s_nop 0
	v_addc_co_u32_e32 v41, vcc, 0, v61, vcc
	v_add_co_u32_e32 v44, vcc, s35, v60
	global_load_dwordx4 v[36:39], v[36:37], off
	s_nop 0
	global_load_dwordx4 v[40:43], v[40:41], off
	v_addc_co_u32_e32 v45, vcc, 0, v61, vcc
	v_add_co_u32_e32 v48, vcc, s36, v60
	v_lshl_add_u64 v[68:69], v[72:73], 0, v[68:69]
	s_nop 0
	v_addc_co_u32_e32 v49, vcc, 0, v61, vcc
	v_add_co_u32_e32 v52, vcc, s21, v60
	global_load_dwordx4 v[44:47], v[44:45], off
	s_nop 0
	global_load_dwordx4 v[48:51], v[48:49], off
	v_addc_co_u32_e32 v53, vcc, 0, v61, vcc
	v_add_co_u32_e32 v56, vcc, s30, v60
	s_nop 1
	v_addc_co_u32_e32 v57, vcc, 0, v61, vcc
	v_add_co_u32_e32 v62, vcc, s26, v60
	global_load_dwordx4 v[52:55], v[52:53], off
	s_nop 0
	global_load_dwordx4 v[56:59], v[56:57], off
	v_addc_co_u32_e32 v63, vcc, 0, v61, vcc
	v_add_co_u32_e32 v64, vcc, s27, v60
	s_nop 1
	v_addc_co_u32_e32 v65, vcc, 0, v61, vcc
	global_load_dwordx4 v[60:63], v[62:63], off
	s_nop 0
	global_load_dwordx4 v[64:67], v[64:65], off
	s_waitcnt vmcnt(14)
	v_cvt_pk_bf16_f32 v72, v4, v8
	s_waitcnt vmcnt(12)
	v_cvt_pk_bf16_f32 v73, v12, v16
	s_waitcnt vmcnt(10)
	v_cvt_pk_bf16_f32 v74, v20, v24
	s_waitcnt vmcnt(8)
	v_cvt_pk_bf16_f32 v75, v28, v32
	v_add_co_u32_e32 v4, vcc, s23, v68
	s_waitcnt vmcnt(6)
	v_cvt_pk_bf16_f32 v76, v36, v40
	s_waitcnt vmcnt(4)
	v_cvt_pk_bf16_f32 v77, v44, v48
	s_waitcnt vmcnt(2)
	v_cvt_pk_bf16_f32 v78, v52, v56
	s_waitcnt vmcnt(0)
	v_cvt_pk_bf16_f32 v79, v60, v64
	global_store_dwordx4 v[68:69], v[72:75], off sc1
	global_store_dwordx4 v[68:69], v[76:79], off offset:16 sc1
	s_nop 0
	v_cvt_pk_bf16_f32 v72, v5, v9
	v_addc_co_u32_e32 v5, vcc, 0, v69, vcc
	v_add_co_u32_e32 v8, vcc, s29, v68
	v_cvt_pk_bf16_f32 v73, v13, v17
	v_cvt_pk_bf16_f32 v74, v21, v25
	v_cvt_pk_bf16_f32 v75, v29, v33
	v_cvt_pk_bf16_f32 v76, v37, v41
	s_nop 1
	v_addc_co_u32_e32 v9, vcc, 0, v69, vcc
	v_cvt_pk_bf16_f32 v77, v45, v49
	v_cvt_pk_bf16_f32 v78, v53, v57
	v_cvt_pk_bf16_f32 v79, v61, v65
	global_store_dwordx4 v[8:9], v[72:75], off offset:-4096 sc1
	global_store_dwordx4 v[4:5], v[76:79], off offset:16 sc1
	v_add_co_u32_e32 v12, vcc, 0x3000, v68
	v_cvt_pk_bf16_f32 v72, v6, v10
	v_cvt_pk_bf16_f32 v73, v14, v18
	v_cvt_pk_bf16_f32 v74, v22, v26
	v_cvt_pk_bf16_f32 v75, v30, v34
	s_nop 0
	v_cvt_pk_bf16_f32 v76, v38, v42
	v_cvt_pk_bf16_f32 v77, v46, v50
	v_cvt_pk_bf16_f32 v78, v54, v58
	v_cvt_pk_bf16_f32 v79, v62, v66
	global_store_dwordx4 v[8:9], v[72:75], off sc1
	global_store_dwordx4 v[8:9], v[76:79], off offset:16 sc1
	v_cvt_pk_bf16_f32 v4, v7, v11
	v_cvt_pk_bf16_f32 v5, v15, v19
	v_cvt_pk_bf16_f32 v6, v23, v27
	v_cvt_pk_bf16_f32 v7, v31, v35
	v_addc_co_u32_e32 v13, vcc, 0, v69, vcc
	v_cvt_pk_bf16_f32 v8, v39, v43
	v_cvt_pk_bf16_f32 v9, v47, v51
	v_cvt_pk_bf16_f32 v10, v55, v59
	v_cvt_pk_bf16_f32 v11, v63, v67
	global_store_dwordx4 v[12:13], v[4:7], off sc1
	global_store_dwordx4 v[12:13], v[8:11], off offset:16 sc1
	s_branch .LBB0_221

.LBB0_263:
	s_and_saveexec_b64 s[72:73], s[6:7]
	s_cbranch_execz .LBB0_228
	s_ashr_i32 s71, s70, 31
	v_lshl_add_u64 v[88:89], s[70:71], 1, v[76:77]
	s_waitcnt vmcnt(0)
	v_cvt_pk_bf16_f32 v80, v6, v10
	v_cvt_pk_bf16_f32 v81, v14, v18
	v_cvt_pk_bf16_f32 v82, v22, v26
	v_cvt_pk_bf16_f32 v83, v30, v34
	v_add_co_u32_e32 v10, vcc, s23, v88
	v_cvt_pk_bf16_f32 v84, v38, v42
	v_cvt_pk_bf16_f32 v85, v46, v50
	v_cvt_pk_bf16_f32 v86, v54, v58
	v_cvt_pk_bf16_f32 v87, v62, v66
	global_store_dwordx4 v[88:89], v[80:83], off sc1
	global_store_dwordx4 v[88:89], v[84:87], off offset:16 sc1
	v_cvt_pk_bf16_f32 v4, v7, v11
	v_addc_co_u32_e32 v11, vcc, 0, v89, vcc
	v_add_co_u32_e32 v14, vcc, s29, v88
	v_cvt_pk_bf16_f32 v5, v15, v19
	v_cvt_pk_bf16_f32 v6, v23, v27
	v_cvt_pk_bf16_f32 v7, v31, v35
	v_cvt_pk_bf16_f32 v80, v39, v43
	s_nop 1
	v_addc_co_u32_e32 v15, vcc, 0, v89, vcc
	v_cvt_pk_bf16_f32 v81, v47, v51
	v_cvt_pk_bf16_f32 v82, v55, v59
	v_cvt_pk_bf16_f32 v83, v63, v67
	global_store_dwordx4 v[14:15], v[4:7], off offset:-4096 sc1
	global_store_dwordx4 v[10:11], v[80:83], off offset:16 sc1
	s_nop 0
	v_cvt_pk_bf16_f32 v4, v8, v12
	v_cvt_pk_bf16_f32 v5, v16, v20
	v_cvt_pk_bf16_f32 v6, v24, v28
	v_cvt_pk_bf16_f32 v7, v32, v36
	v_add_co_u32_e32 v12, vcc, 0x3000, v88
	v_cvt_pk_bf16_f32 v80, v40, v44
	v_cvt_pk_bf16_f32 v81, v48, v52
	v_cvt_pk_bf16_f32 v82, v56, v60
	v_cvt_pk_bf16_f32 v83, v64, v68
	global_store_dwordx4 v[14:15], v[4:7], off sc1
	global_store_dwordx4 v[14:15], v[80:83], off offset:16 sc1
	s_nop 0
	v_cvt_pk_bf16_f32 v4, v9, v13
	v_cvt_pk_bf16_f32 v5, v17, v21
	v_cvt_pk_bf16_f32 v6, v25, v29
	v_cvt_pk_bf16_f32 v7, v33, v37
	v_addc_co_u32_e32 v13, vcc, 0, v89, vcc
	v_cvt_pk_bf16_f32 v8, v41, v45
	v_cvt_pk_bf16_f32 v9, v49, v53
	v_cvt_pk_bf16_f32 v10, v57, v61
	v_cvt_pk_bf16_f32 v11, v65, v69
	global_store_dwordx4 v[12:13], v[4:7], off sc1
	global_store_dwordx4 v[12:13], v[8:11], off offset:16 sc1
	s_branch .LBB0_228

.LBB0_301:
	s_and_saveexec_b64 s[72:73], s[8:9]
	s_cbranch_execz .LBB0_266
	s_ashr_i32 s71, s70, 31
	v_lshl_add_u64 v[88:89], s[70:71], 1, v[76:77]
	v_add_co_u32_e32 v4, vcc, s37, v88
	s_movk_i32 s2, 0x5000
	s_nop 0
	v_addc_co_u32_e32 v5, vcc, 0, v89, vcc
	v_add_co_u32_e32 v90, vcc, s2, v88
	s_waitcnt vmcnt(0)
	v_cvt_pk_bf16_f32 v80, v6, v10
	v_cvt_pk_bf16_f32 v81, v14, v18
	v_cvt_pk_bf16_f32 v82, v22, v26
	v_cvt_pk_bf16_f32 v83, v30, v34
	s_nop 0
	v_addc_co_u32_e32 v91, vcc, 0, v89, vcc
	v_add_co_u32_e32 v10, vcc, s20, v88
	v_cvt_pk_bf16_f32 v84, v38, v42
	v_cvt_pk_bf16_f32 v85, v46, v50
	v_cvt_pk_bf16_f32 v86, v54, v58
	v_cvt_pk_bf16_f32 v87, v62, v66
	global_store_dwordx4 v[90:91], v[80:83], off offset:-4096 sc1
	global_store_dwordx4 v[4:5], v[84:87], off offset:16 sc1
	v_cvt_pk_bf16_f32 v4, v7, v11
	v_cvt_pk_bf16_f32 v5, v15, v19
	v_cvt_pk_bf16_f32 v6, v23, v27
	v_cvt_pk_bf16_f32 v7, v31, v35
	v_addc_co_u32_e32 v11, vcc, 0, v89, vcc
	v_cvt_pk_bf16_f32 v80, v39, v43
	v_cvt_pk_bf16_f32 v81, v47, v51
	v_cvt_pk_bf16_f32 v82, v55, v59
	v_cvt_pk_bf16_f32 v83, v63, v67
	global_store_dwordx4 v[90:91], v[4:7], off sc1
	global_store_dwordx4 v[90:91], v[80:83], off offset:16 sc1
	s_nop 0
	v_cvt_pk_bf16_f32 v4, v8, v12
	v_cvt_pk_bf16_f32 v5, v16, v20
	v_cvt_pk_bf16_f32 v6, v24, v28
	v_cvt_pk_bf16_f32 v7, v32, v36
	v_add_co_u32_e32 v12, vcc, 0x7000, v88
	v_cvt_pk_bf16_f32 v80, v40, v44
	v_cvt_pk_bf16_f32 v81, v48, v52
	v_cvt_pk_bf16_f32 v82, v56, v60
	v_cvt_pk_bf16_f32 v83, v64, v68
	global_store_dwordx4 v[10:11], v[4:7], off sc1
	global_store_dwordx4 v[10:11], v[80:83], off offset:16 sc1
	s_nop 0
	v_cvt_pk_bf16_f32 v4, v9, v13
	v_cvt_pk_bf16_f32 v5, v17, v21
	v_cvt_pk_bf16_f32 v6, v25, v29
	v_cvt_pk_bf16_f32 v7, v33, v37
	v_addc_co_u32_e32 v13, vcc, 0, v89, vcc
	v_cvt_pk_bf16_f32 v8, v41, v45
	v_cvt_pk_bf16_f32 v9, v49, v53
	v_cvt_pk_bf16_f32 v10, v57, v61
	v_cvt_pk_bf16_f32 v11, v65, v69
	global_store_dwordx4 v[12:13], v[4:7], off sc1
	global_store_dwordx4 v[12:13], v[8:11], off offset:16 sc1
	s_branch .LBB0_266

.LBB0_314:
	s_mov_b32 s71, s25
	s_lshl_b64 s[70:71], s[70:71], 1
	s_add_u32 s70, s72, s70
	v_lshl_add_u64 v[222:223], s[74:75], 0, v[172:173]
	s_addc_u32 s71, s73, s71
	v_mov_b32_e32 v187, v2
	v_lshl_add_u64 v[224:225], s[70:71], 0, v[186:187]
	v_mul_lo_u32 v3, v223, s68
	v_mad_u64_u32 v[214:215], s[70:71], v222, s68, 0
	v_add_u32_e32 v215, v215, v3
	s_waitcnt vmcnt(0)
	v_mul_f32_e32 v8, v8, v80
	v_mul_f32_e32 v4, v4, v81
	v_lshl_add_u64 v[226:227], v[214:215], 1, v[224:225]
	v_cvt_pk_bf16_f32 v214, v8, v4
	v_mul_f32_e32 v4, v16, v82
	v_mul_f32_e32 v8, v12, v83
	v_cvt_pk_bf16_f32 v215, v4, v8
	v_mul_f32_e32 v4, v24, v76
	v_mul_f32_e32 v8, v20, v77
	v_cvt_pk_bf16_f32 v216, v4, v8
	v_mul_f32_e32 v4, v32, v78
	v_mul_f32_e32 v8, v28, v79
	v_cvt_pk_bf16_f32 v217, v4, v8
	v_mul_f32_e32 v4, v40, v72
	v_mul_f32_e32 v8, v36, v73
	v_cvt_pk_bf16_f32 v218, v4, v8
	v_mul_f32_e32 v4, v48, v74
	v_mul_f32_e32 v8, v44, v75
	s_mov_b32 s69, s25
	v_cvt_pk_bf16_f32 v219, v4, v8
	v_mul_f32_e32 v4, v56, v68
	v_mul_f32_e32 v8, v52, v69
	v_cvt_pk_bf16_f32 v220, v4, v8
	v_mul_f32_e32 v4, v64, v70
	v_mul_f32_e32 v8, v60, v71
	v_cvt_pk_bf16_f32 v221, v4, v8
	global_store_dwordx4 v[226:227], v[214:217], off sc1
	global_store_dwordx4 v[226:227], v[218:221], off offset:16 sc1
	v_mul_f32_e32 v4, v5, v81
	v_mov_b64_e32 v[214:215], s[68:69]
	v_mad_u64_u32 v[222:223], s[70:71], v222, s68, v[214:215]
	v_add_u32_e32 v223, v3, v223
	v_mul_f32_e32 v3, v9, v80
	v_cvt_pk_bf16_f32 v214, v3, v4
	v_mul_f32_e32 v3, v17, v82
	v_mul_f32_e32 v4, v13, v83
	v_cvt_pk_bf16_f32 v215, v3, v4
	v_mul_f32_e32 v3, v25, v76
	v_mul_f32_e32 v4, v21, v77
	v_cvt_pk_bf16_f32 v216, v3, v4
	v_mul_f32_e32 v3, v33, v78
	v_mul_f32_e32 v4, v29, v79
	v_cvt_pk_bf16_f32 v217, v3, v4
	v_mul_f32_e32 v3, v41, v72
	v_mul_f32_e32 v4, v37, v73
	v_cvt_pk_bf16_f32 v218, v3, v4
	v_mul_f32_e32 v3, v49, v74
	v_mul_f32_e32 v4, v45, v75
	v_cvt_pk_bf16_f32 v219, v3, v4
	v_mul_f32_e32 v3, v57, v68
	v_mul_f32_e32 v4, v53, v69
	v_cvt_pk_bf16_f32 v220, v3, v4
	v_mul_f32_e32 v3, v65, v70
	v_lshl_add_u64 v[226:227], v[222:223], 1, v[224:225]
	v_mul_f32_e32 v4, v61, v71
	v_cvt_pk_bf16_f32 v221, v3, v4
	v_mul_f32_e32 v3, v10, v80
	global_store_dwordx4 v[226:227], v[214:217], off sc1
	global_store_dwordx4 v[226:227], v[218:221], off offset:16 sc1
	v_mul_f32_e32 v6, v6, v81
	v_cvt_pk_bf16_f32 v214, v3, v6
	v_mul_f32_e32 v3, v18, v82
	v_mul_f32_e32 v6, v14, v83
	v_cvt_pk_bf16_f32 v215, v3, v6
	v_mul_f32_e32 v3, v26, v76
	v_mul_f32_e32 v6, v22, v77
	v_cvt_pk_bf16_f32 v216, v3, v6
	v_mul_f32_e32 v3, v34, v78
	v_mul_f32_e32 v6, v30, v79
	v_cvt_pk_bf16_f32 v217, v3, v6
	v_mul_f32_e32 v3, v42, v72
	v_mul_f32_e32 v6, v38, v73
	v_cvt_pk_bf16_f32 v218, v3, v6
	v_mul_f32_e32 v3, v50, v74
	v_lshl_add_u64 v[4:5], v[222:223], 0, s[68:69]
	v_mul_f32_e32 v6, v46, v75
	v_cvt_pk_bf16_f32 v219, v3, v6
	v_mul_f32_e32 v3, v58, v68
	v_lshl_add_u64 v[8:9], v[4:5], 1, v[224:225]
	v_mul_f32_e32 v6, v54, v69
	v_cvt_pk_bf16_f32 v220, v3, v6
	v_mul_f32_e32 v3, v66, v70
	v_lshl_add_u64 v[4:5], v[4:5], 0, s[68:69]
	v_mul_f32_e32 v6, v62, v71
	v_cvt_pk_bf16_f32 v221, v3, v6
	v_lshl_add_u64 v[12:13], v[4:5], 1, v[224:225]
	v_mul_f32_e32 v3, v11, v80
	v_mul_f32_e32 v4, v7, v81
	global_store_dwordx4 v[8:9], v[214:217], off sc1
	global_store_dwordx4 v[8:9], v[218:221], off offset:16 sc1
	v_cvt_pk_bf16_f32 v4, v3, v4
	v_mul_f32_e32 v3, v19, v82
	v_mul_f32_e32 v5, v15, v83
	v_cvt_pk_bf16_f32 v5, v3, v5
	v_mul_f32_e32 v3, v27, v76
	v_mul_f32_e32 v6, v23, v77
	v_cvt_pk_bf16_f32 v6, v3, v6
	v_mul_f32_e32 v3, v35, v78
	v_mul_f32_e32 v7, v31, v79
	v_cvt_pk_bf16_f32 v7, v3, v7
	v_mul_f32_e32 v3, v43, v72
	v_mul_f32_e32 v8, v39, v73
	v_cvt_pk_bf16_f32 v8, v3, v8
	v_mul_f32_e32 v3, v51, v74
	v_mul_f32_e32 v9, v47, v75
	v_cvt_pk_bf16_f32 v9, v3, v9
	v_mul_f32_e32 v3, v59, v68
	v_mul_f32_e32 v10, v55, v69
	v_mul_f32_e32 v11, v63, v71
	v_cvt_pk_bf16_f32 v10, v3, v10
	v_mul_f32_e32 v3, v67, v70
	v_cvt_pk_bf16_f32 v11, v3, v11
	global_store_dwordx4 v[12:13], v[4:7], off sc1
	global_store_dwordx4 v[12:13], v[8:11], off offset:16 sc1
	v_mov_b64_e32 v[60:61], v[144:145]
	v_mov_b64_e32 v[64:65], v[140:141]
	v_mov_b64_e32 v[52:53], v[136:137]
	v_mov_b64_e32 v[56:57], v[132:133]
	v_mov_b64_e32 v[44:45], v[128:129]
	v_mov_b64_e32 v[48:49], v[124:125]
	v_mov_b64_e32 v[36:37], v[120:121]
	v_mov_b64_e32 v[40:41], v[116:117]
	v_mov_b64_e32 v[28:29], v[112:113]
	v_mov_b64_e32 v[32:33], v[108:109]
	v_mov_b64_e32 v[20:21], v[104:105]
	v_mov_b64_e32 v[24:25], v[100:101]
	v_mov_b64_e32 v[12:13], v[96:97]
	v_mov_b64_e32 v[16:17], v[92:93]
	v_mov_b64_e32 v[4:5], v[88:89]
	v_mov_b64_e32 v[8:9], v[84:85]
	s_add_i32 s41, s41, s97
	s_add_i32 s91, s91, s40
	s_add_i32 s43, s43, s90
	s_andn2_b64 vcc, exec, s[80:81]
	v_mov_b64_e32 v[62:63], v[146:147]
	v_mov_b64_e32 v[66:67], v[142:143]
	v_mov_b64_e32 v[54:55], v[138:139]
	v_mov_b64_e32 v[58:59], v[134:135]
	v_mov_b64_e32 v[46:47], v[130:131]
	v_mov_b64_e32 v[50:51], v[126:127]
	v_mov_b64_e32 v[38:39], v[122:123]
	v_mov_b64_e32 v[42:43], v[118:119]
	v_mov_b64_e32 v[30:31], v[114:115]
	v_mov_b64_e32 v[34:35], v[110:111]
	v_mov_b64_e32 v[22:23], v[106:107]
	v_mov_b64_e32 v[26:27], v[102:103]
	v_mov_b64_e32 v[14:15], v[98:99]
	v_mov_b64_e32 v[18:19], v[94:95]
	v_mov_b64_e32 v[6:7], v[90:91]
	v_mov_b64_e32 v[10:11], v[86:87]
	s_mov_b64 s[74:75], s[78:79]
	s_mov_b32 s70, s82
	s_mov_b32 s68, s2
	s_mov_b64 s[72:73], s[76:77]
	v_mov_b32_e32 v68, v148
	v_mov_b32_e32 v69, v149
	v_mov_b32_e32 v70, v150
	v_mov_b32_e32 v71, v151
	v_mov_b32_e32 v72, v152
	v_mov_b32_e32 v73, v153
	v_mov_b32_e32 v74, v154
	v_mov_b32_e32 v75, v155
	v_mov_b32_e32 v76, v156
	v_mov_b32_e32 v77, v157
	v_mov_b32_e32 v78, v158
	v_mov_b32_e32 v79, v159
	v_mov_b32_e32 v80, v160
	v_mov_b32_e32 v81, v161
	v_mov_b32_e32 v82, v162
	v_mov_b32_e32 v83, v163
	s_cbranch_vccz .LBB0_137

.LBB0_349:
	s_lshl_b32 s2, s24, 8
	s_add_i32 s15, s2, s41
	s_lshr_b32 s2, s15, 1
	s_and_b32 s17, s2, 0x1fe0
	s_ashr_i32 s2, s15, 12
	s_lshl_b32 s3, s25, 8
	s_and_b32 s2, s2, -4
	s_ashr_i32 s26, s25, 1
	s_and_b32 s3, s3, 0x100
	s_or_b32 s3, s3, s42
	s_add_i32 s2, s2, s26
	s_lshr_b32 s27, s3, 4
	s_ashr_i32 s3, s2, 31
	s_lshl_b64 s[24:25], s[2:3], 13
	s_or_b32 s2, s24, s27
	s_or_b32 s2, s2, s17
	s_mov_b32 s3, s25
	s_lshl_b64 s[2:3], s[2:3], 11
	s_or_b32 s28, s27, 1
	v_cvt_pk_bf16_f32 v126, v126, v127
	v_cvt_pk_bf16_f32 v127, v128, v129
	v_cvt_pk_bf16_f32 v128, v122, v123
	v_lshl_add_u64 v[122:123], v[130:131], 0, s[2:3]
	s_or_b32 s2, s24, s28
	s_or_b32 s2, s2, s17
	s_mov_b32 s3, s25
	s_lshl_b64 s[2:3], s[2:3], 11
	s_or_b32 s29, s27, 8
	v_cvt_pk_bf16_f32 v129, v124, v125
	global_store_dwordx4 v[122:123], v[126:129], off sc1
	v_cvt_pk_bf16_f32 v118, v118, v119
	v_cvt_pk_bf16_f32 v119, v120, v121
	v_cvt_pk_bf16_f32 v120, v110, v111
	v_cvt_pk_bf16_f32 v121, v112, v113
	global_store_dwordx4 v[122:123], v[118:121], off offset:1024 sc1
	v_cvt_pk_bf16_f32 v110, v114, v115
	v_cvt_pk_bf16_f32 v111, v116, v117
	v_cvt_pk_bf16_f32 v112, v106, v107
	v_lshl_add_u64 v[106:107], v[130:131], 0, s[2:3]
	s_or_b32 s2, s24, s29
	s_or_b32 s2, s2, s17
	s_mov_b32 s3, s25
	s_lshl_b64 s[2:3], s[2:3], 11
	s_or_b32 s30, s27, 9
	v_cvt_pk_bf16_f32 v113, v108, v109
	global_store_dwordx4 v[106:107], v[110:113], off sc1
	v_cvt_pk_bf16_f32 v102, v102, v103
	v_cvt_pk_bf16_f32 v103, v104, v105
	v_cvt_pk_bf16_f32 v104, v98, v99
	v_cvt_pk_bf16_f32 v105, v100, v101
	global_store_dwordx4 v[106:107], v[102:105], off offset:1024 sc1
	v_cvt_pk_bf16_f32 v94, v94, v95
	v_cvt_pk_bf16_f32 v95, v96, v97
	v_cvt_pk_bf16_f32 v96, v90, v91
	v_lshl_add_u64 v[90:91], v[130:131], 0, s[2:3]
	s_or_b32 s2, s30, s17
	s_or_b32 s24, s24, s2
	s_lshl_b64 s[2:3], s[24:25], 11
	s_addk_i32 s15, 0x80
	v_cvt_pk_bf16_f32 v97, v92, v93
	global_store_dwordx4 v[90:91], v[94:97], off sc1
	v_cvt_pk_bf16_f32 v86, v86, v87
	v_cvt_pk_bf16_f32 v87, v88, v89
	v_cvt_pk_bf16_f32 v88, v78, v79
	v_cvt_pk_bf16_f32 v89, v80, v81
	global_store_dwordx4 v[90:91], v[86:89], off offset:1024 sc1
	v_cvt_pk_bf16_f32 v78, v82, v83
	v_cvt_pk_bf16_f32 v79, v84, v85
	v_cvt_pk_bf16_f32 v80, v74, v75
	v_lshl_add_u64 v[74:75], v[130:131], 0, s[2:3]
	s_lshr_b32 s2, s15, 1
	s_and_b32 s17, s2, 0x1fe0
	s_ashr_i32 s2, s15, 12
	s_and_b32 s2, s2, -4
	s_add_i32 s2, s2, s26
	s_ashr_i32 s3, s2, 31
	s_lshl_b64 s[24:25], s[2:3], 13
	s_or_b32 s2, s24, s27
	s_or_b32 s2, s2, s17
	s_mov_b32 s3, s25
	s_lshl_b64 s[2:3], s[2:3], 11
	v_cvt_pk_bf16_f32 v81, v76, v77
	global_store_dwordx4 v[74:75], v[78:81], off sc1
	v_cvt_pk_bf16_f32 v70, v70, v71
	v_cvt_pk_bf16_f32 v71, v72, v73
	v_cvt_pk_bf16_f32 v72, v66, v67
	v_cvt_pk_bf16_f32 v73, v68, v69
	global_store_dwordx4 v[74:75], v[70:73], off offset:1024 sc1
	v_cvt_pk_bf16_f32 v62, v62, v63
	v_cvt_pk_bf16_f32 v63, v64, v65
	v_cvt_pk_bf16_f32 v64, v58, v59
	v_lshl_add_u64 v[58:59], v[130:131], 0, s[2:3]
	s_or_b32 s2, s24, s28
	s_or_b32 s2, s2, s17
	s_mov_b32 s3, s25
	s_lshl_b64 s[2:3], s[2:3], 11
	v_cvt_pk_bf16_f32 v65, v60, v61
	global_store_dwordx4 v[58:59], v[62:65], off sc1
	v_cvt_pk_bf16_f32 v54, v54, v55
	v_cvt_pk_bf16_f32 v55, v56, v57
	v_cvt_pk_bf16_f32 v56, v46, v47
	v_cvt_pk_bf16_f32 v57, v48, v49
	global_store_dwordx4 v[58:59], v[54:57], off offset:1024 sc1
	v_cvt_pk_bf16_f32 v46, v50, v51
	v_cvt_pk_bf16_f32 v47, v52, v53
	v_cvt_pk_bf16_f32 v48, v42, v43
	v_lshl_add_u64 v[42:43], v[130:131], 0, s[2:3]
	s_or_b32 s2, s24, s29
	s_or_b32 s2, s2, s17
	s_mov_b32 s3, s25
	s_lshl_b64 s[2:3], s[2:3], 11
	v_cvt_pk_bf16_f32 v49, v44, v45
	global_store_dwordx4 v[42:43], v[46:49], off sc1
	v_cvt_pk_bf16_f32 v38, v38, v39
	v_cvt_pk_bf16_f32 v39, v40, v41
	v_cvt_pk_bf16_f32 v40, v34, v35
	v_cvt_pk_bf16_f32 v41, v36, v37
	global_store_dwordx4 v[42:43], v[38:41], off offset:1024 sc1
	v_cvt_pk_bf16_f32 v30, v30, v31
	v_cvt_pk_bf16_f32 v31, v32, v33
	v_cvt_pk_bf16_f32 v32, v26, v27
	v_lshl_add_u64 v[26:27], v[130:131], 0, s[2:3]
	s_or_b32 s2, s30, s17
	s_or_b32 s24, s24, s2
	s_lshl_b64 s[2:3], s[24:25], 11
	v_cvt_pk_bf16_f32 v33, v28, v29
	global_store_dwordx4 v[26:27], v[30:33], off sc1
	v_cvt_pk_bf16_f32 v22, v22, v23
	v_cvt_pk_bf16_f32 v23, v24, v25
	v_cvt_pk_bf16_f32 v24, v14, v15
	v_cvt_pk_bf16_f32 v25, v16, v17
	global_store_dwordx4 v[26:27], v[22:25], off offset:1024 sc1
	v_cvt_pk_bf16_f32 v14, v18, v19
	v_cvt_pk_bf16_f32 v15, v20, v21
	v_cvt_pk_bf16_f32 v16, v10, v11
	v_lshl_add_u64 v[10:11], v[130:131], 0, s[2:3]
	s_andn2_b64 vcc, exec, s[6:7]
	s_mov_b64 s[6:7], -1
	v_cvt_pk_bf16_f32 v17, v12, v13
	global_store_dwordx4 v[10:11], v[14:17], off sc1
	v_cvt_pk_bf16_f32 v6, v6, v7
	v_cvt_pk_bf16_f32 v7, v8, v9
	v_cvt_pk_bf16_f32 v8, v2, v3
	v_cvt_pk_bf16_f32 v9, v4, v5
	global_store_dwordx4 v[10:11], v[6:9], off offset:1024 sc1
	s_cbranch_vccnz .LBB0_338
	s_andn2_b64 vcc, exec, s[8:9]
	s_cbranch_vccnz .LBB0_337
	s_barrier
	s_branch .LBB0_337

.LBB0_410:
	s_nop 6
	v_cndmask_b32_e64 v74, v74, 0, s[30:31]
	v_bfe_u32 v78, v74, 16, 1
	v_add3_u32 v74, v74, v78, s71
	ds_write_b16_d16_hi v113, v74
	v_cndmask_b32_e64 v74, v75, 0, s[34:35]
	v_bfe_u32 v75, v74, 16, 1
	v_add3_u32 v74, v74, v75, s71
	ds_write_b16_d16_hi v117, v74
	v_cndmask_b32_e64 v74, v76, 0, s[36:37]
	v_bfe_u32 v75, v74, 16, 1
	v_add3_u32 v74, v74, v75, s71
	ds_write_b16_d16_hi v180, v74
	v_cndmask_b32_e64 v74, v77, 0, s[38:39]
	v_bfe_u32 v75, v74, 16, 1
	v_add3_u32 v74, v74, v75, s71
	ds_write_b16_d16_hi v181, v74
	s_waitcnt lgkmcnt(0)
	s_barrier
	ds_read_b128 v[74:77], v183
	s_lshl_b64 s[74:75], s[40:41], 13
	v_lshl_add_u64 v[78:79], v[94:95], 0, s[74:75]
	s_lshl_b64 s[40:41], s[40:41], 5
	v_or_b32_e32 v150, s40, v96
	s_waitcnt lgkmcnt(0)
	global_store_dwordx4 v[78:79], v[74:77], off sc1
	ds_read2_b64 v[74:77], v93 offset1:4
	v_mov_b32_e32 v79, s41
	v_or_b32_e32 v78, v150, v110
	v_lshlrev_b64 v[78:79], 10, v[78:79]
	v_lshl_add_u64 v[78:79], v[98:99], 0, v[78:79]
	s_waitcnt lgkmcnt(0)
	global_store_dwordx4 v[78:79], v[74:77], off sc1
	ds_read2_b64 v[74:77], v103 offset1:4
	v_mov_b32_e32 v79, s41
	v_or_b32_e32 v78, v150, v112
	v_lshlrev_b64 v[78:79], 10, v[78:79]
	v_lshl_add_u64 v[78:79], v[98:99], 0, v[78:79]
	s_waitcnt lgkmcnt(0)
	global_store_dwordx4 v[78:79], v[74:77], off sc1
	ds_read2_b64 v[74:77], v107 offset1:4
	v_mov_b32_e32 v79, s41
	v_or_b32_e32 v78, v150, v116
	v_lshlrev_b64 v[78:79], 10, v[78:79]
	v_lshl_add_u64 v[152:153], v[98:99], 0, v[78:79]
	ds_read2_b64 v[78:81], v111 offset1:4
	v_mov_b32_e32 v151, s41
	s_waitcnt lgkmcnt(1)
	global_store_dwordx4 v[152:153], v[74:77], off sc1
	s_add_i32 s49, s49, s50
	s_andn2_b64 vcc, exec, s[66:67]
	v_lshl_add_u64 v[74:75], v[150:151], 0, v[122:123]
	v_lshlrev_b64 v[74:75], 10, v[74:75]
	v_lshl_add_u64 v[74:75], v[98:99], 0, v[74:75]
	s_add_i32 s51, s51, s52
	s_waitcnt lgkmcnt(0)
	global_store_dwordx4 v[74:75], v[78:81], off sc1
	s_barrier
	s_cbranch_vccz .LBB0_419
.LBB0_411:
	s_waitcnt vmcnt(14)
	v_readlane_b32 s40, v70, 0
	v_readlane_b32 s41, v71, 0
	s_lshl_b32 s2, s40, 16
	s_and_b32 s40, s40, 0xffff0000
	v_pk_mul_f32 v[74:75], v[4:5], s[40:41] op_sel_hi:[1,0]
	v_pk_mul_f32 v[76:77], v[2:3], s[40:41] op_sel_hi:[1,0]
	s_and_b32 s40, s41, 0xffff0000
	v_readlane_b32 s58, v72, 0
	v_pk_fma_f32 v[74:75], v[28:29], s[2:3], v[74:75] op_sel_hi:[1,0,1]
	v_pk_fma_f32 v[76:77], v[26:27], s[2:3], v[76:77] op_sel_hi:[1,0,1]
	s_lshl_b32 s2, s41, 16
	v_pk_mul_f32 v[80:81], v[10:11], s[40:41] op_sel_hi:[1,0]
	v_pk_add_f32 v[76:77], v[66:67], v[76:77]
	v_pk_mul_f32 v[78:79], v[12:13], s[40:41] op_sel_hi:[1,0]
	v_pk_fma_f32 v[80:81], v[6:7], s[2:3], v[80:81] op_sel_hi:[1,0,1]
	s_and_b32 s40, s58, 0xffff0000
	v_readlane_b32 s66, v73, 0
	v_pk_add_f32 v[74:75], v[68:69], v[74:75]
	v_pk_fma_f32 v[78:79], v[8:9], s[2:3], v[78:79] op_sel_hi:[1,0,1]
	v_pk_add_f32 v[76:77], v[76:77], v[80:81]
	s_lshl_b32 s2, s58, 16
	v_pk_mul_f32 v[80:81], v[18:19], s[40:41] op_sel_hi:[1,0]
	v_pk_add_f32 v[74:75], v[74:75], v[78:79]
	v_pk_mul_f32 v[78:79], v[20:21], s[40:41] op_sel_hi:[1,0]
	v_pk_fma_f32 v[80:81], v[14:15], s[2:3], v[80:81] op_sel_hi:[1,0,1]
	s_and_b32 s40, s66, 0xffff0000
	v_readlane_b32 s67, v70, 1
	v_pk_fma_f32 v[78:79], v[16:17], s[2:3], v[78:79] op_sel_hi:[1,0,1]
	v_pk_add_f32 v[76:77], v[76:77], v[80:81]
	s_lshl_b32 s2, s66, 16
	v_pk_mul_f32 v[80:81], v[30:31], s[40:41] op_sel_hi:[1,0]
	v_pk_add_f32 v[74:75], v[74:75], v[78:79]
	v_pk_mul_f32 v[78:79], v[32:33], s[40:41] op_sel_hi:[1,0]
	v_pk_fma_f32 v[80:81], v[22:23], s[2:3], v[80:81] op_sel_hi:[1,0,1]
	s_and_b32 s40, s67, 0xffff0000
	v_readlane_b32 s73, v71, 1
	v_pk_fma_f32 v[78:79], v[24:25], s[2:3], v[78:79] op_sel_hi:[1,0,1]
	v_pk_add_f32 v[76:77], v[76:77], v[80:81]
	s_lshl_b32 s2, s67, 16
	v_pk_mul_f32 v[80:81], v[38:39], s[40:41] op_sel_hi:[1,0]
	v_pk_add_f32 v[74:75], v[74:75], v[78:79]
	v_pk_mul_f32 v[78:79], v[40:41], s[40:41] op_sel_hi:[1,0]
	v_pk_fma_f32 v[80:81], v[34:35], s[2:3], v[80:81] op_sel_hi:[1,0,1]
	s_and_b32 s40, s73, 0xffff0000
	v_readlane_b32 s74, v72, 1
	v_pk_fma_f32 v[78:79], v[36:37], s[2:3], v[78:79] op_sel_hi:[1,0,1]
	v_pk_add_f32 v[76:77], v[76:77], v[80:81]
	s_lshl_b32 s2, s73, 16
	v_pk_mul_f32 v[80:81], v[46:47], s[40:41] op_sel_hi:[1,0]
	v_pk_add_f32 v[74:75], v[74:75], v[78:79]
	v_pk_mul_f32 v[78:79], v[48:49], s[40:41] op_sel_hi:[1,0]
	v_pk_fma_f32 v[80:81], v[42:43], s[2:3], v[80:81] op_sel_hi:[1,0,1]
	s_and_b32 s40, s74, 0xffff0000
	v_readlane_b32 s75, v73, 1
	v_pk_fma_f32 v[78:79], v[44:45], s[2:3], v[78:79] op_sel_hi:[1,0,1]
	v_pk_add_f32 v[76:77], v[76:77], v[80:81]
	s_lshl_b32 s2, s74, 16
	v_pk_mul_f32 v[80:81], v[54:55], s[40:41] op_sel_hi:[1,0]
	s_and_b32 s58, s75, 0xffff0000
	v_pk_fma_f32 v[80:81], v[50:51], s[2:3], v[80:81] op_sel_hi:[1,0,1]
	v_pk_add_f32 v[74:75], v[74:75], v[78:79]
	v_pk_mul_f32 v[78:79], v[56:57], s[40:41] op_sel_hi:[1,0]
	v_pk_add_f32 v[76:77], v[76:77], v[80:81]
	s_lshl_b32 s40, s75, 16
	v_pk_mul_f32 v[80:81], v[62:63], s[58:59] op_sel_hi:[1,0]
	v_pk_fma_f32 v[78:79], v[52:53], s[2:3], v[78:79] op_sel_hi:[1,0,1]
	v_pk_fma_f32 v[80:81], v[58:59], s[40:41], v[80:81] op_sel_hi:[1,0,1]
	v_pk_add_f32 v[74:75], v[74:75], v[78:79]
	v_pk_add_f32 v[76:77], v[76:77], v[80:81]
	v_pk_mul_f32 v[78:79], v[64:65], s[58:59] op_sel_hi:[1,0]
	v_mul_f32_e64 v80, |v76|, s53
	v_exp_f32_e32 v80, v80
	v_pk_fma_f32 v[78:79], v[60:61], s[40:41], v[78:79] op_sel_hi:[1,0,1]
	v_readlane_b32 s58, v72, 2
	v_pk_add_f32 v[78:79], v[74:75], v[78:79]
	v_add_f32_e32 v80, 1.0, v80
	v_cmp_gt_f32_e32 vcc, s68, v80
	v_min_f32_e32 v74, 0, v76
	v_mul_f32_e64 v76, |v77|, s53
	v_cndmask_b32_e64 v81, 0, 32, vcc
	v_ldexp_f32 v80, v80, v81
	v_log_f32_e32 v80, v80
	v_exp_f32_e32 v76, v76
	v_readlane_b32 s66, v73, 2
	v_readlane_b32 s67, v70, 3
	v_mul_f32_e32 v75, 0x3f317217, v80
	v_fma_f32 v75, v80, s69, -v75
	v_fmac_f32_e32 v75, 0x3377d1cf, v80
	v_fmac_f32_e32 v75, 0x3f317217, v80
	v_cmp_lt_f32_e64 s[40:41], |v80|, s70
	v_readlane_b32 s73, v71, 3
	v_readlane_b32 s74, v72, 3
	v_cndmask_b32_e64 v75, v80, v75, s[40:41]
	v_cndmask_b32_e32 v80, 0, v184, vcc
	v_sub_f32_e32 v75, v75, v80
	v_sub_f32_e32 v74, v74, v75
	v_add_f32_e32 v75, 1.0, v76
	v_cmp_gt_f32_e32 vcc, s68, v75
	v_readlane_b32 s75, v73, 3
	v_mul_f32_e32 v74, 0x3d800000, v74
	v_cndmask_b32_e64 v76, 0, 32, vcc
	v_ldexp_f32 v75, v75, v76
	v_log_f32_e32 v75, v75
	v_min_f32_e32 v76, 0, v77
	v_cndmask_b32_e32 v80, 0, v184, vcc
	v_max_f32_e32 v74, -1.0, v74
	v_mul_f32_e32 v77, 0x3f317217, v75
	v_fma_f32 v77, v75, s69, -v77
	v_fmac_f32_e32 v77, 0x3377d1cf, v75
	v_fmac_f32_e32 v77, 0x3f317217, v75
	v_cmp_lt_f32_e64 s[40:41], |v75|, s70
	v_and_b32_e32 v196, 0xffff0000, v105
	s_nop 0
	v_cndmask_b32_e64 v75, v75, v77, s[40:41]
	v_mul_f32_e64 v77, |v78|, s53
	v_exp_f32_e32 v77, v77
	v_sub_f32_e32 v75, v75, v80
	v_sub_f32_e32 v75, v76, v75
	v_mul_f32_e32 v75, 0x3d800000, v75
	v_add_f32_e32 v76, 1.0, v77
	v_cmp_gt_f32_e32 vcc, s68, v76
	v_max_f32_e32 v75, -1.0, v75
	s_nop 0
	v_cndmask_b32_e64 v77, 0, 32, vcc
	v_ldexp_f32 v76, v76, v77
	v_log_f32_e32 v76, v76
	v_min_f32_e32 v77, 0, v78
	v_cndmask_b32_e32 v80, 0, v184, vcc
	v_mul_f32_e32 v78, 0x3f317217, v76
	v_fma_f32 v78, v76, s69, -v78
	v_fmac_f32_e32 v78, 0x3377d1cf, v76
	v_fmac_f32_e32 v78, 0x3f317217, v76
	v_cmp_lt_f32_e64 s[40:41], |v76|, s70
	s_nop 1
	v_cndmask_b32_e64 v76, v76, v78, s[40:41]
	v_mul_f32_e64 v78, |v79|, s53
	v_exp_f32_e32 v78, v78
	v_sub_f32_e32 v76, v76, v80
	v_sub_f32_e32 v76, v77, v76
	v_mul_f32_e32 v76, 0x3d800000, v76
	v_add_f32_e32 v77, 1.0, v78
	v_cmp_gt_f32_e32 vcc, s68, v77
	v_max_f32_e32 v76, -1.0, v76
	s_nop 0
	v_cndmask_b32_e64 v78, 0, 32, vcc
	v_ldexp_f32 v77, v77, v78
	v_log_f32_e32 v77, v77
	v_min_f32_e32 v78, 0, v79
	v_mul_f32_e32 v79, 0x3f317217, v77
	v_fma_f32 v79, v77, s69, -v79
	v_fmac_f32_e32 v79, 0x3377d1cf, v77
	v_fmac_f32_e32 v79, 0x3f317217, v77
	v_cmp_lt_f32_e64 s[40:41], |v77|, s70
	s_nop 1
	v_cndmask_b32_e64 v77, v77, v79, s[40:41]
	v_cndmask_b32_e32 v79, 0, v184, vcc
	v_readlane_b32 s40, v70, 2
	v_sub_f32_e32 v77, v77, v79
	v_readlane_b32 s41, v71, 2
	s_lshl_b32 s2, s40, 16
	s_and_b32 s40, s40, 0xffff0000
	v_sub_f32_e32 v77, v78, v77
	v_pk_mul_f32 v[78:79], v[4:5], s[40:41] op_sel_hi:[1,0]
	v_pk_mul_f32 v[80:81], v[2:3], s[40:41] op_sel_hi:[1,0]
	s_and_b32 s40, s41, 0xffff0000
	v_pk_fma_f32 v[78:79], v[28:29], s[2:3], v[78:79] op_sel_hi:[1,0,1]
	v_pk_fma_f32 v[80:81], v[26:27], s[2:3], v[80:81] op_sel_hi:[1,0,1]
	s_lshl_b32 s2, s41, 16
	v_pk_mul_f32 v[152:153], v[10:11], s[40:41] op_sel_hi:[1,0]
	v_pk_add_f32 v[80:81], v[66:67], v[80:81]
	v_pk_mul_f32 v[150:151], v[12:13], s[40:41] op_sel_hi:[1,0]
	v_pk_fma_f32 v[152:153], v[6:7], s[2:3], v[152:153] op_sel_hi:[1,0,1]
	s_and_b32 s40, s58, 0xffff0000
	v_pk_add_f32 v[78:79], v[68:69], v[78:79]
	v_pk_fma_f32 v[150:151], v[8:9], s[2:3], v[150:151] op_sel_hi:[1,0,1]
	v_pk_add_f32 v[80:81], v[80:81], v[152:153]
	s_lshl_b32 s2, s58, 16
	v_pk_mul_f32 v[152:153], v[18:19], s[40:41] op_sel_hi:[1,0]
	v_pk_add_f32 v[78:79], v[78:79], v[150:151]
	v_pk_mul_f32 v[150:151], v[20:21], s[40:41] op_sel_hi:[1,0]
	v_pk_fma_f32 v[152:153], v[14:15], s[2:3], v[152:153] op_sel_hi:[1,0,1]
	s_and_b32 s40, s66, 0xffff0000
	v_pk_fma_f32 v[150:151], v[16:17], s[2:3], v[150:151] op_sel_hi:[1,0,1]
	v_pk_add_f32 v[80:81], v[80:81], v[152:153]
	s_lshl_b32 s2, s66, 16
	v_pk_mul_f32 v[152:153], v[30:31], s[40:41] op_sel_hi:[1,0]
	v_pk_add_f32 v[78:79], v[78:79], v[150:151]
	v_pk_mul_f32 v[150:151], v[32:33], s[40:41] op_sel_hi:[1,0]
	v_pk_fma_f32 v[152:153], v[22:23], s[2:3], v[152:153] op_sel_hi:[1,0,1]
	s_and_b32 s40, s67, 0xffff0000
	v_pk_fma_f32 v[150:151], v[24:25], s[2:3], v[150:151] op_sel_hi:[1,0,1]
	v_pk_add_f32 v[80:81], v[80:81], v[152:153]
	s_lshl_b32 s2, s67, 16
	v_pk_mul_f32 v[152:153], v[38:39], s[40:41] op_sel_hi:[1,0]
	v_pk_add_f32 v[78:79], v[78:79], v[150:151]
	v_pk_mul_f32 v[150:151], v[40:41], s[40:41] op_sel_hi:[1,0]
	v_pk_fma_f32 v[152:153], v[34:35], s[2:3], v[152:153] op_sel_hi:[1,0,1]
	s_and_b32 s40, s73, 0xffff0000
	v_pk_fma_f32 v[150:151], v[36:37], s[2:3], v[150:151] op_sel_hi:[1,0,1]
	v_pk_add_f32 v[80:81], v[80:81], v[152:153]
	s_lshl_b32 s2, s73, 16
	v_pk_mul_f32 v[152:153], v[46:47], s[40:41] op_sel_hi:[1,0]
	v_pk_add_f32 v[78:79], v[78:79], v[150:151]
	v_pk_mul_f32 v[150:151], v[48:49], s[40:41] op_sel_hi:[1,0]
	v_pk_fma_f32 v[152:153], v[42:43], s[2:3], v[152:153] op_sel_hi:[1,0,1]
	s_and_b32 s40, s74, 0xffff0000
	v_pk_fma_f32 v[150:151], v[44:45], s[2:3], v[150:151] op_sel_hi:[1,0,1]
	v_pk_add_f32 v[80:81], v[80:81], v[152:153]
	s_lshl_b32 s2, s74, 16
	v_pk_mul_f32 v[152:153], v[54:55], s[40:41] op_sel_hi:[1,0]
	s_and_b32 s58, s75, 0xffff0000
	v_pk_fma_f32 v[152:153], v[50:51], s[2:3], v[152:153] op_sel_hi:[1,0,1]
	v_pk_add_f32 v[78:79], v[78:79], v[150:151]
	v_pk_mul_f32 v[150:151], v[56:57], s[40:41] op_sel_hi:[1,0]
	v_pk_add_f32 v[80:81], v[80:81], v[152:153]
	s_lshl_b32 s40, s75, 16
	v_pk_mul_f32 v[152:153], v[62:63], s[58:59] op_sel_hi:[1,0]
	v_pk_fma_f32 v[150:151], v[52:53], s[2:3], v[150:151] op_sel_hi:[1,0,1]
	v_pk_fma_f32 v[152:153], v[58:59], s[40:41], v[152:153] op_sel_hi:[1,0,1]
	v_pk_add_f32 v[78:79], v[78:79], v[150:151]
	v_pk_add_f32 v[80:81], v[80:81], v[152:153]
	v_pk_mul_f32 v[150:151], v[64:65], s[58:59] op_sel_hi:[1,0]
	v_mul_f32_e64 v152, |v80|, s53
	v_exp_f32_e32 v152, v152
	v_pk_fma_f32 v[150:151], v[60:61], s[40:41], v[150:151] op_sel_hi:[1,0,1]
	v_min_f32_e32 v80, 0, v80
	v_pk_add_f32 v[78:79], v[78:79], v[150:151]
	v_add_f32_e32 v152, 1.0, v152
	v_cmp_gt_f32_e32 vcc, s68, v152
	v_mul_f32_e64 v151, |v81|, s53
	v_exp_f32_e32 v151, v151
	v_cndmask_b32_e64 v153, 0, 32, vcc
	v_ldexp_f32 v152, v152, v153
	v_log_f32_e32 v152, v152
	v_min_f32_e32 v81, 0, v81
	v_readlane_b32 s58, v72, 4
	v_readlane_b32 s66, v73, 4
	v_mul_f32_e32 v150, 0x3f317217, v152
	v_fma_f32 v150, v152, s69, -v150
	v_fmac_f32_e32 v150, 0x3377d1cf, v152
	v_fmac_f32_e32 v150, 0x3f317217, v152
	v_cmp_lt_f32_e64 s[40:41], |v152|, s70
	v_readlane_b32 s67, v70, 5
	v_readlane_b32 s73, v71, 5
	v_cndmask_b32_e64 v150, v152, v150, s[40:41]
	v_cndmask_b32_e32 v152, 0, v184, vcc
	v_sub_f32_e32 v150, v150, v152
	v_sub_f32_e32 v80, v80, v150
	v_add_f32_e32 v150, 1.0, v151
	v_cmp_gt_f32_e32 vcc, s68, v150
	v_readlane_b32 s74, v72, 5
	v_readlane_b32 s75, v73, 5
	v_cndmask_b32_e64 v151, 0, 32, vcc
	v_ldexp_f32 v150, v150, v151
	v_log_f32_e32 v150, v150
	v_cndmask_b32_e32 v152, 0, v184, vcc
	v_mul_f32_e32 v80, 0x3d800000, v80
	v_max_f32_e32 v80, -1.0, v80
	v_mul_f32_e32 v151, 0x3f317217, v150
	v_fma_f32 v151, v150, s69, -v151
	v_fmac_f32_e32 v151, 0x3377d1cf, v150
	v_fmac_f32_e32 v151, 0x3f317217, v150
	v_cmp_lt_f32_e64 s[40:41], |v150|, s70
	v_mul_f32_e32 v77, 0x3d800000, v77
	v_max_f32_e32 v77, -1.0, v77
	v_cndmask_b32_e64 v150, v150, v151, s[40:41]
	v_mul_f32_e64 v151, |v78|, s53
	v_exp_f32_e32 v151, v151
	v_sub_f32_e32 v150, v150, v152
	v_sub_f32_e32 v81, v81, v150
	v_min_f32_e32 v78, 0, v78
	v_add_f32_e32 v150, 1.0, v151
	v_cmp_gt_f32_e32 vcc, s68, v150
	v_mul_f32_e32 v81, 0x3d800000, v81
	v_max_f32_e32 v81, -1.0, v81
	v_cndmask_b32_e64 v151, 0, 32, vcc
	v_ldexp_f32 v150, v150, v151
	v_log_f32_e32 v150, v150
	v_cndmask_b32_e32 v152, 0, v184, vcc
	v_pk_add_f32 v[190:191], v[76:77], 0 op_sel_hi:[1,0]
	v_mul_f32_e32 v151, 0x3f317217, v150
	v_fma_f32 v151, v150, s69, -v151
	v_fmac_f32_e32 v151, 0x3377d1cf, v150
	v_fmac_f32_e32 v151, 0x3f317217, v150
	v_cmp_lt_f32_e64 s[40:41], |v150|, s70
	s_nop 1
	v_cndmask_b32_e64 v150, v150, v151, s[40:41]
	v_mul_f32_e64 v151, |v79|, s53
	v_exp_f32_e32 v151, v151
	v_sub_f32_e32 v150, v150, v152
	v_sub_f32_e32 v78, v78, v150
	v_min_f32_e32 v79, 0, v79
	v_add_f32_e32 v150, 1.0, v151
	v_cmp_gt_f32_e32 vcc, s68, v150
	v_mul_f32_e32 v78, 0x3d800000, v78
	v_max_f32_e32 v78, -1.0, v78
	v_cndmask_b32_e64 v151, 0, 32, vcc
	v_ldexp_f32 v150, v150, v151
	v_log_f32_e32 v150, v150
	s_nop 0
	v_mul_f32_e32 v151, 0x3f317217, v150
	v_fma_f32 v151, v150, s69, -v151
	v_fmac_f32_e32 v151, 0x3377d1cf, v150
	v_fmac_f32_e32 v151, 0x3f317217, v150
	v_cmp_lt_f32_e64 s[40:41], |v150|, s70
	s_nop 1
	v_cndmask_b32_e64 v150, v150, v151, s[40:41]
	v_cndmask_b32_e32 v151, 0, v184, vcc
	v_readlane_b32 s40, v70, 4
	v_sub_f32_e32 v150, v150, v151
	v_readlane_b32 s41, v71, 4
	s_lshl_b32 s2, s40, 16
	s_and_b32 s40, s40, 0xffff0000
	v_sub_f32_e32 v79, v79, v150
	v_pk_mul_f32 v[150:151], v[4:5], s[40:41] op_sel_hi:[1,0]
	v_pk_mul_f32 v[152:153], v[2:3], s[40:41] op_sel_hi:[1,0]
	s_and_b32 s40, s41, 0xffff0000
	v_pk_fma_f32 v[150:151], v[28:29], s[2:3], v[150:151] op_sel_hi:[1,0,1]
	v_pk_fma_f32 v[152:153], v[26:27], s[2:3], v[152:153] op_sel_hi:[1,0,1]
	s_lshl_b32 s2, s41, 16
	v_pk_mul_f32 v[156:157], v[10:11], s[40:41] op_sel_hi:[1,0]
	v_pk_add_f32 v[152:153], v[66:67], v[152:153]
	v_pk_mul_f32 v[154:155], v[12:13], s[40:41] op_sel_hi:[1,0]
	v_pk_fma_f32 v[156:157], v[6:7], s[2:3], v[156:157] op_sel_hi:[1,0,1]
	s_and_b32 s40, s58, 0xffff0000
	v_pk_add_f32 v[150:151], v[68:69], v[150:151]
	v_pk_fma_f32 v[154:155], v[8:9], s[2:3], v[154:155] op_sel_hi:[1,0,1]
	v_pk_add_f32 v[152:153], v[152:153], v[156:157]
	s_lshl_b32 s2, s58, 16
	v_pk_mul_f32 v[156:157], v[18:19], s[40:41] op_sel_hi:[1,0]
	v_pk_add_f32 v[150:151], v[150:151], v[154:155]
	v_pk_mul_f32 v[154:155], v[20:21], s[40:41] op_sel_hi:[1,0]
	v_pk_fma_f32 v[156:157], v[14:15], s[2:3], v[156:157] op_sel_hi:[1,0,1]
	s_and_b32 s40, s66, 0xffff0000
	v_pk_fma_f32 v[154:155], v[16:17], s[2:3], v[154:155] op_sel_hi:[1,0,1]
	v_pk_add_f32 v[152:153], v[152:153], v[156:157]
	s_lshl_b32 s2, s66, 16
	v_pk_mul_f32 v[156:157], v[30:31], s[40:41] op_sel_hi:[1,0]
	v_pk_add_f32 v[150:151], v[150:151], v[154:155]
	v_pk_mul_f32 v[154:155], v[32:33], s[40:41] op_sel_hi:[1,0]
	v_pk_fma_f32 v[156:157], v[22:23], s[2:3], v[156:157] op_sel_hi:[1,0,1]
	s_and_b32 s40, s67, 0xffff0000
	v_pk_fma_f32 v[154:155], v[24:25], s[2:3], v[154:155] op_sel_hi:[1,0,1]
	v_pk_add_f32 v[152:153], v[152:153], v[156:157]
	s_lshl_b32 s2, s67, 16
	v_pk_mul_f32 v[156:157], v[38:39], s[40:41] op_sel_hi:[1,0]
	v_pk_add_f32 v[150:151], v[150:151], v[154:155]
	v_pk_mul_f32 v[154:155], v[40:41], s[40:41] op_sel_hi:[1,0]
	v_pk_fma_f32 v[156:157], v[34:35], s[2:3], v[156:157] op_sel_hi:[1,0,1]
	s_and_b32 s40, s73, 0xffff0000
	v_pk_fma_f32 v[154:155], v[36:37], s[2:3], v[154:155] op_sel_hi:[1,0,1]
	v_pk_add_f32 v[152:153], v[152:153], v[156:157]
	s_lshl_b32 s2, s73, 16
	v_pk_mul_f32 v[156:157], v[46:47], s[40:41] op_sel_hi:[1,0]
	v_pk_add_f32 v[150:151], v[150:151], v[154:155]
	v_pk_mul_f32 v[154:155], v[48:49], s[40:41] op_sel_hi:[1,0]
	v_pk_fma_f32 v[156:157], v[42:43], s[2:3], v[156:157] op_sel_hi:[1,0,1]
	s_and_b32 s40, s74, 0xffff0000
	v_pk_fma_f32 v[154:155], v[44:45], s[2:3], v[154:155] op_sel_hi:[1,0,1]
	v_pk_add_f32 v[152:153], v[152:153], v[156:157]
	s_lshl_b32 s2, s74, 16
	v_pk_mul_f32 v[156:157], v[54:55], s[40:41] op_sel_hi:[1,0]
	s_and_b32 s58, s75, 0xffff0000
	v_pk_fma_f32 v[156:157], v[50:51], s[2:3], v[156:157] op_sel_hi:[1,0,1]
	v_pk_add_f32 v[150:151], v[150:151], v[154:155]
	v_pk_mul_f32 v[154:155], v[56:57], s[40:41] op_sel_hi:[1,0]
	v_pk_add_f32 v[152:153], v[152:153], v[156:157]
	s_lshl_b32 s40, s75, 16
	v_pk_mul_f32 v[156:157], v[62:63], s[58:59] op_sel_hi:[1,0]
	v_pk_fma_f32 v[154:155], v[52:53], s[2:3], v[154:155] op_sel_hi:[1,0,1]
	v_pk_fma_f32 v[156:157], v[58:59], s[40:41], v[156:157] op_sel_hi:[1,0,1]
	v_pk_add_f32 v[150:151], v[150:151], v[154:155]
	v_pk_add_f32 v[152:153], v[152:153], v[156:157]
	v_pk_mul_f32 v[154:155], v[64:65], s[58:59] op_sel_hi:[1,0]
	v_mul_f32_e64 v156, |v152|, s53
	v_exp_f32_e32 v156, v156
	v_pk_fma_f32 v[154:155], v[60:61], s[40:41], v[154:155] op_sel_hi:[1,0,1]
	v_min_f32_e32 v152, 0, v152
	v_pk_add_f32 v[150:151], v[150:151], v[154:155]
	v_add_f32_e32 v156, 1.0, v156
	v_cmp_gt_f32_e32 vcc, s68, v156
	v_mul_f32_e64 v155, |v153|, s53
	v_exp_f32_e32 v155, v155
	v_cndmask_b32_e64 v157, 0, 32, vcc
	v_ldexp_f32 v156, v156, v157
	v_log_f32_e32 v156, v156
	v_min_f32_e32 v153, 0, v153
	v_readlane_b32 s58, v72, 6
	v_readlane_b32 s66, v73, 6
	v_mul_f32_e32 v154, 0x3f317217, v156
	v_fma_f32 v154, v156, s69, -v154
	v_fmac_f32_e32 v154, 0x3377d1cf, v156
	v_fmac_f32_e32 v154, 0x3f317217, v156
	v_cmp_lt_f32_e64 s[40:41], |v156|, s70
	v_readlane_b32 s67, v70, 7
	v_readlane_b32 s73, v71, 7
	v_cndmask_b32_e64 v154, v156, v154, s[40:41]
	v_cndmask_b32_e32 v156, 0, v184, vcc
	v_sub_f32_e32 v154, v154, v156
	v_sub_f32_e32 v152, v152, v154
	v_add_f32_e32 v154, 1.0, v155
	v_cmp_gt_f32_e32 vcc, s68, v154
	v_readlane_b32 s74, v72, 7
	v_readlane_b32 s75, v73, 7
	v_cndmask_b32_e64 v155, 0, 32, vcc
	v_ldexp_f32 v154, v154, v155
	v_log_f32_e32 v154, v154
	v_cndmask_b32_e32 v156, 0, v184, vcc
	v_mul_f32_e32 v152, 0x3d800000, v152
	v_max_f32_e32 v152, -1.0, v152
	v_mul_f32_e32 v155, 0x3f317217, v154
	v_fma_f32 v155, v154, s69, -v155
	v_fmac_f32_e32 v155, 0x3377d1cf, v154
	v_fmac_f32_e32 v155, 0x3f317217, v154
	v_cmp_lt_f32_e64 s[40:41], |v154|, s70
	v_mul_f32_e32 v79, 0x3d800000, v79
	v_max_f32_e32 v79, -1.0, v79
	v_cndmask_b32_e64 v154, v154, v155, s[40:41]
	v_mul_f32_e64 v155, |v150|, s53
	v_exp_f32_e32 v155, v155
	v_sub_f32_e32 v154, v154, v156
	v_sub_f32_e32 v153, v153, v154
	v_min_f32_e32 v150, 0, v150
	v_add_f32_e32 v154, 1.0, v155
	v_cmp_gt_f32_e32 vcc, s68, v154
	v_mul_f32_e32 v153, 0x3d800000, v153
	v_max_f32_e32 v153, -1.0, v153
	v_cndmask_b32_e64 v155, 0, 32, vcc
	v_ldexp_f32 v154, v154, v155
	v_log_f32_e32 v154, v154
	v_cndmask_b32_e32 v156, 0, v184, vcc
	v_mul_f32_e32 v155, 0x3f317217, v154
	v_fma_f32 v155, v154, s69, -v155
	v_fmac_f32_e32 v155, 0x3377d1cf, v154
	v_fmac_f32_e32 v155, 0x3f317217, v154
	v_cmp_lt_f32_e64 s[40:41], |v154|, s70
	s_nop 1
	v_cndmask_b32_e64 v154, v154, v155, s[40:41]
	v_mul_f32_e64 v155, |v151|, s53
	v_exp_f32_e32 v155, v155
	v_sub_f32_e32 v154, v154, v156
	v_sub_f32_e32 v150, v150, v154
	v_min_f32_e32 v151, 0, v151
	v_add_f32_e32 v154, 1.0, v155
	v_cmp_gt_f32_e32 vcc, s68, v154
	v_mul_f32_e32 v150, 0x3d800000, v150
	v_max_f32_e32 v150, -1.0, v150
	v_cndmask_b32_e64 v155, 0, 32, vcc
	v_ldexp_f32 v154, v154, v155
	v_log_f32_e32 v154, v154
	s_nop 0
	v_mul_f32_e32 v155, 0x3f317217, v154
	v_fma_f32 v155, v154, s69, -v155
	v_fmac_f32_e32 v155, 0x3377d1cf, v154
	v_fmac_f32_e32 v155, 0x3f317217, v154
	v_cmp_lt_f32_e64 s[40:41], |v154|, s70
	s_nop 1
	v_cndmask_b32_e64 v154, v154, v155, s[40:41]
	v_cndmask_b32_e32 v155, 0, v184, vcc
	v_readlane_b32 s40, v70, 6
	v_sub_f32_e32 v154, v154, v155
	v_readlane_b32 s41, v71, 6
	s_lshl_b32 s2, s40, 16
	s_and_b32 s40, s40, 0xffff0000
	v_sub_f32_e32 v151, v151, v154
	v_pk_mul_f32 v[154:155], v[4:5], s[40:41] op_sel_hi:[1,0]
	v_pk_mul_f32 v[156:157], v[2:3], s[40:41] op_sel_hi:[1,0]
	s_and_b32 s40, s41, 0xffff0000
	v_pk_fma_f32 v[154:155], v[28:29], s[2:3], v[154:155] op_sel_hi:[1,0,1]
	v_pk_fma_f32 v[156:157], v[26:27], s[2:3], v[156:157] op_sel_hi:[1,0,1]
	s_lshl_b32 s2, s41, 16
	v_pk_mul_f32 v[160:161], v[10:11], s[40:41] op_sel_hi:[1,0]
	v_pk_add_f32 v[156:157], v[66:67], v[156:157]
	v_pk_mul_f32 v[158:159], v[12:13], s[40:41] op_sel_hi:[1,0]
	v_pk_fma_f32 v[160:161], v[6:7], s[2:3], v[160:161] op_sel_hi:[1,0,1]
	s_and_b32 s40, s58, 0xffff0000
	v_pk_add_f32 v[154:155], v[68:69], v[154:155]
	v_pk_fma_f32 v[158:159], v[8:9], s[2:3], v[158:159] op_sel_hi:[1,0,1]
	v_pk_add_f32 v[156:157], v[156:157], v[160:161]
	s_lshl_b32 s2, s58, 16
	v_pk_mul_f32 v[160:161], v[18:19], s[40:41] op_sel_hi:[1,0]
	v_pk_add_f32 v[154:155], v[154:155], v[158:159]
	v_pk_mul_f32 v[158:159], v[20:21], s[40:41] op_sel_hi:[1,0]
	v_pk_fma_f32 v[160:161], v[14:15], s[2:3], v[160:161] op_sel_hi:[1,0,1]
	s_and_b32 s40, s66, 0xffff0000
	v_pk_fma_f32 v[158:159], v[16:17], s[2:3], v[158:159] op_sel_hi:[1,0,1]
	v_pk_add_f32 v[156:157], v[156:157], v[160:161]
	s_lshl_b32 s2, s66, 16
	v_pk_mul_f32 v[160:161], v[30:31], s[40:41] op_sel_hi:[1,0]
	v_pk_add_f32 v[154:155], v[154:155], v[158:159]
	v_pk_mul_f32 v[158:159], v[32:33], s[40:41] op_sel_hi:[1,0]
	v_pk_fma_f32 v[160:161], v[22:23], s[2:3], v[160:161] op_sel_hi:[1,0,1]
	s_and_b32 s40, s67, 0xffff0000
	v_pk_fma_f32 v[158:159], v[24:25], s[2:3], v[158:159] op_sel_hi:[1,0,1]
	v_pk_add_f32 v[156:157], v[156:157], v[160:161]
	s_lshl_b32 s2, s67, 16
	v_pk_mul_f32 v[160:161], v[38:39], s[40:41] op_sel_hi:[1,0]
	v_pk_add_f32 v[154:155], v[154:155], v[158:159]
	v_pk_mul_f32 v[158:159], v[40:41], s[40:41] op_sel_hi:[1,0]
	v_pk_fma_f32 v[160:161], v[34:35], s[2:3], v[160:161] op_sel_hi:[1,0,1]
	s_and_b32 s40, s73, 0xffff0000
	v_pk_fma_f32 v[158:159], v[36:37], s[2:3], v[158:159] op_sel_hi:[1,0,1]
	v_pk_add_f32 v[156:157], v[156:157], v[160:161]
	s_lshl_b32 s2, s73, 16
	v_pk_mul_f32 v[160:161], v[46:47], s[40:41] op_sel_hi:[1,0]
	v_pk_add_f32 v[154:155], v[154:155], v[158:159]
	v_pk_mul_f32 v[158:159], v[48:49], s[40:41] op_sel_hi:[1,0]
	v_pk_fma_f32 v[160:161], v[42:43], s[2:3], v[160:161] op_sel_hi:[1,0,1]
	s_and_b32 s40, s74, 0xffff0000
	v_pk_fma_f32 v[158:159], v[44:45], s[2:3], v[158:159] op_sel_hi:[1,0,1]
	v_pk_add_f32 v[156:157], v[156:157], v[160:161]
	s_lshl_b32 s2, s74, 16
	v_pk_mul_f32 v[160:161], v[54:55], s[40:41] op_sel_hi:[1,0]
	s_and_b32 s58, s75, 0xffff0000
	v_pk_fma_f32 v[160:161], v[50:51], s[2:3], v[160:161] op_sel_hi:[1,0,1]
	v_pk_add_f32 v[154:155], v[154:155], v[158:159]
	v_pk_mul_f32 v[158:159], v[56:57], s[40:41] op_sel_hi:[1,0]
	v_pk_add_f32 v[156:157], v[156:157], v[160:161]
	s_lshl_b32 s40, s75, 16
	v_pk_mul_f32 v[160:161], v[62:63], s[58:59] op_sel_hi:[1,0]
	v_pk_fma_f32 v[158:159], v[52:53], s[2:3], v[158:159] op_sel_hi:[1,0,1]
	v_pk_fma_f32 v[160:161], v[58:59], s[40:41], v[160:161] op_sel_hi:[1,0,1]
	v_pk_add_f32 v[154:155], v[154:155], v[158:159]
	v_pk_add_f32 v[156:157], v[156:157], v[160:161]
	v_pk_mul_f32 v[158:159], v[64:65], s[58:59] op_sel_hi:[1,0]
	v_mul_f32_e64 v160, |v156|, s53
	v_exp_f32_e32 v160, v160
	v_pk_fma_f32 v[158:159], v[60:61], s[40:41], v[158:159] op_sel_hi:[1,0,1]
	v_min_f32_e32 v156, 0, v156
	v_pk_add_f32 v[154:155], v[154:155], v[158:159]
	v_add_f32_e32 v160, 1.0, v160
	v_cmp_gt_f32_e32 vcc, s68, v160
	v_mul_f32_e64 v159, |v157|, s53
	v_exp_f32_e32 v159, v159
	v_cndmask_b32_e64 v161, 0, 32, vcc
	v_ldexp_f32 v160, v160, v161
	v_log_f32_e32 v160, v160
	v_min_f32_e32 v157, 0, v157
	v_readlane_b32 s58, v72, 8
	v_readlane_b32 s66, v73, 8
	v_mul_f32_e32 v158, 0x3f317217, v160
	v_fma_f32 v158, v160, s69, -v158
	v_fmac_f32_e32 v158, 0x3377d1cf, v160
	v_fmac_f32_e32 v158, 0x3f317217, v160
	v_cmp_lt_f32_e64 s[40:41], |v160|, s70
	v_readlane_b32 s67, v70, 9
	v_readlane_b32 s73, v71, 9
	v_cndmask_b32_e64 v158, v160, v158, s[40:41]
	v_cndmask_b32_e32 v160, 0, v184, vcc
	v_sub_f32_e32 v158, v158, v160
	v_sub_f32_e32 v156, v156, v158
	v_add_f32_e32 v158, 1.0, v159
	v_cmp_gt_f32_e32 vcc, s68, v158
	v_readlane_b32 s74, v72, 9
	v_readlane_b32 s75, v73, 9
	v_cndmask_b32_e64 v159, 0, 32, vcc
	v_ldexp_f32 v158, v158, v159
	v_log_f32_e32 v158, v158
	v_cndmask_b32_e32 v160, 0, v184, vcc
	v_mul_f32_e32 v156, 0x3d800000, v156
	v_max_f32_e32 v156, -1.0, v156
	v_mul_f32_e32 v159, 0x3f317217, v158
	v_fma_f32 v159, v158, s69, -v159
	v_fmac_f32_e32 v159, 0x3377d1cf, v158
	v_fmac_f32_e32 v159, 0x3f317217, v158
	v_cmp_lt_f32_e64 s[40:41], |v158|, s70
	v_mul_f32_e32 v151, 0x3d800000, v151
	v_max_f32_e32 v151, -1.0, v151
	v_cndmask_b32_e64 v158, v158, v159, s[40:41]
	v_mul_f32_e64 v159, |v154|, s53
	v_exp_f32_e32 v159, v159
	v_sub_f32_e32 v158, v158, v160
	v_sub_f32_e32 v157, v157, v158
	v_min_f32_e32 v154, 0, v154
	v_add_f32_e32 v158, 1.0, v159
	v_cmp_gt_f32_e32 vcc, s68, v158
	v_mul_f32_e32 v157, 0x3d800000, v157
	v_max_f32_e32 v157, -1.0, v157
	v_cndmask_b32_e64 v159, 0, 32, vcc
	v_ldexp_f32 v158, v158, v159
	v_log_f32_e32 v158, v158
	v_cndmask_b32_e32 v160, 0, v184, vcc
	v_mul_f32_e32 v159, 0x3f317217, v158
	v_fma_f32 v159, v158, s69, -v159
	v_fmac_f32_e32 v159, 0x3377d1cf, v158
	v_fmac_f32_e32 v159, 0x3f317217, v158
	v_cmp_lt_f32_e64 s[40:41], |v158|, s70
	s_nop 1
	v_cndmask_b32_e64 v158, v158, v159, s[40:41]
	v_mul_f32_e64 v159, |v155|, s53
	v_exp_f32_e32 v159, v159
	v_sub_f32_e32 v158, v158, v160
	v_sub_f32_e32 v154, v154, v158
	v_min_f32_e32 v155, 0, v155
	v_add_f32_e32 v158, 1.0, v159
	v_cmp_gt_f32_e32 vcc, s68, v158
	v_mul_f32_e32 v154, 0x3d800000, v154
	v_max_f32_e32 v154, -1.0, v154
	v_cndmask_b32_e64 v159, 0, 32, vcc
	v_ldexp_f32 v158, v158, v159
	v_log_f32_e32 v158, v158
	s_nop 0
	v_mul_f32_e32 v159, 0x3f317217, v158
	v_fma_f32 v159, v158, s69, -v159
	v_fmac_f32_e32 v159, 0x3377d1cf, v158
	v_fmac_f32_e32 v159, 0x3f317217, v158
	v_cmp_lt_f32_e64 s[40:41], |v158|, s70
	s_nop 1
	v_cndmask_b32_e64 v158, v158, v159, s[40:41]
	v_cndmask_b32_e32 v159, 0, v184, vcc
	v_readlane_b32 s40, v70, 8
	v_sub_f32_e32 v158, v158, v159
	v_readlane_b32 s41, v71, 8
	s_lshl_b32 s2, s40, 16
	s_and_b32 s40, s40, 0xffff0000
	v_sub_f32_e32 v155, v155, v158
	v_pk_mul_f32 v[158:159], v[4:5], s[40:41] op_sel_hi:[1,0]
	v_pk_mul_f32 v[160:161], v[2:3], s[40:41] op_sel_hi:[1,0]
	s_and_b32 s40, s41, 0xffff0000
	v_pk_fma_f32 v[158:159], v[28:29], s[2:3], v[158:159] op_sel_hi:[1,0,1]
	v_pk_fma_f32 v[160:161], v[26:27], s[2:3], v[160:161] op_sel_hi:[1,0,1]
	s_lshl_b32 s2, s41, 16
	v_pk_mul_f32 v[164:165], v[10:11], s[40:41] op_sel_hi:[1,0]
	v_pk_add_f32 v[160:161], v[66:67], v[160:161]
	v_pk_mul_f32 v[162:163], v[12:13], s[40:41] op_sel_hi:[1,0]
	v_pk_fma_f32 v[164:165], v[6:7], s[2:3], v[164:165] op_sel_hi:[1,0,1]
	s_and_b32 s40, s58, 0xffff0000
	v_pk_add_f32 v[158:159], v[68:69], v[158:159]
	v_pk_fma_f32 v[162:163], v[8:9], s[2:3], v[162:163] op_sel_hi:[1,0,1]
	v_pk_add_f32 v[160:161], v[160:161], v[164:165]
	s_lshl_b32 s2, s58, 16
	v_pk_mul_f32 v[164:165], v[18:19], s[40:41] op_sel_hi:[1,0]
	v_pk_add_f32 v[158:159], v[158:159], v[162:163]
	v_pk_mul_f32 v[162:163], v[20:21], s[40:41] op_sel_hi:[1,0]
	v_pk_fma_f32 v[164:165], v[14:15], s[2:3], v[164:165] op_sel_hi:[1,0,1]
	s_and_b32 s40, s66, 0xffff0000
	v_pk_fma_f32 v[162:163], v[16:17], s[2:3], v[162:163] op_sel_hi:[1,0,1]
	v_pk_add_f32 v[160:161], v[160:161], v[164:165]
	s_lshl_b32 s2, s66, 16
	v_pk_mul_f32 v[164:165], v[30:31], s[40:41] op_sel_hi:[1,0]
	v_pk_add_f32 v[158:159], v[158:159], v[162:163]
	v_pk_mul_f32 v[162:163], v[32:33], s[40:41] op_sel_hi:[1,0]
	v_pk_fma_f32 v[164:165], v[22:23], s[2:3], v[164:165] op_sel_hi:[1,0,1]
	s_and_b32 s40, s67, 0xffff0000
	v_pk_fma_f32 v[162:163], v[24:25], s[2:3], v[162:163] op_sel_hi:[1,0,1]
	v_pk_add_f32 v[160:161], v[160:161], v[164:165]
	s_lshl_b32 s2, s67, 16
	v_pk_mul_f32 v[164:165], v[38:39], s[40:41] op_sel_hi:[1,0]
	v_pk_add_f32 v[158:159], v[158:159], v[162:163]
	v_pk_mul_f32 v[162:163], v[40:41], s[40:41] op_sel_hi:[1,0]
	v_pk_fma_f32 v[164:165], v[34:35], s[2:3], v[164:165] op_sel_hi:[1,0,1]
	s_and_b32 s40, s73, 0xffff0000
	v_pk_fma_f32 v[162:163], v[36:37], s[2:3], v[162:163] op_sel_hi:[1,0,1]
	v_pk_add_f32 v[160:161], v[160:161], v[164:165]
	s_lshl_b32 s2, s73, 16
	v_pk_mul_f32 v[164:165], v[46:47], s[40:41] op_sel_hi:[1,0]
	v_pk_add_f32 v[158:159], v[158:159], v[162:163]
	v_pk_mul_f32 v[162:163], v[48:49], s[40:41] op_sel_hi:[1,0]
	v_pk_fma_f32 v[164:165], v[42:43], s[2:3], v[164:165] op_sel_hi:[1,0,1]
	s_and_b32 s40, s74, 0xffff0000
	v_pk_fma_f32 v[162:163], v[44:45], s[2:3], v[162:163] op_sel_hi:[1,0,1]
	v_pk_add_f32 v[160:161], v[160:161], v[164:165]
	s_lshl_b32 s2, s74, 16
	v_pk_mul_f32 v[164:165], v[54:55], s[40:41] op_sel_hi:[1,0]
	s_and_b32 s58, s75, 0xffff0000
	v_pk_fma_f32 v[164:165], v[50:51], s[2:3], v[164:165] op_sel_hi:[1,0,1]
	v_pk_add_f32 v[158:159], v[158:159], v[162:163]
	v_pk_mul_f32 v[162:163], v[56:57], s[40:41] op_sel_hi:[1,0]
	v_pk_add_f32 v[160:161], v[160:161], v[164:165]
	s_lshl_b32 s40, s75, 16
	v_pk_mul_f32 v[164:165], v[62:63], s[58:59] op_sel_hi:[1,0]
	v_pk_fma_f32 v[162:163], v[52:53], s[2:3], v[162:163] op_sel_hi:[1,0,1]
	v_pk_fma_f32 v[164:165], v[58:59], s[40:41], v[164:165] op_sel_hi:[1,0,1]
	v_pk_add_f32 v[158:159], v[158:159], v[162:163]
	v_pk_add_f32 v[160:161], v[160:161], v[164:165]
	v_pk_mul_f32 v[162:163], v[64:65], s[58:59] op_sel_hi:[1,0]
	v_mul_f32_e64 v164, |v160|, s53
	v_exp_f32_e32 v164, v164
	v_pk_fma_f32 v[162:163], v[60:61], s[40:41], v[162:163] op_sel_hi:[1,0,1]
	v_min_f32_e32 v160, 0, v160
	v_pk_add_f32 v[158:159], v[158:159], v[162:163]
	v_add_f32_e32 v164, 1.0, v164
	v_cmp_gt_f32_e32 vcc, s68, v164
	v_mul_f32_e64 v163, |v161|, s53
	v_exp_f32_e32 v163, v163
	v_cndmask_b32_e64 v165, 0, 32, vcc
	v_ldexp_f32 v164, v164, v165
	v_log_f32_e32 v164, v164
	v_min_f32_e32 v161, 0, v161
	v_readlane_b32 s58, v72, 10
	v_readlane_b32 s66, v73, 10
	v_mul_f32_e32 v162, 0x3f317217, v164
	v_fma_f32 v162, v164, s69, -v162
	v_fmac_f32_e32 v162, 0x3377d1cf, v164
	v_fmac_f32_e32 v162, 0x3f317217, v164
	v_cmp_lt_f32_e64 s[40:41], |v164|, s70
	v_readlane_b32 s67, v70, 11
	v_readlane_b32 s73, v71, 11
	v_cndmask_b32_e64 v162, v164, v162, s[40:41]
	v_cndmask_b32_e32 v164, 0, v184, vcc
	v_sub_f32_e32 v162, v162, v164
	v_sub_f32_e32 v160, v160, v162
	v_add_f32_e32 v162, 1.0, v163
	v_cmp_gt_f32_e32 vcc, s68, v162
	v_readlane_b32 s74, v72, 11
	v_readlane_b32 s75, v73, 11
	v_cndmask_b32_e64 v163, 0, 32, vcc
	v_ldexp_f32 v162, v162, v163
	v_log_f32_e32 v162, v162
	v_cndmask_b32_e32 v164, 0, v184, vcc
	v_mul_f32_e32 v160, 0x3d800000, v160
	v_max_f32_e32 v160, -1.0, v160
	v_mul_f32_e32 v163, 0x3f317217, v162
	v_fma_f32 v163, v162, s69, -v163
	v_fmac_f32_e32 v163, 0x3377d1cf, v162
	v_fmac_f32_e32 v163, 0x3f317217, v162
	v_cmp_lt_f32_e64 s[40:41], |v162|, s70
	v_mul_f32_e32 v155, 0x3d800000, v155
	v_max_f32_e32 v155, -1.0, v155
	v_cndmask_b32_e64 v162, v162, v163, s[40:41]
	v_mul_f32_e64 v163, |v158|, s53
	v_exp_f32_e32 v163, v163
	v_sub_f32_e32 v162, v162, v164
	v_sub_f32_e32 v161, v161, v162
	v_min_f32_e32 v158, 0, v158
	v_add_f32_e32 v162, 1.0, v163
	v_cmp_gt_f32_e32 vcc, s68, v162
	v_mul_f32_e32 v161, 0x3d800000, v161
	v_max_f32_e32 v161, -1.0, v161
	v_cndmask_b32_e64 v163, 0, 32, vcc
	v_ldexp_f32 v162, v162, v163
	v_log_f32_e32 v162, v162
	v_cndmask_b32_e32 v164, 0, v184, vcc
	v_mul_f32_e32 v163, 0x3f317217, v162
	v_fma_f32 v163, v162, s69, -v163
	v_fmac_f32_e32 v163, 0x3377d1cf, v162
	v_fmac_f32_e32 v163, 0x3f317217, v162
	v_cmp_lt_f32_e64 s[40:41], |v162|, s70
	s_nop 1
	v_cndmask_b32_e64 v162, v162, v163, s[40:41]
	v_mul_f32_e64 v163, |v159|, s53
	v_exp_f32_e32 v163, v163
	v_sub_f32_e32 v162, v162, v164
	v_sub_f32_e32 v158, v158, v162
	v_min_f32_e32 v159, 0, v159
	v_add_f32_e32 v162, 1.0, v163
	v_cmp_gt_f32_e32 vcc, s68, v162
	v_mul_f32_e32 v158, 0x3d800000, v158
	v_max_f32_e32 v158, -1.0, v158
	v_cndmask_b32_e64 v163, 0, 32, vcc
	v_ldexp_f32 v162, v162, v163
	v_log_f32_e32 v162, v162
	s_nop 0
	v_mul_f32_e32 v163, 0x3f317217, v162
	v_fma_f32 v163, v162, s69, -v163
	v_fmac_f32_e32 v163, 0x3377d1cf, v162
	v_fmac_f32_e32 v163, 0x3f317217, v162
	v_cmp_lt_f32_e64 s[40:41], |v162|, s70
	s_nop 1
	v_cndmask_b32_e64 v162, v162, v163, s[40:41]
	v_cndmask_b32_e32 v163, 0, v184, vcc
	v_readlane_b32 s40, v70, 10
	v_sub_f32_e32 v162, v162, v163
	v_readlane_b32 s41, v71, 10
	s_lshl_b32 s2, s40, 16
	s_and_b32 s40, s40, 0xffff0000
	v_sub_f32_e32 v159, v159, v162
	v_pk_mul_f32 v[162:163], v[4:5], s[40:41] op_sel_hi:[1,0]
	v_pk_mul_f32 v[164:165], v[2:3], s[40:41] op_sel_hi:[1,0]
	s_and_b32 s40, s41, 0xffff0000
	v_pk_fma_f32 v[162:163], v[28:29], s[2:3], v[162:163] op_sel_hi:[1,0,1]
	v_pk_fma_f32 v[164:165], v[26:27], s[2:3], v[164:165] op_sel_hi:[1,0,1]
	s_lshl_b32 s2, s41, 16
	v_pk_mul_f32 v[168:169], v[10:11], s[40:41] op_sel_hi:[1,0]
	v_pk_add_f32 v[164:165], v[66:67], v[164:165]
	v_pk_mul_f32 v[166:167], v[12:13], s[40:41] op_sel_hi:[1,0]
	v_pk_fma_f32 v[168:169], v[6:7], s[2:3], v[168:169] op_sel_hi:[1,0,1]
	s_and_b32 s40, s58, 0xffff0000
	v_pk_add_f32 v[162:163], v[68:69], v[162:163]
	v_pk_fma_f32 v[166:167], v[8:9], s[2:3], v[166:167] op_sel_hi:[1,0,1]
	v_pk_add_f32 v[164:165], v[164:165], v[168:169]
	s_lshl_b32 s2, s58, 16
	v_pk_mul_f32 v[168:169], v[18:19], s[40:41] op_sel_hi:[1,0]
	v_pk_add_f32 v[162:163], v[162:163], v[166:167]
	v_pk_mul_f32 v[166:167], v[20:21], s[40:41] op_sel_hi:[1,0]
	v_pk_fma_f32 v[168:169], v[14:15], s[2:3], v[168:169] op_sel_hi:[1,0,1]
	s_and_b32 s40, s66, 0xffff0000
	v_pk_fma_f32 v[166:167], v[16:17], s[2:3], v[166:167] op_sel_hi:[1,0,1]
	v_pk_add_f32 v[164:165], v[164:165], v[168:169]
	s_lshl_b32 s2, s66, 16
	v_pk_mul_f32 v[168:169], v[30:31], s[40:41] op_sel_hi:[1,0]
	v_pk_add_f32 v[162:163], v[162:163], v[166:167]
	v_pk_mul_f32 v[166:167], v[32:33], s[40:41] op_sel_hi:[1,0]
	v_pk_fma_f32 v[168:169], v[22:23], s[2:3], v[168:169] op_sel_hi:[1,0,1]
	s_and_b32 s40, s67, 0xffff0000
	v_pk_fma_f32 v[166:167], v[24:25], s[2:3], v[166:167] op_sel_hi:[1,0,1]
	v_pk_add_f32 v[164:165], v[164:165], v[168:169]
	s_lshl_b32 s2, s67, 16
	v_pk_mul_f32 v[168:169], v[38:39], s[40:41] op_sel_hi:[1,0]
	v_pk_add_f32 v[162:163], v[162:163], v[166:167]
	v_pk_mul_f32 v[166:167], v[40:41], s[40:41] op_sel_hi:[1,0]
	v_pk_fma_f32 v[168:169], v[34:35], s[2:3], v[168:169] op_sel_hi:[1,0,1]
	s_and_b32 s40, s73, 0xffff0000
	v_pk_fma_f32 v[166:167], v[36:37], s[2:3], v[166:167] op_sel_hi:[1,0,1]
	v_pk_add_f32 v[164:165], v[164:165], v[168:169]
	s_lshl_b32 s2, s73, 16
	v_pk_mul_f32 v[168:169], v[46:47], s[40:41] op_sel_hi:[1,0]
	v_pk_add_f32 v[162:163], v[162:163], v[166:167]
	v_pk_mul_f32 v[166:167], v[48:49], s[40:41] op_sel_hi:[1,0]
	v_pk_fma_f32 v[168:169], v[42:43], s[2:3], v[168:169] op_sel_hi:[1,0,1]
	s_and_b32 s40, s74, 0xffff0000
	v_pk_fma_f32 v[166:167], v[44:45], s[2:3], v[166:167] op_sel_hi:[1,0,1]
	v_pk_add_f32 v[164:165], v[164:165], v[168:169]
	s_lshl_b32 s2, s74, 16
	v_pk_mul_f32 v[168:169], v[54:55], s[40:41] op_sel_hi:[1,0]
	s_and_b32 s58, s75, 0xffff0000
	v_pk_fma_f32 v[168:169], v[50:51], s[2:3], v[168:169] op_sel_hi:[1,0,1]
	v_pk_add_f32 v[162:163], v[162:163], v[166:167]
	v_pk_mul_f32 v[166:167], v[56:57], s[40:41] op_sel_hi:[1,0]
	v_pk_add_f32 v[164:165], v[164:165], v[168:169]
	s_lshl_b32 s40, s75, 16
	v_pk_mul_f32 v[168:169], v[62:63], s[58:59] op_sel_hi:[1,0]
	v_pk_fma_f32 v[166:167], v[52:53], s[2:3], v[166:167] op_sel_hi:[1,0,1]
	v_pk_fma_f32 v[168:169], v[58:59], s[40:41], v[168:169] op_sel_hi:[1,0,1]
	v_pk_add_f32 v[162:163], v[162:163], v[166:167]
	v_pk_add_f32 v[164:165], v[164:165], v[168:169]
	v_pk_mul_f32 v[166:167], v[64:65], s[58:59] op_sel_hi:[1,0]
	v_mul_f32_e64 v168, |v164|, s53
	v_exp_f32_e32 v168, v168
	v_pk_fma_f32 v[166:167], v[60:61], s[40:41], v[166:167] op_sel_hi:[1,0,1]
	v_min_f32_e32 v164, 0, v164
	v_pk_add_f32 v[162:163], v[162:163], v[166:167]
	v_add_f32_e32 v168, 1.0, v168
	v_cmp_gt_f32_e32 vcc, s68, v168
	v_mul_f32_e64 v167, |v165|, s53
	v_exp_f32_e32 v167, v167
	v_cndmask_b32_e64 v169, 0, 32, vcc
	v_ldexp_f32 v168, v168, v169
	v_log_f32_e32 v168, v168
	v_readlane_b32 s58, v72, 12
	v_readlane_b32 s66, v73, 12
	v_readlane_b32 s67, v70, 13
	v_mul_f32_e32 v166, 0x3f317217, v168
	v_fma_f32 v166, v168, s69, -v166
	v_fmac_f32_e32 v166, 0x3377d1cf, v168
	v_fmac_f32_e32 v166, 0x3f317217, v168
	v_cmp_lt_f32_e64 s[40:41], |v168|, s70
	v_readlane_b32 s73, v71, 13
	v_readlane_b32 s74, v72, 13
	v_cndmask_b32_e64 v166, v168, v166, s[40:41]
	v_cndmask_b32_e32 v168, 0, v184, vcc
	v_sub_f32_e32 v166, v166, v168
	v_sub_f32_e32 v164, v164, v166
	v_add_f32_e32 v166, 1.0, v167
	v_cmp_gt_f32_e32 vcc, s68, v166
	v_mul_f32_e32 v164, 0x3d800000, v164
	v_readlane_b32 s75, v73, 13
	v_cndmask_b32_e64 v167, 0, 32, vcc
	v_ldexp_f32 v166, v166, v167
	v_log_f32_e32 v167, v166
	v_max_f32_e32 v166, -1.0, v164
	v_min_f32_e32 v164, 0, v165
	v_cndmask_b32_e32 v168, 0, v184, vcc
	v_mul_f32_e32 v165, 0x3f317217, v167
	v_fma_f32 v165, v167, s69, -v165
	v_fmac_f32_e32 v165, 0x3377d1cf, v167
	v_fmac_f32_e32 v165, 0x3f317217, v167
	v_cmp_lt_f32_e64 s[40:41], |v167|, s70
	v_mul_f32_e32 v159, 0x3d800000, v159
	v_max_f32_e32 v159, -1.0, v159
	v_cndmask_b32_e64 v165, v167, v165, s[40:41]
	v_mul_f32_e64 v167, |v162|, s53
	v_exp_f32_e32 v167, v167
	v_sub_f32_e32 v165, v165, v168
	v_sub_f32_e32 v164, v164, v165
	v_mul_f32_e32 v164, 0x3d800000, v164
	v_add_f32_e32 v165, 1.0, v167
	v_cmp_gt_f32_e32 vcc, s68, v165
	v_min_f32_e32 v162, 0, v162
	s_nop 0
	v_cndmask_b32_e64 v167, 0, 32, vcc
	v_ldexp_f32 v165, v165, v167
	v_log_f32_e32 v165, v165
	v_max_f32_e32 v167, -1.0, v164
	v_cndmask_b32_e32 v168, 0, v184, vcc
	v_mul_f32_e32 v164, 0x3f317217, v165
	v_fma_f32 v164, v165, s69, -v164
	v_fmac_f32_e32 v164, 0x3377d1cf, v165
	v_fmac_f32_e32 v164, 0x3f317217, v165
	v_cmp_lt_f32_e64 s[40:41], |v165|, s70
	s_nop 1
	v_cndmask_b32_e64 v164, v165, v164, s[40:41]
	v_mul_f32_e64 v165, |v163|, s53
	v_exp_f32_e32 v165, v165
	v_sub_f32_e32 v164, v164, v168
	v_sub_f32_e32 v162, v162, v164
	v_mul_f32_e32 v162, 0x3d800000, v162
	v_add_f32_e32 v164, 1.0, v165
	v_cmp_gt_f32_e32 vcc, s68, v164
	s_nop 1
	v_cndmask_b32_e64 v165, 0, 32, vcc
	v_ldexp_f32 v164, v164, v165
	v_log_f32_e32 v165, v164
	v_max_f32_e32 v164, -1.0, v162
	v_min_f32_e32 v162, 0, v163
	v_mul_f32_e32 v163, 0x3f317217, v165
	v_fma_f32 v163, v165, s69, -v163
	v_fmac_f32_e32 v163, 0x3377d1cf, v165
	v_fmac_f32_e32 v163, 0x3f317217, v165
	v_cmp_lt_f32_e64 s[40:41], |v165|, s70
	s_nop 1
	v_cndmask_b32_e64 v163, v165, v163, s[40:41]
	v_cndmask_b32_e32 v165, 0, v184, vcc
	v_sub_f32_e32 v163, v163, v165
	v_sub_f32_e32 v162, v162, v163
	v_readlane_b32 s40, v70, 12
	v_mul_f32_e32 v162, 0x3d800000, v162
	v_readlane_b32 s41, v71, 12
	s_lshl_b32 s2, s40, 16
	s_and_b32 s40, s40, 0xffff0000
	v_max_f32_e32 v165, -1.0, v162
	v_pk_mul_f32 v[162:163], v[4:5], s[40:41] op_sel_hi:[1,0]
	v_pk_mul_f32 v[168:169], v[2:3], s[40:41] op_sel_hi:[1,0]
	s_and_b32 s40, s41, 0xffff0000
	v_pk_fma_f32 v[162:163], v[28:29], s[2:3], v[162:163] op_sel_hi:[1,0,1]
	v_pk_fma_f32 v[168:169], v[26:27], s[2:3], v[168:169] op_sel_hi:[1,0,1]
	s_lshl_b32 s2, s41, 16
	v_pk_mul_f32 v[172:173], v[10:11], s[40:41] op_sel_hi:[1,0]
	v_pk_add_f32 v[168:169], v[66:67], v[168:169]
	v_pk_mul_f32 v[170:171], v[12:13], s[40:41] op_sel_hi:[1,0]
	v_pk_fma_f32 v[172:173], v[6:7], s[2:3], v[172:173] op_sel_hi:[1,0,1]
	s_and_b32 s40, s58, 0xffff0000
	v_pk_add_f32 v[162:163], v[68:69], v[162:163]
	v_pk_fma_f32 v[170:171], v[8:9], s[2:3], v[170:171] op_sel_hi:[1,0,1]
	v_pk_add_f32 v[168:169], v[168:169], v[172:173]
	s_lshl_b32 s2, s58, 16
	v_pk_mul_f32 v[172:173], v[18:19], s[40:41] op_sel_hi:[1,0]
	v_pk_add_f32 v[162:163], v[162:163], v[170:171]
	v_pk_mul_f32 v[170:171], v[20:21], s[40:41] op_sel_hi:[1,0]
	v_pk_fma_f32 v[172:173], v[14:15], s[2:3], v[172:173] op_sel_hi:[1,0,1]
	s_and_b32 s40, s66, 0xffff0000
	v_pk_fma_f32 v[170:171], v[16:17], s[2:3], v[170:171] op_sel_hi:[1,0,1]
	v_pk_add_f32 v[168:169], v[168:169], v[172:173]
	s_lshl_b32 s2, s66, 16
	v_pk_mul_f32 v[172:173], v[30:31], s[40:41] op_sel_hi:[1,0]
	v_pk_add_f32 v[162:163], v[162:163], v[170:171]
	v_pk_mul_f32 v[170:171], v[32:33], s[40:41] op_sel_hi:[1,0]
	v_pk_fma_f32 v[172:173], v[22:23], s[2:3], v[172:173] op_sel_hi:[1,0,1]
	s_and_b32 s40, s67, 0xffff0000
	v_pk_fma_f32 v[170:171], v[24:25], s[2:3], v[170:171] op_sel_hi:[1,0,1]
	v_pk_add_f32 v[168:169], v[168:169], v[172:173]
	s_lshl_b32 s2, s67, 16
	v_pk_mul_f32 v[172:173], v[38:39], s[40:41] op_sel_hi:[1,0]
	v_pk_add_f32 v[162:163], v[162:163], v[170:171]
	v_pk_mul_f32 v[170:171], v[40:41], s[40:41] op_sel_hi:[1,0]
	v_pk_fma_f32 v[172:173], v[34:35], s[2:3], v[172:173] op_sel_hi:[1,0,1]
	s_and_b32 s40, s73, 0xffff0000
	v_pk_fma_f32 v[170:171], v[36:37], s[2:3], v[170:171] op_sel_hi:[1,0,1]
	v_pk_add_f32 v[168:169], v[168:169], v[172:173]
	s_lshl_b32 s2, s73, 16
	v_pk_mul_f32 v[172:173], v[46:47], s[40:41] op_sel_hi:[1,0]
	v_pk_add_f32 v[162:163], v[162:163], v[170:171]
	v_pk_mul_f32 v[170:171], v[48:49], s[40:41] op_sel_hi:[1,0]
	v_pk_fma_f32 v[172:173], v[42:43], s[2:3], v[172:173] op_sel_hi:[1,0,1]
	s_and_b32 s40, s74, 0xffff0000
	v_pk_fma_f32 v[170:171], v[44:45], s[2:3], v[170:171] op_sel_hi:[1,0,1]
	v_pk_add_f32 v[168:169], v[168:169], v[172:173]
	s_lshl_b32 s2, s74, 16
	v_pk_mul_f32 v[172:173], v[54:55], s[40:41] op_sel_hi:[1,0]
	s_and_b32 s58, s75, 0xffff0000
	v_pk_fma_f32 v[172:173], v[50:51], s[2:3], v[172:173] op_sel_hi:[1,0,1]
	v_pk_add_f32 v[162:163], v[162:163], v[170:171]
	v_pk_mul_f32 v[170:171], v[56:57], s[40:41] op_sel_hi:[1,0]
	v_pk_add_f32 v[168:169], v[168:169], v[172:173]
	s_lshl_b32 s40, s75, 16
	v_pk_mul_f32 v[172:173], v[62:63], s[58:59] op_sel_hi:[1,0]
	v_pk_fma_f32 v[170:171], v[52:53], s[2:3], v[170:171] op_sel_hi:[1,0,1]
	v_pk_fma_f32 v[172:173], v[58:59], s[40:41], v[172:173] op_sel_hi:[1,0,1]
	v_pk_add_f32 v[162:163], v[162:163], v[170:171]
	v_pk_add_f32 v[168:169], v[168:169], v[172:173]
	v_pk_mul_f32 v[170:171], v[64:65], s[58:59] op_sel_hi:[1,0]
	v_mul_f32_e64 v172, |v168|, s53
	v_exp_f32_e32 v172, v172
	v_pk_fma_f32 v[170:171], v[60:61], s[40:41], v[170:171] op_sel_hi:[1,0,1]
	v_min_f32_e32 v168, 0, v168
	v_pk_add_f32 v[162:163], v[162:163], v[170:171]
	v_add_f32_e32 v172, 1.0, v172
	v_cmp_gt_f32_e32 vcc, s68, v172
	v_mul_f32_e64 v171, |v169|, s53
	v_exp_f32_e32 v171, v171
	v_cndmask_b32_e64 v173, 0, 32, vcc
	v_ldexp_f32 v172, v172, v173
	v_log_f32_e32 v172, v172
	v_readlane_b32 s58, v72, 14
	v_readlane_b32 s66, v73, 14
	v_readlane_b32 s67, v70, 15
	v_mul_f32_e32 v170, 0x3f317217, v172
	v_fma_f32 v170, v172, s69, -v170
	v_fmac_f32_e32 v170, 0x3377d1cf, v172
	v_fmac_f32_e32 v170, 0x3f317217, v172
	v_cmp_lt_f32_e64 s[40:41], |v172|, s70
	v_readlane_b32 s73, v71, 15
	v_readlane_b32 s74, v72, 15
	v_cndmask_b32_e64 v170, v172, v170, s[40:41]
	v_cndmask_b32_e32 v172, 0, v184, vcc
	v_sub_f32_e32 v170, v170, v172
	v_sub_f32_e32 v168, v168, v170
	v_add_f32_e32 v170, 1.0, v171
	v_cmp_gt_f32_e32 vcc, s68, v170
	v_mul_f32_e32 v168, 0x3d800000, v168
	v_readlane_b32 s75, v73, 15
	v_cndmask_b32_e64 v171, 0, 32, vcc
	v_ldexp_f32 v170, v170, v171
	v_log_f32_e32 v171, v170
	v_max_f32_e32 v170, -1.0, v168
	v_min_f32_e32 v168, 0, v169
	v_cndmask_b32_e32 v172, 0, v184, vcc
	v_mul_f32_e32 v169, 0x3f317217, v171
	v_fma_f32 v169, v171, s69, -v169
	v_fmac_f32_e32 v169, 0x3377d1cf, v171
	v_fmac_f32_e32 v169, 0x3f317217, v171
	v_cmp_lt_f32_e64 s[40:41], |v171|, s70
	s_nop 1
	v_cndmask_b32_e64 v169, v171, v169, s[40:41]
	v_mul_f32_e64 v171, |v162|, s53
	v_exp_f32_e32 v171, v171
	v_sub_f32_e32 v169, v169, v172
	v_sub_f32_e32 v168, v168, v169
	v_mul_f32_e32 v168, 0x3d800000, v168
	v_add_f32_e32 v169, 1.0, v171
	v_cmp_gt_f32_e32 vcc, s68, v169
	v_min_f32_e32 v162, 0, v162
	s_nop 0
	v_cndmask_b32_e64 v171, 0, 32, vcc
	v_ldexp_f32 v169, v169, v171
	v_log_f32_e32 v169, v169
	v_max_f32_e32 v171, -1.0, v168
	v_cndmask_b32_e32 v172, 0, v184, vcc
	v_mul_f32_e32 v168, 0x3f317217, v169
	v_fma_f32 v168, v169, s69, -v168
	v_fmac_f32_e32 v168, 0x3377d1cf, v169
	v_fmac_f32_e32 v168, 0x3f317217, v169
	v_cmp_lt_f32_e64 s[40:41], |v169|, s70
	s_nop 1
	v_cndmask_b32_e64 v168, v169, v168, s[40:41]
	v_mul_f32_e64 v169, |v163|, s53
	v_exp_f32_e32 v169, v169
	v_sub_f32_e32 v168, v168, v172
	v_sub_f32_e32 v162, v162, v168
	v_mul_f32_e32 v162, 0x3d800000, v162
	v_add_f32_e32 v168, 1.0, v169
	v_cmp_gt_f32_e32 vcc, s68, v168
	v_max_f32_e32 v178, -1.0, v162
	v_min_f32_e32 v162, 0, v163
	v_cndmask_b32_e64 v169, 0, 32, vcc
	v_ldexp_f32 v168, v168, v169
	v_log_f32_e32 v168, v168
	s_nop 0
	v_mul_f32_e32 v163, 0x3f317217, v168
	v_fma_f32 v163, v168, s69, -v163
	v_fmac_f32_e32 v163, 0x3377d1cf, v168
	v_fmac_f32_e32 v163, 0x3f317217, v168
	v_cmp_lt_f32_e64 s[40:41], |v168|, s70
	s_nop 1
	v_cndmask_b32_e64 v163, v168, v163, s[40:41]
	v_cndmask_b32_e32 v168, 0, v184, vcc
	v_sub_f32_e32 v163, v163, v168
	v_sub_f32_e32 v162, v162, v163
	v_readlane_b32 s40, v70, 14
	v_mul_f32_e32 v162, 0x3d800000, v162
	v_readlane_b32 s41, v71, 14
	s_lshl_b32 s2, s40, 16
	s_and_b32 s40, s40, 0xffff0000
	v_max_f32_e32 v179, -1.0, v162
	v_pk_mul_f32 v[162:163], v[4:5], s[40:41] op_sel_hi:[1,0]
	v_pk_mul_f32 v[168:169], v[2:3], s[40:41] op_sel_hi:[1,0]
	s_and_b32 s40, s41, 0xffff0000
	v_pk_fma_f32 v[162:163], v[28:29], s[2:3], v[162:163] op_sel_hi:[1,0,1]
	v_pk_fma_f32 v[168:169], v[26:27], s[2:3], v[168:169] op_sel_hi:[1,0,1]
	s_lshl_b32 s2, s41, 16
	v_pk_mul_f32 v[174:175], v[10:11], s[40:41] op_sel_hi:[1,0]
	v_pk_add_f32 v[168:169], v[66:67], v[168:169]
	v_pk_mul_f32 v[172:173], v[12:13], s[40:41] op_sel_hi:[1,0]
	v_pk_fma_f32 v[174:175], v[6:7], s[2:3], v[174:175] op_sel_hi:[1,0,1]
	s_and_b32 s40, s58, 0xffff0000
	v_pk_add_f32 v[162:163], v[68:69], v[162:163]
	v_pk_fma_f32 v[172:173], v[8:9], s[2:3], v[172:173] op_sel_hi:[1,0,1]
	v_pk_add_f32 v[168:169], v[168:169], v[174:175]
	s_lshl_b32 s2, s58, 16
	v_pk_mul_f32 v[174:175], v[18:19], s[40:41] op_sel_hi:[1,0]
	v_pk_add_f32 v[162:163], v[162:163], v[172:173]
	v_pk_mul_f32 v[172:173], v[20:21], s[40:41] op_sel_hi:[1,0]
	v_pk_fma_f32 v[174:175], v[14:15], s[2:3], v[174:175] op_sel_hi:[1,0,1]
	s_and_b32 s40, s66, 0xffff0000
	v_pk_fma_f32 v[172:173], v[16:17], s[2:3], v[172:173] op_sel_hi:[1,0,1]
	v_pk_add_f32 v[168:169], v[168:169], v[174:175]
	s_lshl_b32 s2, s66, 16
	v_pk_mul_f32 v[174:175], v[30:31], s[40:41] op_sel_hi:[1,0]
	v_pk_add_f32 v[162:163], v[162:163], v[172:173]
	v_pk_mul_f32 v[172:173], v[32:33], s[40:41] op_sel_hi:[1,0]
	v_pk_fma_f32 v[174:175], v[22:23], s[2:3], v[174:175] op_sel_hi:[1,0,1]
	s_and_b32 s40, s67, 0xffff0000
	v_pk_fma_f32 v[172:173], v[24:25], s[2:3], v[172:173] op_sel_hi:[1,0,1]
	v_pk_add_f32 v[168:169], v[168:169], v[174:175]
	s_lshl_b32 s2, s67, 16
	v_pk_mul_f32 v[174:175], v[38:39], s[40:41] op_sel_hi:[1,0]
	v_pk_add_f32 v[162:163], v[162:163], v[172:173]
	v_pk_mul_f32 v[172:173], v[40:41], s[40:41] op_sel_hi:[1,0]
	v_pk_fma_f32 v[174:175], v[34:35], s[2:3], v[174:175] op_sel_hi:[1,0,1]
	s_and_b32 s40, s73, 0xffff0000
	v_pk_fma_f32 v[172:173], v[36:37], s[2:3], v[172:173] op_sel_hi:[1,0,1]
	v_pk_add_f32 v[168:169], v[168:169], v[174:175]
	s_lshl_b32 s2, s73, 16
	v_pk_mul_f32 v[174:175], v[46:47], s[40:41] op_sel_hi:[1,0]
	v_pk_add_f32 v[162:163], v[162:163], v[172:173]
	v_pk_mul_f32 v[172:173], v[48:49], s[40:41] op_sel_hi:[1,0]
	v_pk_fma_f32 v[174:175], v[42:43], s[2:3], v[174:175] op_sel_hi:[1,0,1]
	s_and_b32 s40, s74, 0xffff0000
	v_pk_fma_f32 v[172:173], v[44:45], s[2:3], v[172:173] op_sel_hi:[1,0,1]
	v_pk_add_f32 v[168:169], v[168:169], v[174:175]
	s_lshl_b32 s2, s74, 16
	v_pk_mul_f32 v[174:175], v[54:55], s[40:41] op_sel_hi:[1,0]
	s_and_b32 s58, s75, 0xffff0000
	v_pk_fma_f32 v[174:175], v[50:51], s[2:3], v[174:175] op_sel_hi:[1,0,1]
	v_pk_add_f32 v[162:163], v[162:163], v[172:173]
	v_pk_mul_f32 v[172:173], v[56:57], s[40:41] op_sel_hi:[1,0]
	v_pk_add_f32 v[168:169], v[168:169], v[174:175]
	s_lshl_b32 s40, s75, 16
	v_pk_mul_f32 v[174:175], v[62:63], s[58:59] op_sel_hi:[1,0]
	v_pk_fma_f32 v[172:173], v[52:53], s[2:3], v[172:173] op_sel_hi:[1,0,1]
	v_pk_fma_f32 v[174:175], v[58:59], s[40:41], v[174:175] op_sel_hi:[1,0,1]
	v_pk_add_f32 v[162:163], v[162:163], v[172:173]
	v_pk_add_f32 v[168:169], v[168:169], v[174:175]
	v_pk_mul_f32 v[172:173], v[64:65], s[58:59] op_sel_hi:[1,0]
	v_mul_f32_e64 v174, |v168|, s53
	v_exp_f32_e32 v174, v174
	v_pk_fma_f32 v[172:173], v[60:61], s[40:41], v[172:173] op_sel_hi:[1,0,1]
	v_add_f32_e32 v174, 1.0, v174
	v_cmp_gt_f32_e32 vcc, s68, v174
	s_nop 1
	v_cndmask_b32_e64 v175, 0, 32, vcc
	v_ldexp_f32 v174, v174, v175
	v_log_f32_e32 v176, v174
	v_pk_add_f32 v[174:175], v[162:163], v[172:173]
	v_min_f32_e32 v162, 0, v168
	v_mul_f32_e64 v168, |v169|, s53
	v_mul_f32_e32 v163, 0x3f317217, v176
	v_fma_f32 v163, v176, s69, -v163
	v_fmac_f32_e32 v163, 0x3377d1cf, v176
	v_exp_f32_e32 v168, v168
	v_fmac_f32_e32 v163, 0x3f317217, v176
	v_cmp_lt_f32_e64 s[40:41], |v176|, s70
	v_cndmask_b32_e32 v172, 0, v184, vcc
	s_nop 0
	v_cndmask_b32_e64 v163, v176, v163, s[40:41]
	v_sub_f32_e32 v163, v163, v172
	v_sub_f32_e32 v162, v162, v163
	v_add_f32_e32 v163, 1.0, v168
	v_cmp_gt_f32_e32 vcc, s68, v163
	v_pk_add_f32 v[176:177], v[74:75], 0 op_sel_hi:[1,0]
	v_mul_f32_e64 v74, |v174|, s53
	v_cndmask_b32_e64 v168, 0, 32, vcc
	v_ldexp_f32 v163, v163, v168
	v_log_f32_e32 v163, v163
	v_exp_f32_e32 v74, v74
	v_mul_f32_e32 v162, 0x3d800000, v162
	v_max_f32_e32 v186, -1.0, v162
	v_mul_f32_e32 v168, 0x3f317217, v163
	v_fma_f32 v168, v163, s69, -v168
	v_fmac_f32_e32 v168, 0x3377d1cf, v163
	v_fmac_f32_e32 v168, 0x3f317217, v163
	v_cmp_lt_f32_e64 s[40:41], |v163|, s70
	v_add_f32_e32 v74, 1.0, v74
	v_min_f32_e32 v162, 0, v169
	v_cndmask_b32_e64 v163, v163, v168, s[40:41]
	v_cndmask_b32_e32 v168, 0, v184, vcc
	v_cmp_gt_f32_e32 vcc, s68, v74
	v_sub_f32_e32 v163, v163, v168
	v_sub_f32_e32 v162, v162, v163
	v_cndmask_b32_e64 v75, 0, 32, vcc
	v_ldexp_f32 v74, v74, v75
	v_pk_add_f32 v[172:173], v[176:177], v[80:81]
	v_log_f32_e32 v80, v74
	v_mul_f32_e32 v162, 0x3d800000, v162
	v_pk_add_f32 v[168:169], v[172:173], v[152:153]
	v_max_f32_e32 v187, -1.0, v162
	v_pk_add_f32 v[162:163], v[168:169], v[156:157]
	v_cmp_lt_f32_e64 s[40:41], |v80|, s70
	v_pk_add_f32 v[160:161], v[162:163], v[160:161]
	v_min_f32_e32 v81, 0, v174
	v_pk_add_f32 v[156:157], v[160:161], v[166:167]
	v_mul_f32_e32 v166, 0x3f317217, v80
	v_fma_f32 v166, v80, s69, -v166
	v_fmac_f32_e32 v166, 0x3377d1cf, v80
	v_fmac_f32_e32 v166, 0x3f317217, v80
	v_cndmask_b32_e64 v80, v80, v166, s[40:41]
	v_mul_f32_e64 v166, |v175|, s53
	v_exp_f32_e32 v166, v166
	v_cndmask_b32_e32 v167, 0, v184, vcc
	v_sub_f32_e32 v80, v80, v167
	v_sub_f32_e32 v80, v81, v80
	v_add_f32_e32 v81, 1.0, v166
	v_cmp_gt_f32_e32 vcc, s68, v81
	v_pk_add_f32 v[152:153], v[156:157], v[170:171]
	v_mul_f32_e32 v80, 0x3d800000, v80
	v_cndmask_b32_e64 v166, 0, 32, vcc
	v_ldexp_f32 v81, v81, v166
	v_log_f32_e32 v81, v81
	v_min_f32_e32 v166, 0, v175
	v_pk_add_f32 v[174:175], v[190:191], v[78:79]
	v_max_f32_e32 v80, -1.0, v80
	v_mul_f32_e32 v167, 0x3f317217, v81
	v_fma_f32 v167, v81, s69, -v167
	v_fmac_f32_e32 v167, 0x3377d1cf, v81
	v_fmac_f32_e32 v167, 0x3f317217, v81
	v_cmp_lt_f32_e64 s[40:41], |v81|, s70
	v_pk_add_f32 v[170:171], v[174:175], v[150:151]
	v_pk_add_f32 v[74:75], v[152:153], v[186:187]
	v_cndmask_b32_e64 v81, v81, v167, s[40:41]
	v_cndmask_b32_e32 v167, 0, v184, vcc
	v_sub_f32_e32 v81, v81, v167
	v_sub_f32_e32 v81, v166, v81
	v_pk_add_f32 v[166:167], v[170:171], v[154:155]
	v_mul_f32_e32 v81, 0x3d800000, v81
	v_pk_add_f32 v[158:159], v[166:167], v[158:159]
	v_max_f32_e32 v81, -1.0, v81
	v_pk_add_f32 v[154:155], v[158:159], v[164:165]
	s_ashr_i32 s41, s72, 31
	v_pk_add_f32 v[150:151], v[154:155], v[178:179]
	s_mov_b32 s40, s72
	v_pk_add_f32 v[76:77], v[150:151], v[80:81]
	ds_write_b128 v85, v[74:77]
	s_waitcnt lgkmcnt(0)
	s_barrier
	ds_read_b128 v[78:81], v97
	ds_read_b128 v[186:189], v97 offset:1024
	s_lshl_b64 s[66:67], s[40:41], 11
	s_andn2_b64 vcc, exec, s[60:61]
	s_waitcnt lgkmcnt(1)
	v_pk_add_f32 v[80:81], v[80:81], 0 op_sel_hi:[1,0]
	v_pk_add_f32 v[78:79], v[78:79], 0 op_sel_hi:[1,0]
	v_cndmask_b32_e64 v179, 0, v81, s[6:7]
	v_cndmask_b32_e64 v165, 0, v79, s[6:7]
	v_cndmask_b32_e64 v164, 0, v78, s[6:7]
	v_cndmask_b32_e64 v178, 0, v80, s[6:7]
	s_waitcnt lgkmcnt(0)
	v_pk_add_f32 v[192:193], v[80:81], v[188:189]
	v_pk_add_f32 v[194:195], v[78:79], v[186:187]
	ds_read_b128 v[78:81], v97 offset:2048
	v_pk_add_f32 v[186:187], v[186:187], v[164:165]
	v_pk_add_f32 v[188:189], v[188:189], v[178:179]
	v_cndmask_b32_e64 v165, v165, v187, s[8:9]
	v_cndmask_b32_e64 v164, v164, v186, s[8:9]
	v_cndmask_b32_e64 v179, v179, v189, s[8:9]
	v_cndmask_b32_e64 v178, v178, v188, s[8:9]
	ds_read_b128 v[186:189], v97 offset:3072
	s_waitcnt lgkmcnt(1)
	v_pk_add_f32 v[192:193], v[192:193], v[80:81]
	v_pk_add_f32 v[194:195], v[194:195], v[78:79]
	v_pk_add_f32 v[78:79], v[78:79], v[164:165]
	v_pk_add_f32 v[80:81], v[80:81], v[178:179]
	v_cndmask_b32_e64 v165, v165, v79, s[10:11]
	v_cndmask_b32_e64 v164, v164, v78, s[10:11]
	v_cndmask_b32_e64 v179, v179, v81, s[10:11]
	v_cndmask_b32_e64 v178, v178, v80, s[10:11]
	ds_read_b128 v[78:81], v97 offset:4096
	s_waitcnt lgkmcnt(1)
	v_pk_add_f32 v[192:193], v[192:193], v[188:189]
	v_pk_add_f32 v[194:195], v[194:195], v[186:187]
	v_pk_add_f32 v[186:187], v[186:187], v[164:165]
	v_pk_add_f32 v[188:189], v[188:189], v[178:179]
	v_cndmask_b32_e64 v165, v165, v187, s[12:13]
	v_cndmask_b32_e64 v164, v164, v186, s[12:13]
	v_cndmask_b32_e64 v179, v179, v189, s[12:13]
	v_cndmask_b32_e64 v178, v178, v188, s[12:13]
	ds_read_b128 v[186:189], v97 offset:5120
	s_waitcnt lgkmcnt(1)
	v_pk_add_f32 v[192:193], v[192:193], v[80:81]
	v_pk_add_f32 v[194:195], v[194:195], v[78:79]
	v_pk_add_f32 v[78:79], v[78:79], v[164:165]
	v_pk_add_f32 v[80:81], v[80:81], v[178:179]
	v_cndmask_b32_e64 v165, v165, v79, s[14:15]
	v_cndmask_b32_e64 v164, v164, v78, s[14:15]
	v_cndmask_b32_e64 v179, v179, v81, s[14:15]
	v_cndmask_b32_e64 v178, v178, v80, s[14:15]
	ds_read_b128 v[78:81], v97 offset:6144
	s_waitcnt lgkmcnt(1)
	v_pk_add_f32 v[192:193], v[192:193], v[188:189]
	v_pk_add_f32 v[194:195], v[194:195], v[186:187]
	v_pk_add_f32 v[186:187], v[186:187], v[164:165]
	v_pk_add_f32 v[188:189], v[188:189], v[178:179]
	v_cndmask_b32_e64 v165, v165, v187, s[16:17]
	v_cndmask_b32_e64 v164, v164, v186, s[16:17]
	v_cndmask_b32_e64 v179, v179, v189, s[16:17]
	v_cndmask_b32_e64 v178, v178, v188, s[16:17]
	ds_read_b128 v[186:189], v97 offset:7168
	s_waitcnt lgkmcnt(1)
	v_pk_add_f32 v[194:195], v[194:195], v[78:79]
	v_pk_add_f32 v[78:79], v[78:79], v[164:165]
	v_pk_add_f32 v[192:193], v[192:193], v[80:81]
	v_cndmask_b32_e64 v165, v165, v79, s[18:19]
	v_cndmask_b32_e64 v164, v164, v78, s[18:19]
	s_waitcnt lgkmcnt(0)
	v_pk_add_f32 v[78:79], v[194:195], v[186:187]
	v_pk_add_f32 v[186:187], v[186:187], v[164:165]
	v_pk_add_f32 v[80:81], v[80:81], v[178:179]
	v_cndmask_b32_e64 v186, v164, v186, s[20:21]
	v_add_f32_e32 v176, v176, v186
	v_mul_f32_e32 v195, 0x3fb8aa3b, v176
	v_exp_f32_e32 v195, v195
	v_mul_f32_e32 v176, 0xbfb8aa3b, v176
	v_exp_f32_e32 v176, v176
	s_waitcnt vmcnt(8)
	v_lshlrev_b32_e32 v164, 16, v126
	v_cndmask_b32_e64 v187, v165, v187, s[20:21]
	v_mul_f32_e32 v164, 0x3d800000, v164
	v_cndmask_b32_e64 v179, v179, v81, s[18:19]
	v_cndmask_b32_e64 v178, v178, v80, s[18:19]
	v_pk_add_f32 v[80:81], v[192:193], v[188:189]
	v_lshlrev_b32_e32 v192, 16, v104
	v_mul_f32_e32 v195, v164, v195
	v_add_f32_e32 v164, v177, v187
	v_mul_f32_e32 v192, v176, v192
	v_mul_f32_e32 v176, 0x3fb8aa3b, v164
	v_mul_f32_e32 v164, 0xbfb8aa3b, v164
	v_exp_f32_e32 v164, v164
	v_exp_f32_e32 v176, v176
	v_pk_add_f32 v[188:189], v[188:189], v[178:179]
	v_and_b32_e32 v165, 0xffff0000, v126
	v_cndmask_b32_e64 v178, v178, v188, s[20:21]
	v_and_b32_e32 v193, 0xffff0000, v104
	v_mul_f32_e32 v165, 0x3d800000, v165
	v_mul_f32_e32 v193, v164, v193
	v_add_f32_e32 v164, v190, v178
	v_mul_f32_e32 v176, v165, v176
	v_mul_f32_e32 v165, 0x3fb8aa3b, v164
	v_mul_f32_e32 v164, 0xbfb8aa3b, v164
	v_exp_f32_e32 v164, v164
	v_exp_f32_e32 v165, v165
	v_cndmask_b32_e64 v179, v179, v189, s[20:21]
	v_lshlrev_b32_e32 v188, 16, v127
	v_lshlrev_b32_e32 v194, 16, v105
	v_mul_f32_e32 v177, 0x3d800000, v188
	v_mul_f32_e32 v188, v164, v194
	v_add_f32_e32 v164, v191, v179
	v_mul_f32_e32 v177, v177, v165
	v_mul_f32_e32 v165, 0x3fb8aa3b, v164
	v_mul_f32_e32 v164, 0xbfb8aa3b, v164
	v_mul_f32_e32 v81, 0x3fb8aa3b, v81
	v_exp_f32_e32 v191, v165
	v_exp_f32_e32 v164, v164
	v_add_f32_e32 v172, v172, v186
	v_exp_f32_e32 v81, v81
	v_mul_f32_e32 v194, 0x3fb8aa3b, v172
	v_mul_f32_e32 v172, 0xbfb8aa3b, v172
	v_and_b32_e32 v189, 0xffff0000, v127
	v_exp_f32_e32 v172, v172
	v_mul_f32_e32 v189, 0x3d800000, v189
	v_mul_f32_e32 v189, v189, v191
	v_mul_f32_e32 v191, v164, v196
	v_cvt_pk_bf16_f32 v176, v195, v176
	v_cvt_pk_bf16_f32 v177, v177, v189
	v_mul_f32_e32 v164, v81, v191
	ds_write_b64 v101, v[176:177]
	v_cvt_pk_bf16_f32 v176, v192, v193
	v_cvt_pk_bf16_f32 v177, v188, v191
	s_waitcnt vmcnt(13)
	v_lshlrev_b32_e32 v191, 16, v108
	v_mul_f32_e32 v78, 0x3fb8aa3b, v78
	v_mul_f32_e32 v191, v172, v191
	v_add_f32_e32 v172, v173, v187
	v_exp_f32_e32 v78, v78
	v_mul_f32_e32 v173, 0x3fb8aa3b, v172
	v_mul_f32_e32 v172, 0xbfb8aa3b, v172
	v_exp_f32_e32 v173, v173
	v_exp_f32_e32 v172, v172
	ds_write_b64 v101, v[176:177] offset:33792
	s_waitcnt vmcnt(12)
	v_and_b32_e32 v177, 0xffff0000, v114
	v_mul_f32_e32 v80, 0x3fb8aa3b, v80
	v_mul_f32_e32 v197, v78, v192
	v_and_b32_e32 v192, 0xffff0000, v108
	v_mul_f32_e32 v177, 0x3d800000, v177
	v_mul_f32_e32 v79, 0x3fb8aa3b, v79
	v_exp_f32_e32 v80, v80
	v_mul_f32_e32 v173, v177, v173
	v_mul_f32_e32 v177, v172, v192
	v_add_f32_e32 v172, v174, v178
	v_exp_f32_e32 v79, v79
	v_mul_f32_e32 v174, 0x3fb8aa3b, v172
	v_mul_f32_e32 v172, 0xbfb8aa3b, v172
	v_exp_f32_e32 v174, v174
	v_exp_f32_e32 v172, v172
	v_mul_f32_e32 v165, v80, v188
	v_lshlrev_b32_e32 v188, 16, v115
	v_mul_f32_e32 v190, v79, v193
	v_lshlrev_b32_e32 v193, 16, v109
	v_mul_f32_e32 v188, 0x3d800000, v188
	v_mul_f32_e32 v174, v188, v174
	v_mul_f32_e32 v188, v172, v193
	v_add_f32_e32 v172, v175, v179
	v_mul_f32_e32 v175, 0x3fb8aa3b, v172
	v_mul_f32_e32 v172, 0xbfb8aa3b, v172
	v_exp_f32_e32 v194, v194
	v_exp_f32_e32 v175, v175
	v_exp_f32_e32 v172, v172
	v_lshlrev_b32_e32 v176, 16, v114
	v_and_b32_e32 v189, 0xffff0000, v115
	v_and_b32_e32 v195, 0xffff0000, v109
	v_mul_f32_e32 v176, 0x3d800000, v176
	v_mul_f32_e32 v189, 0x3d800000, v189
	v_mul_f32_e32 v176, v176, v194
	v_mul_f32_e32 v175, v189, v175
	v_mul_f32_e32 v189, v172, v195
	v_cvt_pk_bf16_f32 v172, v176, v173
	v_cvt_pk_bf16_f32 v173, v174, v175
	v_add_f32_e32 v168, v168, v186
	v_mul_f32_e32 v195, v81, v189
	ds_write_b64 v101, v[172:173] offset:528
	v_cvt_pk_bf16_f32 v172, v191, v177
	v_cvt_pk_bf16_f32 v173, v188, v189
	v_mul_f32_e32 v189, 0x3fb8aa3b, v168
	v_mul_f32_e32 v168, 0xbfb8aa3b, v168
	v_exp_f32_e32 v168, v168
	s_waitcnt vmcnt(10)
	v_lshlrev_b32_e32 v176, 16, v120
	ds_write_b64 v101, v[172:173] offset:34320
	v_and_b32_e32 v173, 0xffff0000, v118
	v_mul_f32_e32 v176, v168, v176
	v_add_f32_e32 v168, v169, v187
	v_mul_f32_e32 v169, 0x3fb8aa3b, v168
	v_mul_f32_e32 v168, 0xbfb8aa3b, v168
	v_exp_f32_e32 v169, v169
	v_exp_f32_e32 v168, v168
	v_mul_f32_e32 v192, v79, v177
	v_and_b32_e32 v177, 0xffff0000, v120
	v_mul_f32_e32 v173, 0x3d800000, v173
	v_mul_f32_e32 v169, v173, v169
	v_mul_f32_e32 v173, v168, v177
	v_add_f32_e32 v168, v170, v178
	v_mul_f32_e32 v170, 0x3fb8aa3b, v168
	v_mul_f32_e32 v168, 0xbfb8aa3b, v168
	v_exp_f32_e32 v170, v170
	v_exp_f32_e32 v168, v168
	v_lshlrev_b32_e32 v174, 16, v119
	v_mul_f32_e32 v193, v80, v188
	v_lshlrev_b32_e32 v188, 16, v121
	v_mul_f32_e32 v174, 0x3d800000, v174
	v_mul_f32_e32 v170, v174, v170
	v_mul_f32_e32 v174, v168, v188
	v_add_f32_e32 v168, v171, v179
	v_mul_f32_e32 v171, 0x3fb8aa3b, v168
	v_mul_f32_e32 v168, 0xbfb8aa3b, v168
	v_exp_f32_e32 v189, v189
	v_exp_f32_e32 v171, v171
	v_exp_f32_e32 v168, v168
	v_lshlrev_b32_e32 v172, 16, v118
	v_and_b32_e32 v175, 0xffff0000, v119
	v_mul_f32_e32 v194, v78, v191
	v_and_b32_e32 v191, 0xffff0000, v121
	v_mul_f32_e32 v172, 0x3d800000, v172
	v_mul_f32_e32 v175, 0x3d800000, v175
	v_mul_f32_e32 v172, v172, v189
	v_mul_f32_e32 v171, v175, v171
	v_mul_f32_e32 v175, v168, v191
	v_cvt_pk_bf16_f32 v168, v172, v169
	v_cvt_pk_bf16_f32 v169, v170, v171
	v_add_f32_e32 v162, v162, v186
	v_mul_f32_e32 v191, v81, v175
	ds_write_b64 v101, v[168:169] offset:1056
	v_cvt_pk_bf16_f32 v168, v176, v173
	v_cvt_pk_bf16_f32 v169, v174, v175
	v_mul_f32_e32 v175, 0x3fb8aa3b, v162
	v_mul_f32_e32 v162, 0xbfb8aa3b, v162
	v_exp_f32_e32 v162, v162
	s_waitcnt vmcnt(3)
	v_lshlrev_b32_e32 v172, 16, v140
	ds_write_b64 v101, v[168:169] offset:34848
	v_and_b32_e32 v169, 0xffff0000, v130
	v_mul_f32_e32 v172, v162, v172
	v_add_f32_e32 v162, v163, v187
	v_mul_f32_e32 v163, 0x3fb8aa3b, v162
	v_mul_f32_e32 v162, 0xbfb8aa3b, v162
	v_exp_f32_e32 v163, v163
	v_exp_f32_e32 v162, v162
	v_mul_f32_e32 v177, v79, v173
	v_and_b32_e32 v173, 0xffff0000, v140
	v_mul_f32_e32 v169, 0x3d800000, v169
	v_mul_f32_e32 v163, v169, v163
	v_mul_f32_e32 v169, v162, v173
	v_add_f32_e32 v162, v166, v178
	v_mul_f32_e32 v166, 0x3fb8aa3b, v162
	v_mul_f32_e32 v162, 0xbfb8aa3b, v162
	v_exp_f32_e32 v166, v166
	v_exp_f32_e32 v162, v162
	v_lshlrev_b32_e32 v170, 16, v131
	v_mul_f32_e32 v188, v80, v174
	v_lshlrev_b32_e32 v174, 16, v141
	v_mul_f32_e32 v170, 0x3d800000, v170
	v_mul_f32_e32 v166, v170, v166
	v_mul_f32_e32 v170, v162, v174
	v_add_f32_e32 v162, v167, v179
	v_mul_f32_e32 v167, 0x3fb8aa3b, v162
	v_mul_f32_e32 v162, 0xbfb8aa3b, v162
	v_exp_f32_e32 v175, v175
	v_exp_f32_e32 v167, v167
	v_exp_f32_e32 v162, v162
	v_lshlrev_b32_e32 v168, 16, v130
	v_and_b32_e32 v171, 0xffff0000, v131
	v_mul_f32_e32 v189, v78, v176
	v_and_b32_e32 v176, 0xffff0000, v141
	v_mul_f32_e32 v168, 0x3d800000, v168
	v_mul_f32_e32 v171, 0x3d800000, v171
	v_mul_f32_e32 v168, v168, v175
	v_mul_f32_e32 v167, v171, v167
	v_mul_f32_e32 v171, v162, v176
	v_cvt_pk_bf16_f32 v162, v168, v163
	v_cvt_pk_bf16_f32 v163, v166, v167
	v_add_f32_e32 v160, v160, v186
	v_mul_f32_e32 v176, v81, v171
	ds_write_b64 v101, v[162:163] offset:1584
	v_cvt_pk_bf16_f32 v162, v172, v169
	v_cvt_pk_bf16_f32 v163, v170, v171
	v_mul_f32_e32 v171, 0x3fb8aa3b, v160
	v_mul_f32_e32 v160, 0xbfb8aa3b, v160
	v_exp_f32_e32 v160, v160
	v_lshlrev_b32_e32 v168, 16, v134
	v_add_f32_e32 v161, v161, v187
	ds_write_b64 v101, v[162:163] offset:35376
	v_mul_f32_e32 v160, v160, v168
	v_mul_f32_e32 v168, 0x3fb8aa3b, v161
	v_exp_f32_e32 v168, v168
	v_and_b32_e32 v163, 0xffff0000, v132
	v_mul_f32_e32 v163, 0x3d800000, v163
	v_add_f32_e32 v158, v158, v178
	v_mul_f32_e32 v163, v163, v168
	v_mul_f32_e32 v168, 0x3fb8aa3b, v158
	v_mul_f32_e32 v158, 0xbfb8aa3b, v158
	v_exp_f32_e32 v168, v168
	v_exp_f32_e32 v158, v158
	v_lshlrev_b32_e32 v166, 16, v133
	v_mul_f32_e32 v174, v80, v170
	v_lshlrev_b32_e32 v170, 16, v135
	v_mul_f32_e32 v166, 0x3d800000, v166
	v_mul_f32_e32 v166, v166, v168
	v_mul_f32_e32 v168, v158, v170
	v_add_f32_e32 v158, v159, v179
	v_mul_f32_e32 v159, 0x3fb8aa3b, v158
	v_exp_f32_e32 v159, v159
	v_mul_f32_e32 v158, 0xbfb8aa3b, v158
	v_exp_f32_e32 v171, v171
	v_mul_f32_e32 v161, 0xbfb8aa3b, v161
	v_exp_f32_e32 v158, v158
	v_and_b32_e32 v167, 0xffff0000, v133
	v_exp_f32_e32 v161, v161
	v_lshlrev_b32_e32 v162, 16, v132
	v_mul_f32_e32 v167, 0x3d800000, v167
	v_mul_f32_e32 v175, v78, v172
	v_and_b32_e32 v172, 0xffff0000, v135
	v_mul_f32_e32 v162, 0x3d800000, v162
	v_mul_f32_e32 v159, v167, v159
	v_mul_f32_e32 v173, v79, v169
	v_and_b32_e32 v169, 0xffff0000, v134
	v_mul_f32_e32 v162, v162, v171
	v_mul_f32_e32 v167, v158, v172
	v_cvt_pk_bf16_f32 v158, v162, v163
	v_cvt_pk_bf16_f32 v159, v166, v159
	v_add_f32_e32 v156, v156, v186
	v_mul_f32_e32 v161, v161, v169
	v_mul_f32_e32 v172, v81, v167
	ds_write_b64 v101, v[158:159] offset:2112
	v_cvt_pk_bf16_f32 v158, v160, v161
	v_cvt_pk_bf16_f32 v159, v168, v167
	v_mul_f32_e32 v167, 0x3fb8aa3b, v156
	v_mul_f32_e32 v156, 0xbfb8aa3b, v156
	v_exp_f32_e32 v156, v156
	s_waitcnt vmcnt(2)
	v_lshlrev_b32_e32 v162, 16, v142
	v_add_f32_e32 v157, v157, v187
	ds_write_b64 v101, v[158:159] offset:35904
	v_mul_f32_e32 v156, v156, v162
	v_mul_f32_e32 v162, 0x3fb8aa3b, v157
	v_exp_f32_e32 v162, v162
	v_and_b32_e32 v159, 0xffff0000, v136
	v_mul_f32_e32 v159, 0x3d800000, v159
	v_add_f32_e32 v154, v154, v178
	v_mul_f32_e32 v159, v159, v162
	v_mul_f32_e32 v162, 0x3fb8aa3b, v154
	v_mul_f32_e32 v154, 0xbfb8aa3b, v154
	v_exp_f32_e32 v162, v162
	v_exp_f32_e32 v154, v154
	v_mul_f32_e32 v171, v78, v160
	v_lshlrev_b32_e32 v160, 16, v137
	v_lshlrev_b32_e32 v166, 16, v143
	v_mul_f32_e32 v160, 0x3d800000, v160
	v_mul_f32_e32 v160, v160, v162
	v_mul_f32_e32 v162, v154, v166
	v_add_f32_e32 v154, v155, v179
	v_mul_f32_e32 v155, 0x3fb8aa3b, v154
	v_exp_f32_e32 v155, v155
	v_mul_f32_e32 v154, 0xbfb8aa3b, v154
	v_exp_f32_e32 v167, v167
	v_mul_f32_e32 v157, 0xbfb8aa3b, v157
	v_exp_f32_e32 v154, v154
	v_mul_f32_e32 v169, v79, v161
	v_and_b32_e32 v161, 0xffff0000, v137
	v_exp_f32_e32 v157, v157
	v_lshlrev_b32_e32 v158, 16, v136
	v_mul_f32_e32 v161, 0x3d800000, v161
	v_mul_f32_e32 v170, v80, v168
	v_and_b32_e32 v168, 0xffff0000, v143
	v_mul_f32_e32 v158, 0x3d800000, v158
	v_mul_f32_e32 v155, v161, v155
	v_and_b32_e32 v163, 0xffff0000, v142
	v_mul_f32_e32 v158, v158, v167
	v_mul_f32_e32 v161, v154, v168
	v_cvt_pk_bf16_f32 v154, v158, v159
	v_cvt_pk_bf16_f32 v155, v160, v155
	v_add_f32_e32 v152, v152, v186
	v_mul_f32_e32 v157, v157, v163
	v_mul_f32_e32 v168, v81, v161
	ds_write_b64 v101, v[154:155] offset:2640
	v_cvt_pk_bf16_f32 v154, v156, v157
	v_cvt_pk_bf16_f32 v155, v162, v161
	v_mul_f32_e32 v161, 0x3fb8aa3b, v152
	v_mul_f32_e32 v152, 0xbfb8aa3b, v152
	v_exp_f32_e32 v152, v152
	v_lshlrev_b32_e32 v158, 16, v144
	v_add_f32_e32 v153, v153, v187
	ds_write_b64 v101, v[154:155] offset:36432
	v_mul_f32_e32 v152, v152, v158
	v_mul_f32_e32 v158, 0x3fb8aa3b, v153
	v_exp_f32_e32 v158, v158
	v_and_b32_e32 v155, 0xffff0000, v138
	v_mul_f32_e32 v155, 0x3d800000, v155
	v_add_f32_e32 v150, v150, v178
	v_mul_f32_e32 v155, v155, v158
	v_mul_f32_e32 v158, 0x3fb8aa3b, v150
	v_mul_f32_e32 v150, 0xbfb8aa3b, v150
	v_exp_f32_e32 v158, v158
	v_exp_f32_e32 v150, v150
	v_mul_f32_e32 v167, v78, v156
	v_lshlrev_b32_e32 v156, 16, v139
	v_lshlrev_b32_e32 v160, 16, v145
	v_mul_f32_e32 v156, 0x3d800000, v156
	v_mul_f32_e32 v156, v156, v158
	v_mul_f32_e32 v158, v150, v160
	v_add_f32_e32 v150, v151, v179
	v_mul_f32_e32 v151, 0x3fb8aa3b, v150
	v_exp_f32_e32 v151, v151
	v_mul_f32_e32 v150, 0xbfb8aa3b, v150
	v_exp_f32_e32 v161, v161
	v_mul_f32_e32 v153, 0xbfb8aa3b, v153
	v_exp_f32_e32 v150, v150
	v_mul_f32_e32 v163, v79, v157
	v_and_b32_e32 v157, 0xffff0000, v139
	v_exp_f32_e32 v153, v153
	v_lshlrev_b32_e32 v154, 16, v138
	v_mul_f32_e32 v157, 0x3d800000, v157
	v_mul_f32_e32 v166, v80, v162
	v_and_b32_e32 v162, 0xffff0000, v145
	v_mul_f32_e32 v154, 0x3d800000, v154
	v_mul_f32_e32 v151, v157, v151
	v_and_b32_e32 v159, 0xffff0000, v144
	v_mul_f32_e32 v154, v154, v161
	v_mul_f32_e32 v157, v150, v162
	v_cvt_pk_bf16_f32 v150, v154, v155
	v_cvt_pk_bf16_f32 v151, v156, v151
	v_add_f32_e32 v74, v74, v186
	v_mul_f32_e32 v153, v153, v159
	v_mul_f32_e32 v162, v81, v157
	ds_write_b64 v101, v[150:151] offset:3168
	v_cvt_pk_bf16_f32 v150, v152, v153
	v_cvt_pk_bf16_f32 v151, v158, v157
	v_mul_f32_e32 v157, 0x3fb8aa3b, v74
	v_mul_f32_e32 v74, 0xbfb8aa3b, v74
	v_exp_f32_e32 v74, v74
	s_waitcnt vmcnt(0)
	v_lshlrev_b32_e32 v154, 16, v148
	ds_write_b64 v101, v[150:151] offset:36960
	v_and_b32_e32 v151, 0xffff0000, v146
	v_mul_f32_e32 v154, v74, v154
	v_add_f32_e32 v74, v75, v187
	v_mul_f32_e32 v75, 0x3fb8aa3b, v74
	v_mul_f32_e32 v74, 0xbfb8aa3b, v74
	v_exp_f32_e32 v75, v75
	v_exp_f32_e32 v74, v74
	v_and_b32_e32 v155, 0xffff0000, v148
	v_mul_f32_e32 v151, 0x3d800000, v151
	v_mul_f32_e32 v75, v151, v75
	v_mul_f32_e32 v151, v74, v155
	v_add_f32_e32 v74, v76, v178
	v_mul_f32_e32 v76, 0x3fb8aa3b, v74
	v_mul_f32_e32 v74, 0xbfb8aa3b, v74
	v_exp_f32_e32 v76, v76
	v_exp_f32_e32 v74, v74
	v_mul_f32_e32 v161, v78, v152
	v_lshlrev_b32_e32 v152, 16, v147
	v_lshlrev_b32_e32 v156, 16, v149
	v_mul_f32_e32 v152, 0x3d800000, v152
	v_mul_f32_e32 v76, v152, v76
	v_mul_f32_e32 v152, v74, v156
	v_add_f32_e32 v74, v77, v179
	v_mul_f32_e32 v77, 0x3fb8aa3b, v74
	v_mul_f32_e32 v74, 0xbfb8aa3b, v74
	v_exp_f32_e32 v157, v157
	v_exp_f32_e32 v77, v77
	v_exp_f32_e32 v74, v74
	v_mul_f32_e32 v159, v79, v153
	v_lshlrev_b32_e32 v150, 16, v146
	v_and_b32_e32 v153, 0xffff0000, v147
	v_mul_f32_e32 v160, v80, v158
	v_and_b32_e32 v158, 0xffff0000, v149
	v_mul_f32_e32 v150, 0x3d800000, v150
	v_mul_f32_e32 v153, 0x3d800000, v153
	v_mul_f32_e32 v150, v150, v157
	v_mul_f32_e32 v77, v153, v77
	v_mul_f32_e32 v153, v74, v158
	v_cvt_pk_bf16_f32 v74, v150, v75
	v_mul_f32_e32 v155, v79, v151
	v_cvt_pk_bf16_f32 v75, v76, v77
	ds_write_b64 v101, v[74:75] offset:3696
	v_cvt_pk_bf16_f32 v74, v154, v151
	v_lshl_add_u64 v[150:151], v[128:129], 0, s[66:67]
	v_mul_f32_e32 v156, v80, v152
	v_mul_f32_e32 v158, v81, v153
	v_cvt_pk_bf16_f32 v75, v152, v153
	v_or_b32_e32 v152, v150, v84
	v_mov_b32_e32 v153, v151
	v_lshl_add_u64 v[152:153], v[152:153], 4, s[56:57]
	v_mul_f32_e32 v157, v78, v154
	ds_write_b64 v101, v[74:75] offset:37488
	v_cvt_pk_bf16_f32 v74, v197, v194
	v_cvt_pk_bf16_f32 v75, v189, v175
	v_cvt_pk_bf16_f32 v76, v171, v167
	v_cvt_pk_bf16_f32 v77, v161, v157
	global_store_dwordx4 v[152:153], v[74:77], off sc1
	v_or_b32_e32 v152, v150, v100
	v_mov_b32_e32 v153, v151
	v_lshl_add_u64 v[152:153], v[152:153], 4, s[56:57]
	v_cvt_pk_bf16_f32 v74, v190, v192
	v_cvt_pk_bf16_f32 v75, v177, v173
	v_cvt_pk_bf16_f32 v76, v169, v163
	v_cvt_pk_bf16_f32 v77, v159, v155
	global_store_dwordx4 v[152:153], v[74:77], off sc1
	v_or_b32_e32 v152, v150, v102
	v_mov_b32_e32 v153, v151
	v_or_b32_e32 v150, v150, v106
	v_cvt_pk_bf16_f32 v74, v165, v193
	v_cvt_pk_bf16_f32 v75, v188, v174
	v_cvt_pk_bf16_f32 v76, v170, v166
	v_cvt_pk_bf16_f32 v77, v160, v156
	v_lshl_add_u64 v[152:153], v[152:153], 4, s[56:57]
	v_lshl_add_u64 v[150:151], v[150:151], 4, s[56:57]
	global_store_dwordx4 v[152:153], v[74:77], off sc1
	s_nop 1
	v_cvt_pk_bf16_f32 v74, v164, v195
	v_cvt_pk_bf16_f32 v75, v191, v176
	v_cvt_pk_bf16_f32 v76, v172, v168
	v_cvt_pk_bf16_f32 v77, v162, v158
	global_store_dwordx4 v[150:151], v[74:77], off sc1
	s_cbranch_vccnz .LBB0_413
	s_lshl_b64 s[66:67], s[40:41], 10
	v_lshl_add_u64 v[74:75], v[86:87], 0, s[66:67]
	global_store_dwordx4 v[74:75], v[78:81], off sc1

.LBB0_476:
	s_waitcnt vmcnt(6)
	s_barrier
	v_add_u32_e32 v103, 0, v86
	ds_read_b128 v[74:77], v100 offset:32960
	ds_read_b128 v[78:81], v100 offset:32896
	ds_read_b128 v[82:85], v100 offset:32832
	ds_read_b128 v[104:107], v100 offset:32768
	ds_read_b128 v[108:111], v103 offset:7168
	ds_read_b128 v[112:115], v103 offset:6144
	ds_read_b128 v[116:119], v103 offset:5120
	ds_read_b128 v[120:123], v103 offset:4096
	ds_read_b128 v[124:127], v103 offset:3072
	ds_read_b128 v[128:131], v103 offset:2048
	ds_read_b128 v[132:135], v103 offset:1024
	ds_read_b128 v[136:139], v103
	v_add_u32_e32 v70, s5, v86
	ds_read_b128 v[66:69], v70 offset:34816
	ds_read_b128 v[70:73], v70 offset:33792
	ds_read_b128 v[140:143], v103 offset:8192
	ds_read_b128 v[144:147], v103 offset:9216
	ds_read_b128 v[148:151], v103 offset:10240
	ds_read_b128 v[152:155], v103 offset:11264
	ds_read_b128 v[156:159], v103 offset:12288
	ds_read_b128 v[160:163], v103 offset:13312
	ds_read_b128 v[164:167], v103 offset:14336
	ds_read_b128 v[168:171], v103 offset:15360
	ds_read_b128 v[172:175], v100 offset:33024
	ds_read_b128 v[176:179], v100 offset:33088
	ds_read_b128 v[180:183], v100 offset:33152
	ds_read_b128 v[184:187], v100 offset:33216
	s_waitcnt lgkmcnt(0)
	v_pk_mul_f32 v[64:65], v[64:65], v[106:107]
	v_pk_mul_f32 v[62:63], v[62:63], v[104:105]
	v_pk_mul_f32 v[60:61], v[60:61], v[84:85]
	v_pk_mul_f32 v[58:59], v[58:59], v[82:83]
	v_mfma_f32_16x16x32_bf16 v[62:65], v[136:139], v[70:73], v[62:65]
	v_mul_f32_e64 v80, v56, v80
	v_mul_f32_e64 v81, v57, v81
	v_pk_mul_f32 v[78:79], v[54:55], v[78:79]
	v_pk_mul_f32 v[52:53], v[52:53], v[76:77]
	v_mfma_f32_16x16x32_bf16 v[58:61], v[128:131], v[70:73], v[58:61]
	v_mul_f32_e64 v50, v50, v74
	v_mul_f32_e64 v51, v51, v75
	v_mfma_f32_16x16x32_bf16 v[62:65], v[132:135], v[66:69], v[62:65]
	v_mfma_f32_16x16x32_bf16 v[56:59], v[124:127], v[66:69], v[58:61]
	v_mfma_f32_16x16x32_bf16 v[74:77], v[120:123], v[70:73], v[78:81]
	s_nop 2
	ds_read_b128 v[78:81], v103 offset:16384
	ds_read_b128 v[104:107], v103 offset:17408
	ds_read_b128 v[120:123], v103 offset:18432
	ds_read_b128 v[124:127], v103 offset:19456
	ds_read_b128 v[128:131], v103 offset:20480
	ds_read_b128 v[132:135], v103 offset:21504
	ds_read_b128 v[136:139], v103 offset:22528
	ds_read_b128 v[188:191], v103 offset:23552
	v_mfma_f32_16x16x32_bf16 v[50:53], v[112:115], v[70:73], v[50:53]
	ds_read_b128 v[112:115], v100 offset:33280
	ds_read_b128 v[192:195], v100 offset:33344
	ds_read_b128 v[196:199], v100 offset:33408
	ds_read_b128 v[200:203], v100 offset:33472
	v_mfma_f32_16x16x32_bf16 v[116:119], v[116:119], v[66:69], v[74:77]
	v_mfma_f32_16x16x32_bf16 v[82:85], v[108:111], v[66:69], v[50:53]
	v_mul_f32_e64 v48, v48, v174
	v_mul_f32_e64 v49, v49, v175
	v_pk_mul_f32 v[46:47], v[46:47], v[172:173]
	v_pk_mul_f32 v[44:45], v[44:45], v[178:179]
	v_pk_mul_f32 v[42:43], v[42:43], v[176:177]
	v_pk_mul_f32 v[52:53], v[40:41], v[182:183]
	v_pk_mul_f32 v[50:51], v[38:39], v[180:181]
	v_mfma_f32_16x16x32_bf16 v[46:49], v[140:143], v[70:73], v[46:49]
	v_mul_f32_e64 v36, v36, v186
	v_mul_f32_e64 v37, v37, v187
	v_pk_mul_f32 v[34:35], v[34:35], v[184:185]
	v_mfma_f32_16x16x32_bf16 v[42:45], v[148:151], v[70:73], v[42:45]
	v_mfma_f32_16x16x32_bf16 v[50:53], v[156:159], v[70:73], v[50:53]
	v_mfma_f32_16x16x32_bf16 v[46:49], v[144:147], v[66:69], v[46:49]
	ds_read_b128 v[108:111], v103 offset:24576
	ds_read_b128 v[140:143], v103 offset:25600
	ds_read_b128 v[144:147], v103 offset:26624
	ds_read_b128 v[148:151], v103 offset:27648
	v_mfma_f32_16x16x32_bf16 v[40:43], v[152:155], v[66:69], v[42:45]
	v_mfma_f32_16x16x32_bf16 v[74:77], v[160:163], v[66:69], v[50:53]
	ds_read_b128 v[152:155], v103 offset:28672
	ds_read_b128 v[156:159], v103 offset:29696
	ds_read_b128 v[160:163], v103 offset:30720
	ds_read_b128 v[172:175], v103 offset:31744
	v_mfma_f32_16x16x32_bf16 v[34:37], v[164:167], v[70:73], v[34:37]
	ds_read_b128 v[164:167], v100 offset:33536
	ds_read_b128 v[176:179], v100 offset:33600
	ds_read_b128 v[180:183], v100 offset:33664
	ds_read_b128 v[184:187], v100 offset:33728
	v_mfma_f32_16x16x32_bf16 v[50:53], v[168:171], v[66:69], v[34:37]
	s_waitcnt lgkmcnt(0)
	v_pk_mul_f32 v[32:33], v[32:33], v[114:115]
	v_pk_mul_f32 v[30:31], v[30:31], v[112:113]
	v_pk_mul_f32 v[24:25], v[24:25], v[194:195]
	v_pk_mul_f32 v[22:23], v[22:23], v[192:193]
	v_pk_mul_f32 v[20:21], v[20:21], v[198:199]
	v_pk_mul_f32 v[18:19], v[18:19], v[196:197]
	v_pk_mul_f32 v[12:13], v[12:13], v[202:203]
	v_pk_mul_f32 v[10:11], v[10:11], v[200:201]
	v_mfma_f32_16x16x32_bf16 v[30:33], v[78:81], v[70:73], v[30:33]
	v_mfma_f32_16x16x32_bf16 v[22:25], v[120:123], v[70:73], v[22:25]
	v_mfma_f32_16x16x32_bf16 v[18:21], v[128:131], v[70:73], v[18:21]
	v_mfma_f32_16x16x32_bf16 v[10:13], v[136:139], v[70:73], v[10:13]
	v_mfma_f32_16x16x32_bf16 v[30:33], v[104:107], v[66:69], v[30:33]
	v_mfma_f32_16x16x32_bf16 v[22:25], v[124:127], v[66:69], v[22:25]
	v_mfma_f32_16x16x32_bf16 v[18:21], v[132:135], v[66:69], v[18:21]
	v_mfma_f32_16x16x32_bf16 v[10:13], v[188:191], v[66:69], v[10:13]
	v_mul_f32_e64 v8, v8, v166
	v_mul_f32_e64 v9, v9, v167
	v_pk_mul_f32 v[6:7], v[6:7], v[164:165]
	v_pk_mul_f32 v[4:5], v[4:5], v[178:179]
	v_pk_mul_f32 v[2:3], v[2:3], v[176:177]
	v_mfma_f32_16x16x32_bf16 v[6:9], v[108:111], v[70:73], v[6:9]
	s_waitcnt vmcnt(0)
	s_barrier
	v_mfma_f32_16x16x32_bf16 v[2:5], v[144:147], v[70:73], v[2:5]
	v_add_u32_e32 v38, 0x14400, v100
	v_mfma_f32_16x16x32_bf16 v[34:37], v[140:143], v[66:69], v[6:9]
	s_nop 3
	v_mul_f32_e64 v8, v28, v182
	v_mul_f32_e64 v9, v29, v183
	v_pk_mul_f32 v[6:7], v[26:27], v[180:181]
	v_pk_mul_f32 v[28:29], v[16:17], v[186:187]
	v_pk_mul_f32 v[26:27], v[14:15], v[184:185]
	v_mfma_f32_16x16x32_bf16 v[78:81], v[148:151], v[66:69], v[2:5]
	s_nop 2
	v_add_u32_e32 v2, s33, v86
	v_mfma_f32_16x16x32_bf16 v[14:17], v[152:155], v[70:73], v[6:9]
	s_nop 2
	ds_read_b128 v[6:9], v2
	ds_read_b128 v[2:5], v2 offset:1024
	ds_read_b128 v[104:107], v103 offset:50176
	ds_read_b128 v[108:111], v103 offset:51200
	ds_read_b128 v[112:115], v103 offset:52224
	ds_read_b128 v[120:123], v103 offset:53248
	ds_read_b128 v[124:127], v103 offset:54272
	ds_read_b128 v[128:131], v103 offset:55296
	v_mfma_f32_16x16x32_bf16 v[26:29], v[160:163], v[70:73], v[26:29]
	ds_read_b128 v[70:73], v103 offset:56320
	ds_read_b128 v[132:135], v103 offset:57344
	ds_read_b128 v[136:139], v38
	ds_read_b128 v[140:143], v38 offset:64
	ds_read_b128 v[144:147], v38 offset:128
	ds_read_b128 v[148:151], v38 offset:192
	v_mfma_f32_16x16x32_bf16 v[14:17], v[156:159], v[66:69], v[14:17]
	v_mfma_f32_16x16x32_bf16 v[26:29], v[172:175], v[66:69], v[26:29]
	ds_read_b128 v[66:69], v103 offset:59392
	ds_read_b128 v[152:155], v103 offset:60416
	ds_read_b128 v[156:159], v103 offset:61440
	ds_read_b128 v[160:163], v103 offset:62464
	ds_read_b128 v[164:167], v103 offset:63488
	ds_read_b128 v[168:171], v103 offset:64512
	ds_read_b128 v[172:175], v103 offset:58368
	ds_read_b128 v[176:179], v1 offset:15360
	v_add_u32_e32 v38, 0x14500, v100
	v_add_u32_e32 v39, 0x14540, v100
	ds_read_b128 v[180:183], v38
	ds_read_b128 v[184:187], v39
	v_add_u32_e32 v38, 0x14580, v100
	v_add_u32_e32 v39, 0x145c0, v100
	ds_read_b128 v[188:191], v38
	ds_read_b128 v[192:195], v39
	s_waitcnt lgkmcnt(0)
	v_pk_mul_f32 v[64:65], v[64:65], v[138:139]
	v_pk_mul_f32 v[62:63], v[62:63], v[136:137]
	v_pk_mul_f32 v[58:59], v[58:59], v[142:143]
	v_pk_mul_f32 v[56:57], v[56:57], v[140:141]
	v_mfma_f32_16x16x32_bf16 v[60:63], v[104:107], v[6:9], v[62:65]
	v_mul_f32_e64 v106, v118, v146
	v_mul_f32_e64 v107, v119, v147
	v_pk_mul_f32 v[104:105], v[116:117], v[144:145]
	v_add_u32_e32 v38, 0x14600, v100
	v_mfma_f32_16x16x32_bf16 v[54:57], v[112:115], v[6:9], v[56:59]
	v_mul_f32_e64 v84, v84, v150
	v_mul_f32_e64 v85, v85, v151
	v_pk_mul_f32 v[82:83], v[82:83], v[148:149]
	v_add_u32_e32 v39, 0x14640, v100
	v_mfma_f32_16x16x32_bf16 v[104:107], v[124:127], v[6:9], v[104:107]
	v_mfma_f32_16x16x32_bf16 v[60:63], v[108:111], v[2:5], v[60:63]
	ds_read_b128 v[108:111], v1 offset:16384
	ds_read_b128 v[112:115], v1 offset:17408
	v_mfma_f32_16x16x32_bf16 v[54:57], v[120:123], v[2:5], v[54:57]
	ds_read_b128 v[116:119], v1 offset:18432
	ds_read_b128 v[120:123], v1 offset:19456
	ds_read_b128 v[136:139], v1 offset:20480
	ds_read_b128 v[140:143], v1 offset:21504
	ds_read_b128 v[124:127], v1 offset:22528
	ds_read_b128 v[144:147], v1 offset:23552
	v_mfma_f32_16x16x32_bf16 v[104:107], v[128:131], v[2:5], v[104:107]
	ds_read_b128 v[128:131], v38
	ds_read_b128 v[148:151], v39
	v_add_u32_e32 v38, 0x14680, v100
	v_add_u32_e32 v39, 0x146c0, v100
	v_mfma_f32_16x16x32_bf16 v[70:73], v[70:73], v[6:9], v[82:85]
	s_nop 2
	ds_read_b128 v[82:85], v38
	ds_read_b128 v[196:199], v39
	v_mfma_f32_16x16x32_bf16 v[70:73], v[132:135], v[2:5], v[70:73]
	v_mul_f32_e64 v48, v48, v182
	v_mul_f32_e64 v49, v49, v183
	v_pk_mul_f32 v[46:47], v[46:47], v[180:181]
	v_pk_mul_f32 v[42:43], v[42:43], v[186:187]
	v_pk_mul_f32 v[40:41], v[40:41], v[184:185]
	v_mfma_f32_16x16x32_bf16 v[44:47], v[172:175], v[6:9], v[46:49]
	v_mul_f32_e64 v64, v74, v188
	v_mul_f32_e64 v65, v75, v189
	v_pk_mul_f32 v[52:53], v[52:53], v[194:195]
	v_pk_mul_f32 v[50:51], v[50:51], v[192:193]
	v_mfma_f32_16x16x32_bf16 v[44:47], v[66:69], v[2:5], v[44:47]
	v_mul_f32_e64 v66, v76, v190
	v_mul_f32_e64 v67, v77, v191
	ds_read_b128 v[74:77], v1 offset:24576
	ds_read_b128 v[132:135], v1 offset:25600
	v_mfma_f32_16x16x32_bf16 v[38:41], v[152:155], v[6:9], v[40:43]
	v_mfma_f32_16x16x32_bf16 v[64:67], v[160:163], v[6:9], v[64:67]
	s_nop 1
	v_add_u32_e32 v42, 0x14700, v100
	v_add_u32_e32 v43, 0x14740, v100
	v_mfma_f32_16x16x32_bf16 v[38:41], v[156:159], v[2:5], v[38:41]
	ds_read_b128 v[152:155], v1 offset:26624
	ds_read_b128 v[156:159], v1 offset:27648
	ds_read_b128 v[172:175], v1 offset:28672
	ds_read_b128 v[180:183], v1 offset:29696
	ds_read_b128 v[160:163], v1 offset:30720
	ds_read_b128 v[184:187], v1 offset:31744
	v_mfma_f32_16x16x32_bf16 v[64:67], v[164:167], v[2:5], v[64:67]
	ds_read_b128 v[164:167], v42
	ds_read_b128 v[188:191], v43
	v_add_u32_e32 v42, 0x14780, v100
	v_add_u32_e32 v43, 0x147c0, v100
	v_mfma_f32_16x16x32_bf16 v[48:51], v[168:171], v[6:9], v[50:53]
	ds_read_b128 v[168:171], v42
	ds_read_b128 v[192:195], v43
	v_mfma_f32_16x16x32_bf16 v[48:51], v[176:179], v[2:5], v[48:51]
	s_waitcnt lgkmcnt(0)
	v_pk_mul_f32 v[32:33], v[32:33], v[130:131]
	v_pk_mul_f32 v[30:31], v[30:31], v[128:129]
	v_pk_mul_f32 v[24:25], v[24:25], v[150:151]
	v_pk_mul_f32 v[22:23], v[22:23], v[148:149]
	v_pk_mul_f32 v[20:21], v[20:21], v[84:85]
	v_pk_mul_f32 v[18:19], v[18:19], v[82:83]
	v_pk_mul_f32 v[12:13], v[12:13], v[198:199]
	v_pk_mul_f32 v[10:11], v[10:11], v[196:197]
	v_mfma_f32_16x16x32_bf16 v[30:33], v[108:111], v[6:9], v[30:33]
	v_mfma_f32_16x16x32_bf16 v[22:25], v[116:119], v[6:9], v[22:25]
	v_mfma_f32_16x16x32_bf16 v[18:21], v[136:139], v[6:9], v[18:21]
	v_mfma_f32_16x16x32_bf16 v[10:13], v[124:127], v[6:9], v[10:13]
	v_mfma_f32_16x16x32_bf16 v[30:33], v[112:115], v[2:5], v[30:33]
	v_mfma_f32_16x16x32_bf16 v[22:25], v[120:123], v[2:5], v[22:25]
	v_mfma_f32_16x16x32_bf16 v[18:21], v[140:143], v[2:5], v[18:21]
	v_mfma_f32_16x16x32_bf16 v[10:13], v[144:147], v[2:5], v[10:13]
	s_add_i32 s6, s12, s62
	v_pk_mul_f32 v[36:37], v[36:37], v[166:167]
	v_pk_mul_f32 v[34:35], v[34:35], v[164:165]
	s_ashr_i32 s7, s6, 31
	s_lshl_b64 s[6:7], s[6:7], 14
	v_mfma_f32_16x16x32_bf16 v[34:37], v[74:77], v[6:9], v[34:37]
	v_mul_f32_e64 v76, v80, v190
	v_mul_f32_e64 v77, v81, v191
	v_pk_mul_f32 v[74:75], v[78:79], v[188:189]
	v_pk_mul_f32 v[16:17], v[16:17], v[170:171]
	v_pk_mul_f32 v[14:15], v[14:15], v[168:169]
	v_mfma_f32_16x16x32_bf16 v[74:77], v[152:155], v[6:9], v[74:77]
	v_mul_f32_e64 v28, v28, v194
	v_mul_f32_e64 v29, v29, v195
	v_pk_mul_f32 v[26:27], v[26:27], v[192:193]
	v_lshl_add_u64 v[42:43], v[98:99], 0, s[6:7]
	v_mfma_f32_16x16x32_bf16 v[14:17], v[172:175], v[6:9], v[14:17]
	v_add_co_u32_e32 v52, vcc, s75, v42
	s_add_i32 s78, s78, s91
	v_mfma_f32_16x16x32_bf16 v[6:9], v[160:163], v[6:9], v[26:29]
	v_addc_co_u32_e32 v53, vcc, 0, v43, vcc
	s_add_i32 s77, s77, s91
	v_mfma_f32_16x16x32_bf16 v[34:37], v[132:135], v[2:5], v[34:37]
	v_add_co_u32_e32 v26, vcc, s76, v42
	s_cmpk_gt_i32 s78, 0xff
	v_mfma_f32_16x16x32_bf16 v[74:77], v[156:159], v[2:5], v[74:77]
	v_addc_co_u32_e32 v27, vcc, 0, v43, vcc
	global_store_dwordx4 v[42:43], v[60:63], off sc1
	global_store_dwordx4 v[42:43], v[54:57], off offset:1024 sc1
	global_store_dwordx4 v[42:43], v[104:107], off offset:2048 sc1
	v_mfma_f32_16x16x32_bf16 v[14:17], v[180:183], v[2:5], v[14:17]
	global_store_dwordx4 v[42:43], v[70:73], off offset:3072 sc1
	global_store_dwordx4 v[26:27], v[44:47], off offset:-4096 sc1
	global_store_dwordx4 v[52:53], v[38:41], off offset:1024 sc1
	global_store_dwordx4 v[52:53], v[64:67], off offset:2048 sc1
	global_store_dwordx4 v[52:53], v[48:51], off offset:3072 sc1
	global_store_dwordx4 v[26:27], v[30:33], off sc1
	global_store_dwordx4 v[26:27], v[22:25], off offset:1024 sc1
	global_store_dwordx4 v[26:27], v[18:21], off offset:2048 sc1
	global_store_dwordx4 v[26:27], v[10:13], off offset:3072 sc1
	v_mfma_f32_16x16x32_bf16 v[2:5], v[184:187], v[2:5], v[6:9]
	s_nop 2
	v_add_co_u32_e32 v6, vcc, 0x3000, v42
	s_nop 1
	v_addc_co_u32_e32 v7, vcc, 0, v43, vcc
	global_store_dwordx4 v[6:7], v[34:37], off sc1
	global_store_dwordx4 v[6:7], v[74:77], off offset:1024 sc1
	global_store_dwordx4 v[6:7], v[14:17], off offset:2048 sc1
	global_store_dwordx4 v[6:7], v[2:5], off offset:3072 sc1
	s_waitcnt vmcnt(0)
	s_barrier
	s_cbranch_scc1 .LBB0_489

.LBB0_716:
	v_lshl_or_b32 v4, s14, 8, v181
	v_lshl_add_u32 v186, s16, 8, v1
	v_ashrrev_i32_e32 v5, 31, v4
	v_lshlrev_b64 v[220:221], 1, v[4:5]
	v_ashrrev_i32_e32 v187, 31, v186
	v_lshl_add_u64 v[184:185], s[20:21], 0, v[220:221]
	v_lshlrev_b64 v[222:223], 12, v[186:187]
	v_lshl_add_u64 v[134:135], v[184:185], 0, v[222:223]
	global_load_dwordx4 v[212:215], v[134:135], off
	global_load_dwordx4 v[216:219], v[134:135], off offset:256
	v_lshl_add_u64 v[188:189], v[186:187], 2, s[26:27]
	global_load_dword v224, v[188:189], off
	v_or_b32_e32 v202, 16, v186
	v_or_b32_e32 v198, 32, v186
	v_or_b32_e32 v192, 48, v186
	v_ashrrev_i32_e32 v203, 31, v202
	v_ashrrev_i32_e32 v199, 31, v198
	v_ashrrev_i32_e32 v193, 31, v192
	v_lshlrev_b64 v[136:137], 12, v[202:203]
	v_lshlrev_b64 v[140:141], 12, v[198:199]
	v_lshl_add_u64 v[134:135], v[202:203], 2, s[26:27]
	v_lshl_add_u64 v[138:139], v[198:199], 2, s[26:27]
	v_lshlrev_b64 v[142:143], 12, v[192:193]
	v_lshl_add_u64 v[136:137], v[184:185], 0, v[136:137]
	v_lshl_add_u64 v[140:141], v[184:185], 0, v[140:141]
	v_lshl_add_u64 v[226:227], v[192:193], 2, s[26:27]
	v_lshl_add_u64 v[228:229], v[184:185], 0, v[142:143]
	global_load_dword v206, v[134:135], off
	global_load_dwordx4 v[154:157], v[136:137], off
	global_load_dwordx4 v[150:153], v[136:137], off offset:256
	global_load_dword v200, v[138:139], off
	global_load_dwordx4 v[146:149], v[140:141], off
	global_load_dwordx4 v[142:145], v[140:141], off offset:256
	global_load_dword v194, v[226:227], off
	s_nop 0
	global_load_dwordx4 v[138:141], v[228:229], off
	global_load_dwordx4 v[134:137], v[228:229], off offset:256
	s_waitcnt vmcnt(0)
	v_lshlrev_b32_e32 v226, 16, v212
	v_and_b32_e32 v227, 0xffff0000, v212
	v_lshlrev_b32_e32 v212, 16, v213
	v_and_b32_e32 v213, 0xffff0000, v213
	v_lshlrev_b32_e32 v230, 16, v216
	v_and_b32_e32 v231, 0xffff0000, v216
	v_lshlrev_b32_e32 v216, 16, v217
	v_and_b32_e32 v217, 0xffff0000, v217
	v_lshlrev_b32_e32 v228, 16, v214
	v_and_b32_e32 v229, 0xffff0000, v214
	v_lshlrev_b32_e32 v214, 16, v215
	v_and_b32_e32 v215, 0xffff0000, v215
	v_lshlrev_b32_e32 v232, 16, v218
	v_and_b32_e32 v233, 0xffff0000, v218
	v_lshlrev_b32_e32 v218, 16, v219
	v_and_b32_e32 v219, 0xffff0000, v219
	v_pk_mul_f32 v[226:227], v[224:225], v[226:227] op_sel_hi:[0,1]
	v_pk_mul_f32 v[212:213], v[224:225], v[212:213] op_sel_hi:[0,1]
	v_pk_mul_f32 v[230:231], v[224:225], v[230:231] op_sel_hi:[0,1]
	v_pk_mul_f32 v[216:217], v[224:225], v[216:217] op_sel_hi:[0,1]
	v_pk_mul_f32 v[228:229], v[224:225], v[228:229] op_sel_hi:[0,1]
	v_pk_mul_f32 v[214:215], v[224:225], v[214:215] op_sel_hi:[0,1]
	v_pk_mul_f32 v[232:233], v[224:225], v[232:233] op_sel_hi:[0,1]
	v_pk_mul_f32 v[218:219], v[224:225], v[218:219] op_sel_hi:[0,1]
	v_pk_fma_f32 v[132:133], v[132:133], v[208:209], v[212:213] op_sel_hi:[1,0,1]
	v_pk_fma_f32 v[130:131], v[130:131], v[208:209], v[226:227] op_sel_hi:[1,0,1]
	v_pk_fma_f32 v[124:125], v[124:125], v[208:209], v[216:217] op_sel_hi:[1,0,1]
	v_pk_fma_f32 v[122:123], v[122:123], v[208:209], v[230:231] op_sel_hi:[1,0,1]
	v_pk_fma_f32 v[128:129], v[128:129], v[208:209], v[214:215] op_sel_hi:[1,0,1]
	v_pk_fma_f32 v[126:127], v[126:127], v[208:209], v[228:229] op_sel_hi:[1,0,1]
	v_pk_fma_f32 v[212:213], v[120:121], v[208:209], v[218:219] op_sel_hi:[1,0,1]
	v_pk_fma_f32 v[208:209], v[118:119], v[208:209], v[232:233] op_sel_hi:[1,0,1]
	v_cvt_pk_bf16_f32 v118, v130, v131
	v_cvt_pk_bf16_f32 v119, v132, v133
	v_mul_f32_e32 v3, v131, v131
	v_mul_f32_e32 v131, v133, v133
	v_mul_f32_e32 v133, v123, v123
	v_mul_f32_e32 v179, v125, v125
	v_cvt_pk_bf16_f32 v120, v126, v127
	v_mul_f32_e32 v127, v127, v127
	v_mul_f32_e32 v183, v209, v209
	v_fmac_f32_e32 v3, v130, v130
	v_fmac_f32_e32 v131, v132, v132
	v_fmac_f32_e32 v133, v122, v122
	v_fmac_f32_e32 v179, v124, v124
	v_cvt_pk_bf16_f32 v121, v128, v129
	v_mul_f32_e32 v129, v129, v129
	v_mul_f32_e32 v197, v213, v213
	v_fmac_f32_e32 v127, v126, v126
	v_fmac_f32_e32 v183, v208, v208
	v_add_f32_e32 v3, v3, v131
	v_add_f32_e32 v126, v133, v179
	v_fmac_f32_e32 v129, v128, v128
	v_add_f32_e32 v3, v127, v3
	v_add_f32_e32 v126, v183, v126
	v_fmac_f32_e32 v197, v212, v212
	v_add_f32_e32 v3, v129, v3
	v_add_f32_e32 v126, v197, v126
	v_add_f32_e32 v128, v3, v126
	v_and_b32_e32 v126, 64, v211
	v_xor_b32_e32 v3, 16, v211
	v_add_u32_e32 v129, 64, v126
	v_cmp_lt_i32_e32 vcc, v3, v129
	v_lshl_add_u64 v[126:127], s[22:23], 0, v[222:223]
	v_lshl_add_u64 v[126:127], v[126:127], 0, v[220:221]
	v_cndmask_b32_e32 v3, v211, v3, vcc
	v_lshlrev_b32_e32 v3, 2, v3
	ds_bpermute_b32 v130, v3, v128
	global_store_dwordx4 v[126:127], v[118:121], off sc1
	v_cvt_pk_bf16_f32 v122, v122, v123
	v_cvt_pk_bf16_f32 v123, v124, v125
	v_cvt_pk_bf16_f32 v124, v208, v209
	v_cvt_pk_bf16_f32 v125, v212, v213
	global_store_dwordx4 v[126:127], v[122:125], off offset:256 sc1
	s_nop 0
	v_xor_b32_e32 v118, 32, v211
	v_cmp_lt_i32_e32 vcc, v118, v129
	s_waitcnt lgkmcnt(0)
	v_add_f32_e32 v119, v128, v130
	v_cndmask_b32_e32 v118, v211, v118, vcc
	v_lshlrev_b32_e32 v118, 2, v118
	ds_bpermute_b32 v120, v118, v119
	s_and_saveexec_b64 s[54:55], s[8:9]
	s_cbranch_execz .LBB0_718
	s_waitcnt lgkmcnt(0)
	v_add_f32_e32 v119, v119, v120
	s_lshl_b32 s56, s14, 2
	v_lshlrev_b64 v[120:121], 7, v[186:187]
	s_ashr_i32 s57, s56, 31
	v_lshl_add_u64 v[120:121], s[24:25], 0, v[120:121]
	v_lshl_add_u64 v[120:121], s[56:57], 2, v[120:121]
	s_lshl_b32 s16, s50, 2
	v_lshl_add_u64 v[120:121], v[120:121], 0, s[16:17]
	global_store_dword v[120:121], v119, off
.LBB0_718:
	s_or_b64 exec, exec, s[54:55]
	v_lshlrev_b32_e32 v122, 16, v154
	v_and_b32_e32 v123, 0xffff0000, v154
	v_lshlrev_b32_e32 v124, 16, v155
	v_and_b32_e32 v125, 0xffff0000, v155
	v_lshlrev_b32_e32 v126, 16, v156
	v_and_b32_e32 v127, 0xffff0000, v156
	v_pk_mul_f32 v[122:123], v[206:207], v[122:123] op_sel_hi:[0,1]
	v_pk_mul_f32 v[124:125], v[206:207], v[124:125] op_sel_hi:[0,1]
	v_pk_fma_f32 v[114:115], v[114:115], v[204:205], v[122:123] op_sel_hi:[1,0,1]
	v_pk_mul_f32 v[122:123], v[206:207], v[126:127] op_sel_hi:[0,1]
	v_pk_fma_f32 v[116:117], v[116:117], v[204:205], v[124:125] op_sel_hi:[1,0,1]
	v_pk_fma_f32 v[122:123], v[110:111], v[204:205], v[122:123] op_sel_hi:[1,0,1]
	v_cvt_pk_bf16_f32 v110, v114, v115
	v_mul_f32_e32 v115, v115, v115
	v_fmac_f32_e32 v115, v114, v114
	v_mul_f32_e32 v114, v117, v117
	v_lshlrev_b32_e32 v128, 16, v157
	v_and_b32_e32 v129, 0xffff0000, v157
	v_fmac_f32_e32 v114, v116, v116
	v_pk_mul_f32 v[124:125], v[206:207], v[128:129] op_sel_hi:[0,1]
	v_add_f32_e32 v114, v115, v114
	v_mul_f32_e32 v115, v123, v123
	v_pk_fma_f32 v[124:125], v[112:113], v[204:205], v[124:125] op_sel_hi:[1,0,1]
	v_fmac_f32_e32 v115, v122, v122
	v_add_f32_e32 v114, v115, v114
	v_mul_f32_e32 v115, v125, v125
	v_lshlrev_b32_e32 v130, 16, v150
	v_and_b32_e32 v131, 0xffff0000, v150
	v_lshlrev_b32_e32 v132, 16, v151
	v_and_b32_e32 v133, 0xffff0000, v151
	v_fmac_f32_e32 v115, v124, v124
	v_lshlrev_b32_e32 v150, 16, v152
	v_and_b32_e32 v151, 0xffff0000, v152
	v_cvt_pk_bf16_f32 v111, v116, v117
	v_add_f32_e32 v119, v115, v114
	v_pk_mul_f32 v[114:115], v[206:207], v[130:131] op_sel_hi:[0,1]
	v_pk_mul_f32 v[116:117], v[206:207], v[132:133] op_sel_hi:[0,1]
	v_pk_fma_f32 v[108:109], v[108:109], v[204:205], v[116:117] op_sel_hi:[1,0,1]
	v_pk_fma_f32 v[106:107], v[106:107], v[204:205], v[114:115] op_sel_hi:[1,0,1]
	v_pk_mul_f32 v[114:115], v[206:207], v[150:151] op_sel_hi:[0,1]
	v_pk_fma_f32 v[114:115], v[102:103], v[204:205], v[114:115] op_sel_hi:[1,0,1]
	v_mul_f32_e32 v102, v107, v107
	v_mul_f32_e32 v103, v109, v109
	v_lshlrev_b32_e32 v152, 16, v153
	v_and_b32_e32 v153, 0xffff0000, v153
	v_fmac_f32_e32 v102, v106, v106
	v_fmac_f32_e32 v103, v108, v108
	v_pk_mul_f32 v[116:117], v[206:207], v[152:153] op_sel_hi:[0,1]
	v_add_f32_e32 v102, v102, v103
	v_mul_f32_e32 v103, v115, v115
	v_pk_fma_f32 v[116:117], v[104:105], v[204:205], v[116:117] op_sel_hi:[1,0,1]
	v_fmac_f32_e32 v103, v114, v114
	v_add_f32_e32 v102, v103, v102
	v_mul_f32_e32 v103, v117, v117
	v_fmac_f32_e32 v103, v116, v116
	v_add_f32_e32 v102, v103, v102
	v_add_f32_e32 v105, v119, v102
	ds_bpermute_b32 v119, v3, v105
	s_waitcnt lgkmcnt(1)
	v_lshlrev_b64 v[120:121], 11, v[202:203]
	v_lshl_add_u64 v[102:103], v[120:121], 1, s[22:23]
	v_lshl_add_u64 v[120:121], v[4:5], 1, v[102:103]
	v_cvt_pk_bf16_f32 v112, v122, v123
	s_waitcnt lgkmcnt(0)
	v_add_f32_e32 v102, v105, v119
	ds_bpermute_b32 v103, v118, v102
	v_cvt_pk_bf16_f32 v113, v124, v125
	global_store_dwordx4 v[120:121], v[110:113], off sc1
	v_cvt_pk_bf16_f32 v104, v106, v107
	v_cvt_pk_bf16_f32 v105, v108, v109
	v_cvt_pk_bf16_f32 v106, v114, v115
	v_cvt_pk_bf16_f32 v107, v116, v117
	global_store_dwordx4 v[120:121], v[104:107], off offset:256 sc1
	s_and_saveexec_b64 s[54:55], s[8:9]
	s_cbranch_execz .LBB0_720
	s_waitcnt lgkmcnt(0)
	v_add_f32_e32 v104, v102, v103
	s_lshl_b32 s56, s14, 2
	v_lshlrev_b64 v[102:103], 7, v[202:203]
	s_ashr_i32 s57, s56, 31
	v_lshl_add_u64 v[102:103], s[24:25], 0, v[102:103]
	v_lshl_add_u64 v[102:103], s[56:57], 2, v[102:103]
	s_lshl_b32 s16, s50, 2
	v_lshl_add_u64 v[102:103], v[102:103], 0, s[16:17]
	global_store_dword v[102:103], v104, off
.LBB0_720:
	s_or_b64 exec, exec, s[54:55]
	v_lshlrev_b32_e32 v104, 16, v146
	v_and_b32_e32 v105, 0xffff0000, v146
	v_lshlrev_b32_e32 v106, 16, v147
	v_and_b32_e32 v107, 0xffff0000, v147
	v_lshlrev_b32_e32 v108, 16, v148
	v_and_b32_e32 v109, 0xffff0000, v148
	v_pk_mul_f32 v[104:105], v[200:201], v[104:105] op_sel_hi:[0,1]
	v_pk_mul_f32 v[106:107], v[200:201], v[106:107] op_sel_hi:[0,1]
	v_pk_fma_f32 v[98:99], v[98:99], v[196:197], v[104:105] op_sel_hi:[1,0,1]
	v_pk_mul_f32 v[104:105], v[200:201], v[108:109] op_sel_hi:[0,1]
	v_pk_fma_f32 v[100:101], v[100:101], v[196:197], v[106:107] op_sel_hi:[1,0,1]
	v_pk_fma_f32 v[104:105], v[94:95], v[196:197], v[104:105] op_sel_hi:[1,0,1]
	v_cvt_pk_bf16_f32 v94, v98, v99
	v_mul_f32_e32 v99, v99, v99
	v_fmac_f32_e32 v99, v98, v98
	v_mul_f32_e32 v98, v101, v101
	v_lshlrev_b32_e32 v110, 16, v149
	v_and_b32_e32 v111, 0xffff0000, v149
	v_fmac_f32_e32 v98, v100, v100
	v_pk_mul_f32 v[106:107], v[200:201], v[110:111] op_sel_hi:[0,1]
	v_add_f32_e32 v98, v99, v98
	v_mul_f32_e32 v99, v105, v105
	v_pk_fma_f32 v[106:107], v[96:97], v[196:197], v[106:107] op_sel_hi:[1,0,1]
	v_fmac_f32_e32 v99, v104, v104
	v_add_f32_e32 v98, v99, v98
	v_mul_f32_e32 v99, v107, v107
	v_lshlrev_b32_e32 v112, 16, v142
	v_and_b32_e32 v113, 0xffff0000, v142
	v_lshlrev_b32_e32 v114, 16, v143
	v_and_b32_e32 v115, 0xffff0000, v143
	v_fmac_f32_e32 v99, v106, v106
	v_lshlrev_b32_e32 v116, 16, v144
	v_and_b32_e32 v117, 0xffff0000, v144
	v_cvt_pk_bf16_f32 v95, v100, v101
	v_cvt_pk_bf16_f32 v96, v104, v105
	v_add_f32_e32 v104, v99, v98
	v_pk_mul_f32 v[98:99], v[200:201], v[112:113] op_sel_hi:[0,1]
	v_pk_mul_f32 v[100:101], v[200:201], v[114:115] op_sel_hi:[0,1]
	v_pk_fma_f32 v[92:93], v[92:93], v[196:197], v[100:101] op_sel_hi:[1,0,1]
	v_pk_fma_f32 v[90:91], v[90:91], v[196:197], v[98:99] op_sel_hi:[1,0,1]
	v_pk_mul_f32 v[98:99], v[200:201], v[116:117] op_sel_hi:[0,1]
	v_pk_fma_f32 v[98:99], v[86:87], v[196:197], v[98:99] op_sel_hi:[1,0,1]
	v_mul_f32_e32 v86, v91, v91
	v_mul_f32_e32 v87, v93, v93
	v_lshlrev_b32_e32 v120, 16, v145
	v_and_b32_e32 v121, 0xffff0000, v145
	v_fmac_f32_e32 v86, v90, v90
	v_fmac_f32_e32 v87, v92, v92
	v_pk_mul_f32 v[100:101], v[200:201], v[120:121] op_sel_hi:[0,1]
	v_add_f32_e32 v86, v86, v87
	v_mul_f32_e32 v87, v99, v99
	v_pk_fma_f32 v[100:101], v[88:89], v[196:197], v[100:101] op_sel_hi:[1,0,1]
	v_fmac_f32_e32 v87, v98, v98
	v_add_f32_e32 v86, v87, v86
	v_mul_f32_e32 v87, v101, v101
	v_fmac_f32_e32 v87, v100, v100
	v_add_f32_e32 v86, v87, v86
	v_add_f32_e32 v89, v104, v86
	ds_bpermute_b32 v104, v3, v89
	s_waitcnt lgkmcnt(1)
	v_lshlrev_b64 v[102:103], 11, v[198:199]
	v_lshl_add_u64 v[86:87], v[102:103], 1, s[22:23]
	v_lshl_add_u64 v[102:103], v[4:5], 1, v[86:87]
	v_cvt_pk_bf16_f32 v97, v106, v107
	s_waitcnt lgkmcnt(0)
	v_add_f32_e32 v86, v89, v104
	ds_bpermute_b32 v87, v118, v86
	global_store_dwordx4 v[102:103], v[94:97], off sc1
	v_cvt_pk_bf16_f32 v88, v90, v91
	v_cvt_pk_bf16_f32 v89, v92, v93
	v_cvt_pk_bf16_f32 v90, v98, v99
	v_cvt_pk_bf16_f32 v91, v100, v101
	global_store_dwordx4 v[102:103], v[88:91], off offset:256 sc1
	s_and_saveexec_b64 s[54:55], s[8:9]
	s_cbranch_execz .LBB0_722
	s_waitcnt lgkmcnt(0)
	v_add_f32_e32 v88, v86, v87
	s_lshl_b32 s56, s14, 2
	v_lshlrev_b64 v[86:87], 7, v[198:199]
	s_ashr_i32 s57, s56, 31
	v_lshl_add_u64 v[86:87], s[24:25], 0, v[86:87]
	v_lshl_add_u64 v[86:87], s[56:57], 2, v[86:87]
	s_lshl_b32 s16, s50, 2
	v_lshl_add_u64 v[86:87], v[86:87], 0, s[16:17]
	global_store_dword v[86:87], v88, off
.LBB0_722:
	s_or_b64 exec, exec, s[54:55]
	v_lshlrev_b32_e32 v88, 16, v138
	v_and_b32_e32 v89, 0xffff0000, v138
	v_lshlrev_b32_e32 v90, 16, v139
	v_and_b32_e32 v91, 0xffff0000, v139
	v_lshlrev_b32_e32 v92, 16, v140
	v_and_b32_e32 v93, 0xffff0000, v140
	v_pk_mul_f32 v[88:89], v[194:195], v[88:89] op_sel_hi:[0,1]
	v_pk_mul_f32 v[90:91], v[194:195], v[90:91] op_sel_hi:[0,1]
	v_pk_fma_f32 v[82:83], v[82:83], v[190:191], v[88:89] op_sel_hi:[1,0,1]
	v_pk_mul_f32 v[88:89], v[194:195], v[92:93] op_sel_hi:[0,1]
	v_pk_fma_f32 v[84:85], v[84:85], v[190:191], v[90:91] op_sel_hi:[1,0,1]
	v_pk_fma_f32 v[88:89], v[78:79], v[190:191], v[88:89] op_sel_hi:[1,0,1]
	v_cvt_pk_bf16_f32 v78, v82, v83
	v_mul_f32_e32 v83, v83, v83
	v_fmac_f32_e32 v83, v82, v82
	v_mul_f32_e32 v82, v85, v85
	v_lshlrev_b32_e32 v94, 16, v141
	v_and_b32_e32 v95, 0xffff0000, v141
	v_fmac_f32_e32 v82, v84, v84
	v_pk_mul_f32 v[90:91], v[194:195], v[94:95] op_sel_hi:[0,1]
	v_add_f32_e32 v82, v83, v82
	v_mul_f32_e32 v83, v89, v89
	v_pk_fma_f32 v[90:91], v[80:81], v[190:191], v[90:91] op_sel_hi:[1,0,1]
	v_fmac_f32_e32 v83, v88, v88
	v_add_f32_e32 v82, v83, v82
	v_mul_f32_e32 v83, v91, v91
	v_lshlrev_b32_e32 v96, 16, v134
	v_and_b32_e32 v97, 0xffff0000, v134
	v_lshlrev_b32_e32 v98, 16, v135
	v_and_b32_e32 v99, 0xffff0000, v135
	v_fmac_f32_e32 v83, v90, v90
	v_lshlrev_b32_e32 v100, 16, v136
	v_and_b32_e32 v101, 0xffff0000, v136
	v_cvt_pk_bf16_f32 v79, v84, v85
	v_cvt_pk_bf16_f32 v80, v88, v89
	v_add_f32_e32 v88, v83, v82
	v_pk_mul_f32 v[82:83], v[194:195], v[96:97] op_sel_hi:[0,1]
	v_pk_mul_f32 v[84:85], v[194:195], v[98:99] op_sel_hi:[0,1]
	v_pk_fma_f32 v[76:77], v[76:77], v[190:191], v[84:85] op_sel_hi:[1,0,1]
	v_pk_fma_f32 v[74:75], v[74:75], v[190:191], v[82:83] op_sel_hi:[1,0,1]
	v_pk_mul_f32 v[82:83], v[194:195], v[100:101] op_sel_hi:[0,1]
	v_pk_fma_f32 v[82:83], v[70:71], v[190:191], v[82:83] op_sel_hi:[1,0,1]
	v_mul_f32_e32 v70, v75, v75
	v_mul_f32_e32 v71, v77, v77
	v_lshlrev_b32_e32 v102, 16, v137
	v_and_b32_e32 v103, 0xffff0000, v137
	v_fmac_f32_e32 v70, v74, v74
	v_fmac_f32_e32 v71, v76, v76
	v_pk_mul_f32 v[84:85], v[194:195], v[102:103] op_sel_hi:[0,1]
	v_add_f32_e32 v70, v70, v71
	v_mul_f32_e32 v71, v83, v83
	v_pk_fma_f32 v[84:85], v[72:73], v[190:191], v[84:85] op_sel_hi:[1,0,1]
	v_fmac_f32_e32 v71, v82, v82
	v_add_f32_e32 v70, v71, v70
	v_mul_f32_e32 v71, v85, v85
	v_fmac_f32_e32 v71, v84, v84
	v_add_f32_e32 v70, v71, v70
	v_add_f32_e32 v73, v88, v70
	ds_bpermute_b32 v88, v3, v73
	s_waitcnt lgkmcnt(1)
	v_lshlrev_b64 v[86:87], 11, v[192:193]
	v_lshl_add_u64 v[70:71], v[86:87], 1, s[22:23]
	v_lshl_add_u64 v[86:87], v[4:5], 1, v[70:71]
	v_cvt_pk_bf16_f32 v81, v90, v91
	s_waitcnt lgkmcnt(0)
	v_add_f32_e32 v70, v73, v88
	ds_bpermute_b32 v71, v118, v70
	global_store_dwordx4 v[86:87], v[78:81], off sc1
	v_cvt_pk_bf16_f32 v72, v74, v75
	v_cvt_pk_bf16_f32 v73, v76, v77
	v_cvt_pk_bf16_f32 v74, v82, v83
	v_cvt_pk_bf16_f32 v75, v84, v85
	global_store_dwordx4 v[86:87], v[72:75], off offset:256 sc1
	s_and_saveexec_b64 s[54:55], s[8:9]
	s_cbranch_execz .LBB0_724
	s_waitcnt lgkmcnt(0)
	v_add_f32_e32 v72, v70, v71
	s_lshl_b32 s56, s14, 2
	v_lshlrev_b64 v[70:71], 7, v[192:193]
	s_ashr_i32 s57, s56, 31
	v_lshl_add_u64 v[70:71], s[24:25], 0, v[70:71]
	v_lshl_add_u64 v[70:71], s[56:57], 2, v[70:71]
	s_lshl_b32 s16, s50, 2
	v_lshl_add_u64 v[70:71], v[70:71], 0, s[16:17]
	global_store_dword v[70:71], v72, off
.LBB0_724:
	s_or_b64 exec, exec, s[54:55]
	v_add_u32_e32 v106, 0x80, v186
	v_ashrrev_i32_e32 v107, 31, v106
	v_lshlrev_b64 v[116:117], 12, v[106:107]
	s_waitcnt lgkmcnt(0)
	v_lshl_add_u64 v[70:71], v[184:185], 0, v[116:117]
	global_load_dwordx4 v[108:111], v[70:71], off
	global_load_dwordx4 v[112:115], v[70:71], off offset:256
	global_load_dword v120, v[188:189], off offset:512
	v_add_u32_e32 v102, 0x90, v186
	v_add_u32_e32 v98, 0xa0, v186
	v_add_u32_e32 v94, 0xb0, v186
	v_ashrrev_i32_e32 v103, 31, v102
	v_ashrrev_i32_e32 v99, 31, v98
	v_ashrrev_i32_e32 v95, 31, v94
	v_lshlrev_b64 v[70:71], 12, v[102:103]
	v_lshlrev_b64 v[72:73], 12, v[98:99]
	v_lshlrev_b64 v[74:75], 12, v[94:95]
	v_lshl_add_u64 v[70:71], v[184:185], 0, v[70:71]
	v_lshl_add_u64 v[72:73], v[184:185], 0, v[72:73]
	global_load_dword v104, v[188:189], off offset:576
	global_load_dword v100, v[188:189], off offset:640
	global_load_dword v96, v[188:189], off offset:704
	v_lshl_add_u64 v[122:123], v[184:185], 0, v[74:75]
	global_load_dwordx4 v[90:93], v[70:71], off
	global_load_dwordx4 v[86:89], v[70:71], off offset:256
	global_load_dwordx4 v[82:85], v[72:73], off
	global_load_dwordx4 v[78:81], v[72:73], off offset:256
	global_load_dwordx4 v[74:77], v[122:123], off
	s_nop 0
	global_load_dwordx4 v[70:73], v[122:123], off offset:256
	s_waitcnt vmcnt(11)
	v_lshlrev_b32_e32 v122, 16, v108
	v_and_b32_e32 v123, 0xffff0000, v108
	v_lshlrev_b32_e32 v108, 16, v109
	v_and_b32_e32 v109, 0xffff0000, v109
	s_waitcnt vmcnt(10)
	v_lshlrev_b32_e32 v126, 16, v112
	v_and_b32_e32 v127, 0xffff0000, v112
	v_lshlrev_b32_e32 v112, 16, v113
	v_and_b32_e32 v113, 0xffff0000, v113
	v_lshlrev_b32_e32 v124, 16, v110
	v_and_b32_e32 v125, 0xffff0000, v110
	v_lshlrev_b32_e32 v110, 16, v111
	v_and_b32_e32 v111, 0xffff0000, v111
	v_lshlrev_b32_e32 v128, 16, v114
	v_and_b32_e32 v129, 0xffff0000, v114
	s_waitcnt vmcnt(9)
	v_pk_mul_f32 v[122:123], v[120:121], v[122:123] op_sel_hi:[0,1]
	v_pk_mul_f32 v[108:109], v[120:121], v[108:109] op_sel_hi:[0,1]
	v_pk_mul_f32 v[126:127], v[120:121], v[126:127] op_sel_hi:[0,1]
	v_pk_mul_f32 v[112:113], v[120:121], v[112:113] op_sel_hi:[0,1]
	v_lshlrev_b32_e32 v114, 16, v115
	v_and_b32_e32 v115, 0xffff0000, v115
	v_pk_mul_f32 v[124:125], v[120:121], v[124:125] op_sel_hi:[0,1]
	v_pk_mul_f32 v[110:111], v[120:121], v[110:111] op_sel_hi:[0,1]
	v_pk_mul_f32 v[128:129], v[120:121], v[128:129] op_sel_hi:[0,1]
	v_pk_fma_f32 v[68:69], v[68:69], v[182:183], v[108:109] op_sel_hi:[1,0,1]
	v_pk_fma_f32 v[66:67], v[66:67], v[182:183], v[122:123] op_sel_hi:[1,0,1]
	v_pk_fma_f32 v[60:61], v[60:61], v[182:183], v[112:113] op_sel_hi:[1,0,1]
	v_pk_fma_f32 v[58:59], v[58:59], v[182:183], v[126:127] op_sel_hi:[1,0,1]
	v_pk_mul_f32 v[114:115], v[120:121], v[114:115] op_sel_hi:[0,1]
	v_pk_fma_f32 v[64:65], v[64:65], v[182:183], v[110:111] op_sel_hi:[1,0,1]
	v_pk_fma_f32 v[62:63], v[62:63], v[182:183], v[124:125] op_sel_hi:[1,0,1]
	v_pk_fma_f32 v[110:111], v[54:55], v[182:183], v[128:129] op_sel_hi:[1,0,1]
	v_cvt_pk_bf16_f32 v54, v66, v67
	v_cvt_pk_bf16_f32 v55, v68, v69
	v_mul_f32_e32 v67, v67, v67
	v_mul_f32_e32 v69, v69, v69
	v_mul_f32_e32 v97, v59, v59
	v_mul_f32_e32 v101, v61, v61
	v_pk_fma_f32 v[108:109], v[56:57], v[182:183], v[114:115] op_sel_hi:[1,0,1]
	v_cvt_pk_bf16_f32 v56, v62, v63
	v_cvt_pk_bf16_f32 v57, v64, v65
	v_mul_f32_e32 v63, v63, v63
	v_mul_f32_e32 v65, v65, v65
	v_mul_f32_e32 v105, v111, v111
	v_fmac_f32_e32 v67, v66, v66
	v_fmac_f32_e32 v69, v68, v68
	v_fmac_f32_e32 v97, v58, v58
	v_fmac_f32_e32 v101, v60, v60
	v_mul_f32_e32 v112, v109, v109
	v_fmac_f32_e32 v63, v62, v62
	v_fmac_f32_e32 v65, v64, v64
	v_fmac_f32_e32 v105, v110, v110
	v_add_f32_e32 v62, v67, v69
	v_add_f32_e32 v64, v97, v101
	v_fmac_f32_e32 v112, v108, v108
	v_add_f32_e32 v62, v63, v62
	v_add_f32_e32 v63, v105, v64
	v_add_f32_e32 v62, v65, v62
	v_add_f32_e32 v63, v112, v63
	v_add_f32_e32 v64, v62, v63
	ds_bpermute_b32 v65, v3, v64
	v_lshl_add_u64 v[62:63], s[22:23], 0, v[116:117]
	v_lshl_add_u64 v[62:63], v[4:5], 1, v[62:63]
	global_store_dwordx4 v[62:63], v[54:57], off sc1
	s_waitcnt lgkmcnt(0)
	s_nop 0
	v_add_f32_e32 v54, v64, v65
	ds_bpermute_b32 v55, v118, v54
	v_cvt_pk_bf16_f32 v56, v58, v59
	v_cvt_pk_bf16_f32 v57, v60, v61
	v_cvt_pk_bf16_f32 v58, v110, v111
	v_cvt_pk_bf16_f32 v59, v108, v109
	global_store_dwordx4 v[62:63], v[56:59], off offset:256 sc1
	s_and_saveexec_b64 s[54:55], s[8:9]
	s_cbranch_execz .LBB0_726
	s_waitcnt lgkmcnt(0)
	v_add_f32_e32 v56, v54, v55
	s_lshl_b32 s56, s14, 2
	v_lshlrev_b64 v[54:55], 7, v[106:107]
	s_ashr_i32 s57, s56, 31
	v_lshl_add_u64 v[54:55], s[24:25], 0, v[54:55]
	v_lshl_add_u64 v[54:55], s[56:57], 2, v[54:55]
	s_lshl_b32 s16, s50, 2
	v_lshl_add_u64 v[54:55], v[54:55], 0, s[16:17]
	global_store_dword v[54:55], v56, off
.LBB0_726:
	s_or_b64 exec, exec, s[54:55]
	s_waitcnt vmcnt(7)
	v_lshlrev_b32_e32 v56, 16, v90
	v_and_b32_e32 v57, 0xffff0000, v90
	v_lshlrev_b32_e32 v58, 16, v91
	v_and_b32_e32 v59, 0xffff0000, v91
	v_lshlrev_b32_e32 v60, 16, v92
	v_and_b32_e32 v61, 0xffff0000, v92
	v_pk_mul_f32 v[56:57], v[104:105], v[56:57] op_sel_hi:[0,1]
	v_pk_mul_f32 v[58:59], v[104:105], v[58:59] op_sel_hi:[0,1]
	v_pk_fma_f32 v[50:51], v[50:51], v[180:181], v[56:57] op_sel_hi:[1,0,1]
	v_pk_mul_f32 v[56:57], v[104:105], v[60:61] op_sel_hi:[0,1]
	v_pk_fma_f32 v[52:53], v[52:53], v[180:181], v[58:59] op_sel_hi:[1,0,1]
	v_pk_fma_f32 v[56:57], v[46:47], v[180:181], v[56:57] op_sel_hi:[1,0,1]
	v_cvt_pk_bf16_f32 v46, v50, v51
	v_mul_f32_e32 v51, v51, v51
	v_fmac_f32_e32 v51, v50, v50
	v_mul_f32_e32 v50, v53, v53
	v_lshlrev_b32_e32 v62, 16, v93
	v_and_b32_e32 v63, 0xffff0000, v93
	v_fmac_f32_e32 v50, v52, v52
	v_pk_mul_f32 v[58:59], v[104:105], v[62:63] op_sel_hi:[0,1]
	v_add_f32_e32 v50, v51, v50
	v_mul_f32_e32 v51, v57, v57
	v_pk_fma_f32 v[58:59], v[48:49], v[180:181], v[58:59] op_sel_hi:[1,0,1]
	v_fmac_f32_e32 v51, v56, v56
	v_add_f32_e32 v50, v51, v50
	v_mul_f32_e32 v51, v59, v59
	s_waitcnt vmcnt(6)
	v_lshlrev_b32_e32 v64, 16, v86
	v_and_b32_e32 v65, 0xffff0000, v86
	v_lshlrev_b32_e32 v66, 16, v87
	v_and_b32_e32 v67, 0xffff0000, v87
	v_fmac_f32_e32 v51, v58, v58
	v_lshlrev_b32_e32 v68, 16, v88
	v_and_b32_e32 v69, 0xffff0000, v88
	v_cvt_pk_bf16_f32 v47, v52, v53
	v_cvt_pk_bf16_f32 v48, v56, v57
	v_add_f32_e32 v56, v51, v50
	v_pk_mul_f32 v[50:51], v[104:105], v[64:65] op_sel_hi:[0,1]
	v_pk_mul_f32 v[52:53], v[104:105], v[66:67] op_sel_hi:[0,1]
	v_pk_fma_f32 v[44:45], v[44:45], v[180:181], v[52:53] op_sel_hi:[1,0,1]
	v_pk_fma_f32 v[42:43], v[42:43], v[180:181], v[50:51] op_sel_hi:[1,0,1]
	v_pk_mul_f32 v[50:51], v[104:105], v[68:69] op_sel_hi:[0,1]
	v_pk_fma_f32 v[50:51], v[38:39], v[180:181], v[50:51] op_sel_hi:[1,0,1]
	v_mul_f32_e32 v38, v43, v43
	v_mul_f32_e32 v39, v45, v45
	v_lshlrev_b32_e32 v86, 16, v89
	v_and_b32_e32 v87, 0xffff0000, v89
	v_fmac_f32_e32 v38, v42, v42
	v_fmac_f32_e32 v39, v44, v44
	v_pk_mul_f32 v[52:53], v[104:105], v[86:87] op_sel_hi:[0,1]
	v_add_f32_e32 v38, v38, v39
	v_mul_f32_e32 v39, v51, v51
	v_pk_fma_f32 v[52:53], v[40:41], v[180:181], v[52:53] op_sel_hi:[1,0,1]
	v_fmac_f32_e32 v39, v50, v50
	v_add_f32_e32 v38, v39, v38
	v_mul_f32_e32 v39, v53, v53
	v_fmac_f32_e32 v39, v52, v52
	v_add_f32_e32 v38, v39, v38
	v_add_f32_e32 v41, v56, v38
	ds_bpermute_b32 v56, v3, v41
	s_waitcnt lgkmcnt(1)
	v_lshlrev_b64 v[54:55], 11, v[102:103]
	v_lshl_add_u64 v[38:39], v[54:55], 1, s[22:23]
	v_lshl_add_u64 v[54:55], v[4:5], 1, v[38:39]
	v_cvt_pk_bf16_f32 v49, v58, v59
	s_waitcnt lgkmcnt(0)
	v_add_f32_e32 v38, v41, v56
	ds_bpermute_b32 v39, v118, v38
	global_store_dwordx4 v[54:55], v[46:49], off sc1
	v_cvt_pk_bf16_f32 v40, v42, v43
	v_cvt_pk_bf16_f32 v41, v44, v45
	v_cvt_pk_bf16_f32 v42, v50, v51
	v_cvt_pk_bf16_f32 v43, v52, v53
	global_store_dwordx4 v[54:55], v[40:43], off offset:256 sc1
	s_and_saveexec_b64 s[54:55], s[8:9]
	s_cbranch_execz .LBB0_728
	s_waitcnt lgkmcnt(0)
	v_add_f32_e32 v40, v38, v39
	s_lshl_b32 s56, s14, 2
	v_lshlrev_b64 v[38:39], 7, v[102:103]
	s_ashr_i32 s57, s56, 31
	v_lshl_add_u64 v[38:39], s[24:25], 0, v[38:39]
	v_lshl_add_u64 v[38:39], s[56:57], 2, v[38:39]
	s_lshl_b32 s16, s50, 2
	v_lshl_add_u64 v[38:39], v[38:39], 0, s[16:17]
	global_store_dword v[38:39], v40, off
.LBB0_728:
	s_or_b64 exec, exec, s[54:55]
	s_waitcnt vmcnt(7)
	v_lshlrev_b32_e32 v40, 16, v82
	v_and_b32_e32 v41, 0xffff0000, v82
	v_lshlrev_b32_e32 v42, 16, v83
	v_and_b32_e32 v43, 0xffff0000, v83
	v_lshlrev_b32_e32 v44, 16, v84
	v_and_b32_e32 v45, 0xffff0000, v84
	v_pk_mul_f32 v[40:41], v[100:101], v[40:41] op_sel_hi:[0,1]
	v_pk_mul_f32 v[42:43], v[100:101], v[42:43] op_sel_hi:[0,1]
	v_pk_fma_f32 v[34:35], v[34:35], v[178:179], v[40:41] op_sel_hi:[1,0,1]
	v_pk_mul_f32 v[40:41], v[100:101], v[44:45] op_sel_hi:[0,1]
	v_pk_fma_f32 v[36:37], v[36:37], v[178:179], v[42:43] op_sel_hi:[1,0,1]
	v_pk_fma_f32 v[40:41], v[30:31], v[178:179], v[40:41] op_sel_hi:[1,0,1]
	v_cvt_pk_bf16_f32 v30, v34, v35
	v_mul_f32_e32 v35, v35, v35
	v_fmac_f32_e32 v35, v34, v34
	v_mul_f32_e32 v34, v37, v37
	v_lshlrev_b32_e32 v46, 16, v85
	v_and_b32_e32 v47, 0xffff0000, v85
	v_fmac_f32_e32 v34, v36, v36
	v_pk_mul_f32 v[42:43], v[100:101], v[46:47] op_sel_hi:[0,1]
	v_add_f32_e32 v34, v35, v34
	v_mul_f32_e32 v35, v41, v41
	v_pk_fma_f32 v[42:43], v[32:33], v[178:179], v[42:43] op_sel_hi:[1,0,1]
	v_fmac_f32_e32 v35, v40, v40
	v_add_f32_e32 v34, v35, v34
	v_mul_f32_e32 v35, v43, v43
	s_waitcnt vmcnt(6)
	v_lshlrev_b32_e32 v48, 16, v78
	v_and_b32_e32 v49, 0xffff0000, v78
	v_lshlrev_b32_e32 v50, 16, v79
	v_and_b32_e32 v51, 0xffff0000, v79
	v_fmac_f32_e32 v35, v42, v42
	v_lshlrev_b32_e32 v52, 16, v80
	v_and_b32_e32 v53, 0xffff0000, v80
	v_cvt_pk_bf16_f32 v31, v36, v37
	v_cvt_pk_bf16_f32 v32, v40, v41
	v_add_f32_e32 v40, v35, v34
	v_pk_mul_f32 v[34:35], v[100:101], v[48:49] op_sel_hi:[0,1]
	v_pk_mul_f32 v[36:37], v[100:101], v[50:51] op_sel_hi:[0,1]
	v_pk_fma_f32 v[28:29], v[28:29], v[178:179], v[36:37] op_sel_hi:[1,0,1]
	v_pk_fma_f32 v[26:27], v[26:27], v[178:179], v[34:35] op_sel_hi:[1,0,1]
	v_pk_mul_f32 v[34:35], v[100:101], v[52:53] op_sel_hi:[0,1]
	v_pk_fma_f32 v[34:35], v[22:23], v[178:179], v[34:35] op_sel_hi:[1,0,1]
	v_mul_f32_e32 v22, v27, v27
	v_mul_f32_e32 v23, v29, v29
	v_lshlrev_b32_e32 v54, 16, v81
	v_and_b32_e32 v55, 0xffff0000, v81
	v_fmac_f32_e32 v22, v26, v26
	v_fmac_f32_e32 v23, v28, v28
	v_pk_mul_f32 v[36:37], v[100:101], v[54:55] op_sel_hi:[0,1]
	v_add_f32_e32 v22, v22, v23
	v_mul_f32_e32 v23, v35, v35
	v_pk_fma_f32 v[36:37], v[24:25], v[178:179], v[36:37] op_sel_hi:[1,0,1]
	v_fmac_f32_e32 v23, v34, v34
	v_add_f32_e32 v22, v23, v22
	v_mul_f32_e32 v23, v37, v37
	v_fmac_f32_e32 v23, v36, v36
	v_add_f32_e32 v22, v23, v22
	v_add_f32_e32 v25, v40, v22
	ds_bpermute_b32 v40, v3, v25
	s_waitcnt lgkmcnt(1)
	v_lshlrev_b64 v[38:39], 11, v[98:99]
	v_lshl_add_u64 v[22:23], v[38:39], 1, s[22:23]
	v_lshl_add_u64 v[38:39], v[4:5], 1, v[22:23]
	v_cvt_pk_bf16_f32 v33, v42, v43
	s_waitcnt lgkmcnt(0)
	v_add_f32_e32 v22, v25, v40
	ds_bpermute_b32 v23, v118, v22
	global_store_dwordx4 v[38:39], v[30:33], off sc1
	v_cvt_pk_bf16_f32 v24, v26, v27
	v_cvt_pk_bf16_f32 v25, v28, v29
	v_cvt_pk_bf16_f32 v26, v34, v35
	v_cvt_pk_bf16_f32 v27, v36, v37
	global_store_dwordx4 v[38:39], v[24:27], off offset:256 sc1
	s_and_saveexec_b64 s[54:55], s[8:9]
	s_cbranch_execz .LBB0_730
	s_waitcnt lgkmcnt(0)
	v_add_f32_e32 v24, v22, v23
	s_lshl_b32 s56, s14, 2
	v_lshlrev_b64 v[22:23], 7, v[98:99]
	s_ashr_i32 s57, s56, 31
	v_lshl_add_u64 v[22:23], s[24:25], 0, v[22:23]
	v_lshl_add_u64 v[22:23], s[56:57], 2, v[22:23]
	s_lshl_b32 s16, s50, 2
	v_lshl_add_u64 v[22:23], v[22:23], 0, s[16:17]
	global_store_dword v[22:23], v24, off
.LBB0_730:
	s_or_b64 exec, exec, s[54:55]
	s_waitcnt vmcnt(7)
	v_lshlrev_b32_e32 v24, 16, v74
	v_and_b32_e32 v25, 0xffff0000, v74
	v_lshlrev_b32_e32 v26, 16, v75
	v_and_b32_e32 v27, 0xffff0000, v75
	v_lshlrev_b32_e32 v28, 16, v76
	v_and_b32_e32 v29, 0xffff0000, v76
	v_pk_mul_f32 v[24:25], v[96:97], v[24:25] op_sel_hi:[0,1]
	v_pk_mul_f32 v[26:27], v[96:97], v[26:27] op_sel_hi:[0,1]
	v_pk_fma_f32 v[18:19], v[18:19], v[176:177], v[24:25] op_sel_hi:[1,0,1]
	v_pk_mul_f32 v[24:25], v[96:97], v[28:29] op_sel_hi:[0,1]
	v_pk_fma_f32 v[20:21], v[20:21], v[176:177], v[26:27] op_sel_hi:[1,0,1]
	v_pk_fma_f32 v[24:25], v[14:15], v[176:177], v[24:25] op_sel_hi:[1,0,1]
	v_cvt_pk_bf16_f32 v14, v18, v19
	v_mul_f32_e32 v19, v19, v19
	v_fmac_f32_e32 v19, v18, v18
	v_mul_f32_e32 v18, v21, v21
	v_lshlrev_b32_e32 v30, 16, v77
	v_and_b32_e32 v31, 0xffff0000, v77
	v_fmac_f32_e32 v18, v20, v20
	v_pk_mul_f32 v[26:27], v[96:97], v[30:31] op_sel_hi:[0,1]
	v_add_f32_e32 v18, v19, v18
	v_mul_f32_e32 v19, v25, v25
	v_pk_fma_f32 v[26:27], v[16:17], v[176:177], v[26:27] op_sel_hi:[1,0,1]
	v_fmac_f32_e32 v19, v24, v24
	v_add_f32_e32 v18, v19, v18
	v_mul_f32_e32 v19, v27, v27
	s_waitcnt vmcnt(6)
	v_lshlrev_b32_e32 v32, 16, v70
	v_and_b32_e32 v33, 0xffff0000, v70
	v_lshlrev_b32_e32 v34, 16, v71
	v_and_b32_e32 v35, 0xffff0000, v71
	v_fmac_f32_e32 v19, v26, v26
	v_lshlrev_b32_e32 v36, 16, v72
	v_and_b32_e32 v37, 0xffff0000, v72
	v_lshlrev_b32_e32 v38, 16, v73
	v_and_b32_e32 v39, 0xffff0000, v73
	v_cvt_pk_bf16_f32 v15, v20, v21
	v_cvt_pk_bf16_f32 v16, v24, v25
	v_add_f32_e32 v24, v19, v18
	v_pk_mul_f32 v[18:19], v[96:97], v[32:33] op_sel_hi:[0,1]
	v_pk_mul_f32 v[20:21], v[96:97], v[34:35] op_sel_hi:[0,1]
	v_pk_fma_f32 v[12:13], v[12:13], v[176:177], v[20:21] op_sel_hi:[1,0,1]
	v_pk_fma_f32 v[10:11], v[10:11], v[176:177], v[18:19] op_sel_hi:[1,0,1]
	v_pk_mul_f32 v[18:19], v[96:97], v[36:37] op_sel_hi:[0,1]
	v_pk_mul_f32 v[20:21], v[96:97], v[38:39] op_sel_hi:[0,1]
	v_pk_fma_f32 v[20:21], v[8:9], v[176:177], v[20:21] op_sel_hi:[1,0,1]
	v_pk_fma_f32 v[8:9], v[6:7], v[176:177], v[18:19] op_sel_hi:[1,0,1]
	v_mul_f32_e32 v6, v11, v11
	v_mul_f32_e32 v7, v13, v13
	v_fmac_f32_e32 v6, v10, v10
	v_fmac_f32_e32 v7, v12, v12
	v_add_f32_e32 v6, v6, v7
	v_mul_f32_e32 v7, v9, v9
	v_fmac_f32_e32 v7, v8, v8
	v_add_f32_e32 v6, v7, v6
	v_mul_f32_e32 v7, v21, v21
	v_fmac_f32_e32 v7, v20, v20
	v_add_f32_e32 v6, v7, v6
	v_add_f32_e32 v24, v24, v6
	ds_bpermute_b32 v3, v3, v24
	s_waitcnt lgkmcnt(1)
	v_lshlrev_b64 v[22:23], 11, v[94:95]
	v_lshl_add_u64 v[6:7], v[22:23], 1, s[22:23]
	v_lshl_add_u64 v[18:19], v[4:5], 1, v[6:7]
	v_cvt_pk_bf16_f32 v17, v26, v27
	s_waitcnt lgkmcnt(0)
	v_add_f32_e32 v3, v24, v3
	ds_bpermute_b32 v4, v118, v3
	global_store_dwordx4 v[18:19], v[14:17], off sc1
	v_cvt_pk_bf16_f32 v6, v10, v11
	v_cvt_pk_bf16_f32 v7, v12, v13
	v_cvt_pk_bf16_f32 v8, v8, v9
	v_cvt_pk_bf16_f32 v9, v20, v21
	global_store_dwordx4 v[18:19], v[6:9], off offset:256 sc1
	s_and_saveexec_b64 s[54:55], s[8:9]
	s_cbranch_execz .LBB0_732
	s_waitcnt lgkmcnt(0)
	v_add_f32_e32 v3, v3, v4
	s_lshl_b32 s56, s14, 2
	v_lshlrev_b64 v[4:5], 7, v[94:95]
	s_ashr_i32 s57, s56, 31
	v_lshl_add_u64 v[4:5], s[24:25], 0, v[4:5]
	v_lshl_add_u64 v[4:5], s[56:57], 2, v[4:5]
	s_lshl_b32 s16, s50, 2
	v_lshl_add_u64 v[4:5], v[4:5], 0, s[16:17]
	global_store_dword v[4:5], v3, off

.LBB0_812:
	s_mov_b64 s[56:57], s[38:39]
	s_add_u32 s74, s71, s56
	s_addc_u32 s75, s72, s57
	s_add_u32 s38, s56, 0x100
	s_addc_u32 s39, s57, 0
	s_cmp_eq_u32 s73, 12
	s_cselect_b64 s[40:41], -1, 0
	s_and_b64 s[54:55], s[40:41], exec
	s_cselect_b32 s75, s27, s75
	s_cselect_b32 s74, s29, s74
	s_cselect_b32 s54, 0, s38
	s_add_i32 s81, s68, s43
	s_add_i32 m0, s48, 0xc000
	s_add_i32 s80, s48, 0xe000
	s_add_i32 s82, s81, 0x2000
	s_add_u32 s76, s74, 0x80000
	s_addc_u32 s77, s75, 0
	s_and_b64 s[40:41], s[6:7], s[40:41]
	s_and_b64 s[40:41], s[40:41], exec
	s_cselect_b32 s41, s30, s14
	s_cselect_b32 s40, s31, s15
	s_add_u32 s78, s41, s54
	ds_read_b128 v[66:69], v135
	ds_read_b128 v[70:73], v135 offset:1024
	ds_read_b128 v[74:77], v135 offset:2048
	ds_read_b128 v[78:81], v135 offset:3072
	s_addc_u32 s79, s40, 0
	s_add_i32 s83, 0, 0x18000
	s_add_u32 s54, s78, 0x80000
	s_addc_u32 s55, s79, 0
	s_add_i32 s84, s83, s43
	s_add_i32 s85, s84, 0x2000
	s_add_u32 s40, s74, 0x80080
	s_addc_u32 s41, s75, 0
	s_cmp_lg_u32 s73, 12
	v_lshl_add_u64 v[138:139], v[128:129], 0, s[56:57]
	ds_read_b128 v[82:85], v136
	ds_read_b128 v[86:89], v136 offset:1024
	ds_read_b128 v[90:93], v136 offset:2048
	ds_read_b128 v[94:97], v136 offset:3072
	ds_read_b128 v[98:101], v136 offset:4096
	ds_read_b128 v[102:105], v136 offset:5120
	ds_read_b128 v[106:109], v136 offset:6144
	ds_read_b128 v[110:113], v136 offset:7168
	global_load_lds_dwordx4 v[138:139], off
	v_lshl_add_u64 v[138:139], v[130:131], 0, s[56:57]
	s_mov_b32 m0, s80
	s_nop 0
	global_load_lds_dwordx4 v[138:139], off
	s_waitcnt vmcnt(8)
	s_waitcnt lgkmcnt(0)
	s_barrier
	s_setprio 1
	s_waitcnt lgkmcnt(0)
	v_mfma_f32_16x16x32_bf16 v[62:65], v[66:69], v[82:85], v[62:65]
	v_mfma_f32_16x16x32_bf16 v[54:57], v[74:77], v[82:85], v[54:57]
	v_mfma_f32_16x16x32_bf16 v[46:49], v[66:69], v[90:93], v[46:49]
	v_mfma_f32_16x16x32_bf16 v[42:45], v[74:77], v[90:93], v[42:45]
	v_mfma_f32_16x16x32_bf16 v[38:41], v[66:69], v[98:101], v[38:41]
	v_mfma_f32_16x16x32_bf16 v[30:33], v[74:77], v[98:101], v[30:33]
	v_mfma_f32_16x16x32_bf16 v[22:25], v[66:69], v[106:109], v[22:25]
	v_mfma_f32_16x16x32_bf16 v[18:21], v[74:77], v[106:109], v[18:21]
	v_mfma_f32_16x16x32_bf16 v[62:65], v[70:73], v[86:89], v[62:65]
	v_mfma_f32_16x16x32_bf16 v[54:57], v[78:81], v[86:89], v[54:57]
	v_mfma_f32_16x16x32_bf16 v[46:49], v[70:73], v[94:97], v[46:49]
	v_mfma_f32_16x16x32_bf16 v[42:45], v[78:81], v[94:97], v[42:45]
	v_mfma_f32_16x16x32_bf16 v[38:41], v[70:73], v[102:105], v[38:41]
	v_mfma_f32_16x16x32_bf16 v[30:33], v[78:81], v[102:105], v[30:33]
	v_mfma_f32_16x16x32_bf16 v[22:25], v[70:73], v[110:113], v[22:25]
	v_mfma_f32_16x16x32_bf16 v[18:21], v[78:81], v[110:113], v[18:21]
	s_setprio 0
	s_setprio 1
	s_setprio 0
	s_barrier
	s_mov_b32 m0, s81
	v_lshl_add_u64 v[138:139], s[74:75], 0, v[114:115]
	ds_read_b128 v[82:85], v136 offset:16384
	ds_read_b128 v[86:89], v136 offset:17408
	ds_read_b128 v[90:93], v136 offset:18432
	ds_read_b128 v[94:97], v136 offset:19456
	ds_read_b128 v[98:101], v136 offset:20480
	ds_read_b128 v[102:105], v136 offset:21504
	ds_read_b128 v[106:109], v136 offset:22528
	ds_read_b128 v[110:113], v136 offset:23552
	global_load_lds_dwordx4 v[138:139], off
	v_lshl_add_u64 v[140:141], s[74:75], 0, v[116:117]
	s_mov_b32 m0, s82
	v_lshl_add_u64 v[142:143], s[76:77], 0, v[114:115]
	global_load_lds_dwordx4 v[140:141], off
	s_mov_b32 m0, s49
	v_lshl_add_u64 v[144:145], s[78:79], 0, v[116:117]
	global_load_lds_dwordx4 v[142:143], off
	v_lshl_add_u64 v[142:143], s[76:77], 0, v[116:117]
	s_mov_b32 m0, s50
	s_nop 0
	global_load_lds_dwordx4 v[142:143], off
	v_lshl_add_u64 v[142:143], s[78:79], 0, v[114:115]
	s_mov_b32 m0, s48
	s_nop 0
	global_load_lds_dwordx4 v[142:143], off
	s_mov_b32 m0, s51
	s_nop 0
	global_load_lds_dwordx4 v[144:145], off
	s_waitcnt vmcnt(8)
	s_waitcnt lgkmcnt(0)
	s_barrier
	s_setprio 1
	s_waitcnt lgkmcnt(0)
	v_mfma_f32_16x16x32_bf16 v[58:61], v[66:69], v[82:85], v[58:61]
	v_mfma_f32_16x16x32_bf16 v[50:53], v[74:77], v[82:85], v[50:53]
	v_mfma_f32_16x16x32_bf16 v[34:37], v[66:69], v[90:93], v[34:37]
	v_mfma_f32_16x16x32_bf16 v[26:29], v[74:77], v[90:93], v[26:29]
	v_mfma_f32_16x16x32_bf16 v[14:17], v[66:69], v[98:101], v[14:17]
	v_mfma_f32_16x16x32_bf16 v[10:13], v[74:77], v[98:101], v[10:13]
	v_mfma_f32_16x16x32_bf16 v[6:9], v[66:69], v[106:109], v[6:9]
	v_mfma_f32_16x16x32_bf16 v[2:5], v[74:77], v[106:109], v[2:5]
	v_mfma_f32_16x16x32_bf16 v[58:61], v[70:73], v[86:89], v[58:61]
	v_mfma_f32_16x16x32_bf16 v[50:53], v[78:81], v[86:89], v[50:53]
	v_mfma_f32_16x16x32_bf16 v[34:37], v[70:73], v[94:97], v[34:37]
	v_mfma_f32_16x16x32_bf16 v[26:29], v[78:81], v[94:97], v[26:29]
	v_mfma_f32_16x16x32_bf16 v[14:17], v[70:73], v[102:105], v[14:17]
	v_mfma_f32_16x16x32_bf16 v[10:13], v[78:81], v[102:105], v[10:13]
	v_mfma_f32_16x16x32_bf16 v[6:9], v[70:73], v[110:113], v[6:9]
	v_mfma_f32_16x16x32_bf16 v[2:5], v[78:81], v[110:113], v[2:5]
	s_setprio 0
	s_setprio 1
	s_setprio 0
	s_barrier
	v_add_u32_e32 v78, s83, v133
	ds_read_b128 v[66:69], v78
	ds_read_b128 v[70:73], v78 offset:1024
	ds_read_b128 v[74:77], v78 offset:2048
	ds_read_b128 v[78:81], v78 offset:3072
	s_mov_b32 m0, s52
	v_lshl_add_u64 v[146:147], s[54:55], 0, v[114:115]
	ds_read_b128 v[82:85], v136 offset:32768
	ds_read_b128 v[86:89], v136 offset:33792
	ds_read_b128 v[90:93], v136 offset:34816
	ds_read_b128 v[94:97], v136 offset:35840
	ds_read_b128 v[98:101], v136 offset:36864
	ds_read_b128 v[102:105], v136 offset:37888
	ds_read_b128 v[106:109], v136 offset:38912
	ds_read_b128 v[110:113], v136 offset:39936
	global_load_lds_dwordx4 v[146:147], off
	v_lshl_add_u64 v[146:147], s[54:55], 0, v[116:117]
	s_mov_b32 m0, s53
	s_nop 0
	global_load_lds_dwordx4 v[146:147], off
	s_waitcnt vmcnt(8)
	s_waitcnt lgkmcnt(0)
	s_barrier
	s_setprio 1
	s_waitcnt lgkmcnt(0)
	v_mfma_f32_16x16x32_bf16 v[62:65], v[66:69], v[82:85], v[62:65]
	v_mfma_f32_16x16x32_bf16 v[54:57], v[74:77], v[82:85], v[54:57]
	v_mfma_f32_16x16x32_bf16 v[46:49], v[66:69], v[90:93], v[46:49]
	v_mfma_f32_16x16x32_bf16 v[42:45], v[74:77], v[90:93], v[42:45]
	v_mfma_f32_16x16x32_bf16 v[38:41], v[66:69], v[98:101], v[38:41]
	v_mfma_f32_16x16x32_bf16 v[30:33], v[74:77], v[98:101], v[30:33]
	v_mfma_f32_16x16x32_bf16 v[22:25], v[66:69], v[106:109], v[22:25]
	v_mfma_f32_16x16x32_bf16 v[18:21], v[74:77], v[106:109], v[18:21]
	v_mfma_f32_16x16x32_bf16 v[62:65], v[70:73], v[86:89], v[62:65]
	v_mfma_f32_16x16x32_bf16 v[54:57], v[78:81], v[86:89], v[54:57]
	v_mfma_f32_16x16x32_bf16 v[46:49], v[70:73], v[94:97], v[46:49]
	v_mfma_f32_16x16x32_bf16 v[42:45], v[78:81], v[94:97], v[42:45]
	v_mfma_f32_16x16x32_bf16 v[38:41], v[70:73], v[102:105], v[38:41]
	v_mfma_f32_16x16x32_bf16 v[30:33], v[78:81], v[102:105], v[30:33]
	v_mfma_f32_16x16x32_bf16 v[22:25], v[70:73], v[110:113], v[22:25]
	v_mfma_f32_16x16x32_bf16 v[18:21], v[78:81], v[110:113], v[18:21]
	s_setprio 0
	s_setprio 1
	s_setprio 0
	s_barrier
	s_mov_b32 m0, s84
	v_lshl_add_u64 v[138:139], v[138:139], 0, s[12:13]
	ds_read_b128 v[106:109], v136 offset:49152
	ds_read_b128 v[110:113], v136 offset:50176
	ds_read_b128 v[98:101], v136 offset:51200
	ds_read_b128 v[102:105], v136 offset:52224
	ds_read_b128 v[90:93], v136 offset:53248
	ds_read_b128 v[94:97], v136 offset:54272
	ds_read_b128 v[82:85], v136 offset:55296
	ds_read_b128 v[86:89], v136 offset:56320
	global_load_lds_dwordx4 v[138:139], off
	v_lshl_add_u64 v[138:139], v[140:141], 0, s[12:13]
	s_mov_b32 m0, s85
	s_nop 0
	global_load_lds_dwordx4 v[138:139], off
	v_lshl_add_u64 v[138:139], s[40:41], 0, v[114:115]
	s_mov_b32 m0, s65
	s_nop 0
	global_load_lds_dwordx4 v[138:139], off
	v_lshl_add_u64 v[138:139], s[40:41], 0, v[116:117]
	s_mov_b32 m0, s66
	s_nop 0
	global_load_lds_dwordx4 v[138:139], off
	v_lshl_add_u64 v[138:139], v[142:143], 0, s[12:13]
	s_mov_b32 m0, s63
	s_nop 0
	global_load_lds_dwordx4 v[138:139], off
	v_lshl_add_u64 v[138:139], v[144:145], 0, s[12:13]
	s_mov_b32 m0, s64
	s_nop 0
	global_load_lds_dwordx4 v[138:139], off
	s_waitcnt vmcnt(8)
	s_waitcnt lgkmcnt(0)
	s_barrier
	s_cbranch_scc1 .LBB0_811
	v_mov_b32_e32 v137, v1
	v_mov_b32_e32 v138, v132
	s_andn2_b64 vcc, exec, s[16:17]
	s_cbranch_vccnz .LBB0_810
	v_add_u32_e32 v140, s70, v137
	v_ashrrev_i32_e32 v141, 31, v140
	v_lshl_add_u32 v138, v138, 2, s62
	v_lshlrev_b64 v[140:141], 8, v[140:141]
	v_ashrrev_i32_e32 v139, 31, v138
	v_lshl_add_u64 v[140:141], s[36:37], 0, v[140:141]
	v_lshl_add_u64 v[138:139], v[138:139], 2, v[140:141]
	v_add_co_u32_e32 v142, vcc, 0x1000, v138
	global_store_dwordx4 v[138:139], v[62:65], off sc1
	global_store_dwordx4 v[138:139], v[54:57], off offset:64 sc1
	v_addc_co_u32_e32 v143, vcc, 0, v139, vcc
	v_lshl_add_u64 v[140:141], v[138:139], 0, s[20:21]
	global_store_dwordx4 v[142:143], v[46:49], off sc1
	global_store_dwordx4 v[140:141], v[42:45], off offset:64 sc1
	v_add_co_u32_e32 v142, vcc, 0x2000, v138
	v_lshl_add_u64 v[140:141], v[138:139], 0, s[22:23]
	s_nop 0
	v_addc_co_u32_e32 v143, vcc, 0, v139, vcc
	global_store_dwordx4 v[142:143], v[38:41], off sc1
	global_store_dwordx4 v[140:141], v[30:33], off offset:64 sc1
	v_lshl_add_u64 v[140:141], v[138:139], 0, s[24:25]
	v_add_co_u32_e32 v138, vcc, 0x3000, v138
	s_nop 1
	v_addc_co_u32_e32 v139, vcc, 0, v139, vcc
	global_store_dwordx4 v[138:139], v[22:25], off sc1
	global_store_dwordx4 v[140:141], v[18:21], off offset:64 sc1
	s_branch .LBB0_810

.LBB0_819:
	v_add_u32_e32 v18, s2, v134
	v_ashrrev_i32_e32 v19, 31, v18
	v_lshlrev_b64 v[20:21], 8, v[18:19]
	v_lshl_add_u64 v[20:21], s[36:37], 0, v[20:21]
	v_lshl_add_u64 v[20:21], v[20:21], 0, v[118:119]
	global_store_dwordx4 v[20:21], v[58:61], off sc1
	global_store_dwordx4 v[20:21], v[50:53], off offset:64 sc1
	v_or_b32_e32 v20, 16, v18
	v_ashrrev_i32_e32 v21, 31, v20
	v_lshlrev_b64 v[20:21], 8, v[20:21]
	v_lshl_add_u64 v[20:21], s[36:37], 0, v[20:21]
	v_lshl_add_u64 v[20:21], v[20:21], 0, v[118:119]
	global_store_dwordx4 v[20:21], v[34:37], off sc1
	global_store_dwordx4 v[20:21], v[26:29], off offset:64 sc1
	v_or_b32_e32 v20, 32, v18
	v_ashrrev_i32_e32 v21, 31, v20
	v_lshlrev_b64 v[20:21], 8, v[20:21]
	v_lshl_add_u64 v[20:21], s[36:37], 0, v[20:21]
	v_lshl_add_u64 v[20:21], v[20:21], 0, v[118:119]
	global_store_dwordx4 v[20:21], v[14:17], off sc1
	global_store_dwordx4 v[20:21], v[10:13], off offset:64 sc1
	s_nop 1
	v_or_b32_e32 v10, 48, v18
	v_ashrrev_i32_e32 v11, 31, v10
	v_lshlrev_b64 v[10:11], 8, v[10:11]
	v_lshl_add_u64 v[10:11], s[36:37], 0, v[10:11]
	v_lshl_add_u64 v[10:11], v[10:11], 0, v[118:119]
	global_store_dwordx4 v[10:11], v[6:9], off sc1
	global_store_dwordx4 v[10:11], v[2:5], off offset:64 sc1
	s_andn2_b64 vcc, exec, s[6:7]
	s_mov_b64 s[6:7], -1
	s_cbranch_vccnz .LBB0_802

.LBB0_1294:
	s_mov_b64 s[56:57], s[40:41]
	s_add_u32 s2, s71, s56
	s_addc_u32 s22, s72, s57
	s_add_u32 s40, s56, 0x100
	s_addc_u32 s41, s57, 0
	s_cmp_eq_u32 s73, 28
	s_cselect_b64 s[8:9], -1, 0
	s_and_b64 s[12:13], s[8:9], exec
	s_cselect_b32 s61, s67, s22
	s_cselect_b32 s60, s68, s2
	s_cselect_b32 s2, 0, s40
	s_add_i32 s22, s86, s42
	s_add_i32 m0, s51, 0xc000
	s_add_i32 s13, s51, 0xe000
	s_add_i32 s23, s22, 0x2000
	s_add_u32 s62, s60, 0x80000
	s_addc_u32 s63, s61, 0
	s_add_i32 s24, s87, s42
	s_add_i32 s25, s24, 0x2000
	s_and_b64 s[8:9], s[6:7], s[8:9]
	ds_read_b128 v[130:133], v229
	ds_read_b128 v[134:137], v229 offset:1024
	ds_read_b128 v[138:141], v229 offset:2048
	ds_read_b128 v[142:145], v229 offset:3072
	ds_read_b128 v[146:149], v230
	ds_read_b128 v[150:153], v230 offset:1024
	ds_read_b128 v[154:157], v230 offset:2048
	ds_read_b128 v[158:161], v230 offset:3072
	s_and_b64 s[8:9], s[8:9], exec
	s_cselect_b32 s9, s30, s36
	s_cselect_b32 s8, s31, s37
	s_add_u32 s64, s9, s2
	s_addc_u32 s65, s8, 0
	s_add_i32 s82, 0, 0x18000
	s_add_i32 s83, 0, 0x1c000
	s_add_u32 s58, s64, 0x80000
	s_addc_u32 s59, s65, 0
	s_add_i32 s8, s82, s42
	s_add_i32 s2, s8, 0x2000
	s_add_u32 s54, s60, 0x80080
	s_addc_u32 s55, s61, 0
	s_add_i32 s12, s83, s42
	s_add_i32 s9, s12, 0x2000
	s_cmp_lg_u32 s73, 28
	v_lshl_add_u64 v[224:225], v[220:221], 0, s[56:57]
	ds_read_b128 v[162:165], v231
	ds_read_b128 v[166:169], v231 offset:1024
	ds_read_b128 v[170:173], v231 offset:2048
	ds_read_b128 v[174:177], v231 offset:3072
	ds_read_b128 v[178:181], v231 offset:4096
	ds_read_b128 v[182:185], v231 offset:5120
	ds_read_b128 v[186:189], v231 offset:6144
	ds_read_b128 v[190:193], v231 offset:7168
	global_load_lds_dwordx4 v[224:225], off
	v_lshl_add_u64 v[224:225], v[222:223], 0, s[56:57]
	s_mov_b32 m0, s13
	s_nop 0
	global_load_lds_dwordx4 v[224:225], off
	s_waitcnt vmcnt(8)
	s_waitcnt lgkmcnt(0)
	s_barrier
	s_setprio 1
	s_waitcnt lgkmcnt(0)
	v_mfma_f32_16x16x32_bf16 v[62:65], v[130:133], v[162:165], v[62:65]
	v_mfma_f32_16x16x32_bf16 v[58:61], v[138:141], v[162:165], v[58:61]
	v_mfma_f32_16x16x32_bf16 v[54:57], v[130:133], v[170:173], v[54:57]
	v_mfma_f32_16x16x32_bf16 v[50:53], v[138:141], v[170:173], v[50:53]
	v_mfma_f32_16x16x32_bf16 v[46:49], v[130:133], v[178:181], v[46:49]
	v_mfma_f32_16x16x32_bf16 v[42:45], v[138:141], v[178:181], v[42:45]
	v_mfma_f32_16x16x32_bf16 v[38:41], v[130:133], v[186:189], v[38:41]
	v_mfma_f32_16x16x32_bf16 v[34:37], v[138:141], v[186:189], v[34:37]
	v_mfma_f32_16x16x32_bf16 v[62:65], v[134:137], v[166:169], v[62:65]
	v_mfma_f32_16x16x32_bf16 v[58:61], v[142:145], v[166:169], v[58:61]
	v_mfma_f32_16x16x32_bf16 v[54:57], v[134:137], v[174:177], v[54:57]
	v_mfma_f32_16x16x32_bf16 v[50:53], v[142:145], v[174:177], v[50:53]
	v_mfma_f32_16x16x32_bf16 v[46:49], v[134:137], v[182:185], v[46:49]
	v_mfma_f32_16x16x32_bf16 v[42:45], v[142:145], v[182:185], v[42:45]
	v_mfma_f32_16x16x32_bf16 v[38:41], v[134:137], v[190:193], v[38:41]
	v_mfma_f32_16x16x32_bf16 v[34:37], v[142:145], v[190:193], v[34:37]
	s_setprio 0
	s_setprio 1
	v_mfma_f32_16x16x32_bf16 v[30:33], v[146:149], v[162:165], v[30:33]
	v_mfma_f32_16x16x32_bf16 v[26:29], v[154:157], v[162:165], v[26:29]
	v_mfma_f32_16x16x32_bf16 v[22:25], v[146:149], v[170:173], v[22:25]
	v_mfma_f32_16x16x32_bf16 v[18:21], v[154:157], v[170:173], v[18:21]
	v_mfma_f32_16x16x32_bf16 v[14:17], v[146:149], v[178:181], v[14:17]
	v_mfma_f32_16x16x32_bf16 v[10:13], v[154:157], v[178:181], v[10:13]
	v_mfma_f32_16x16x32_bf16 v[6:9], v[146:149], v[186:189], v[6:9]
	v_mfma_f32_16x16x32_bf16 v[2:5], v[154:157], v[186:189], v[2:5]
	v_mfma_f32_16x16x32_bf16 v[30:33], v[150:153], v[166:169], v[30:33]
	v_mfma_f32_16x16x32_bf16 v[26:29], v[158:161], v[166:169], v[26:29]
	v_mfma_f32_16x16x32_bf16 v[22:25], v[150:153], v[174:177], v[22:25]
	v_mfma_f32_16x16x32_bf16 v[18:21], v[158:161], v[174:177], v[18:21]
	v_mfma_f32_16x16x32_bf16 v[14:17], v[150:153], v[182:185], v[14:17]
	v_mfma_f32_16x16x32_bf16 v[10:13], v[158:161], v[182:185], v[10:13]
	v_mfma_f32_16x16x32_bf16 v[6:9], v[150:153], v[190:193], v[6:9]
	v_mfma_f32_16x16x32_bf16 v[2:5], v[158:161], v[190:193], v[2:5]
	s_setprio 0
	s_barrier
	s_mov_b32 m0, s22
	v_lshl_add_u64 v[224:225], s[60:61], 0, v[196:197]
	ds_read_b128 v[162:165], v231 offset:16384
	ds_read_b128 v[166:169], v231 offset:17408
	ds_read_b128 v[170:173], v231 offset:18432
	ds_read_b128 v[174:177], v231 offset:19456
	ds_read_b128 v[178:181], v231 offset:20480
	ds_read_b128 v[182:185], v231 offset:21504
	ds_read_b128 v[186:189], v231 offset:22528
	ds_read_b128 v[190:193], v231 offset:23552
	global_load_lds_dwordx4 v[224:225], off
	v_lshl_add_u64 v[232:233], s[60:61], 0, v[200:201]
	s_mov_b32 m0, s23
	v_lshl_add_u64 v[234:235], s[62:63], 0, v[196:197]
	global_load_lds_dwordx4 v[232:233], off
	s_mov_b32 m0, s24
	v_lshl_add_u64 v[236:237], s[64:65], 0, v[198:199]
	global_load_lds_dwordx4 v[234:235], off
	v_lshl_add_u64 v[234:235], s[62:63], 0, v[200:201]
	s_mov_b32 m0, s25
	s_nop 0
	global_load_lds_dwordx4 v[234:235], off
	v_lshl_add_u64 v[234:235], s[64:65], 0, v[194:195]
	s_mov_b32 m0, s51
	s_nop 0
	global_load_lds_dwordx4 v[234:235], off
	s_mov_b32 m0, s52
	s_nop 0
	global_load_lds_dwordx4 v[236:237], off
	s_waitcnt vmcnt(8)
	s_waitcnt lgkmcnt(0)
	s_barrier
	s_setprio 1
	s_waitcnt lgkmcnt(0)
	v_mfma_f32_16x16x32_bf16 v[126:129], v[130:133], v[162:165], v[126:129]
	v_mfma_f32_16x16x32_bf16 v[122:125], v[138:141], v[162:165], v[122:125]
	v_mfma_f32_16x16x32_bf16 v[114:117], v[130:133], v[170:173], v[114:117]
	v_mfma_f32_16x16x32_bf16 v[106:109], v[138:141], v[170:173], v[106:109]
	v_mfma_f32_16x16x32_bf16 v[102:105], v[130:133], v[178:181], v[102:105]
	v_mfma_f32_16x16x32_bf16 v[94:97], v[138:141], v[178:181], v[94:97]
	v_mfma_f32_16x16x32_bf16 v[86:89], v[130:133], v[186:189], v[86:89]
	v_mfma_f32_16x16x32_bf16 v[78:81], v[138:141], v[186:189], v[78:81]
	v_mfma_f32_16x16x32_bf16 v[126:129], v[134:137], v[166:169], v[126:129]
	v_mfma_f32_16x16x32_bf16 v[122:125], v[142:145], v[166:169], v[122:125]
	v_mfma_f32_16x16x32_bf16 v[114:117], v[134:137], v[174:177], v[114:117]
	v_mfma_f32_16x16x32_bf16 v[106:109], v[142:145], v[174:177], v[106:109]
	v_mfma_f32_16x16x32_bf16 v[102:105], v[134:137], v[182:185], v[102:105]
	v_mfma_f32_16x16x32_bf16 v[94:97], v[142:145], v[182:185], v[94:97]
	v_mfma_f32_16x16x32_bf16 v[86:89], v[134:137], v[190:193], v[86:89]
	v_mfma_f32_16x16x32_bf16 v[78:81], v[142:145], v[190:193], v[78:81]
	s_setprio 0
	s_setprio 1
	v_mfma_f32_16x16x32_bf16 v[118:121], v[146:149], v[162:165], v[118:121]
	v_mfma_f32_16x16x32_bf16 v[110:113], v[154:157], v[162:165], v[110:113]
	v_mfma_f32_16x16x32_bf16 v[98:101], v[146:149], v[170:173], v[98:101]
	v_mfma_f32_16x16x32_bf16 v[90:93], v[154:157], v[170:173], v[90:93]
	v_mfma_f32_16x16x32_bf16 v[82:85], v[146:149], v[178:181], v[82:85]
	v_mfma_f32_16x16x32_bf16 v[74:77], v[154:157], v[178:181], v[74:77]
	v_mfma_f32_16x16x32_bf16 v[70:73], v[146:149], v[186:189], v[70:73]
	v_mfma_f32_16x16x32_bf16 v[66:69], v[154:157], v[186:189], v[66:69]
	v_mfma_f32_16x16x32_bf16 v[118:121], v[150:153], v[166:169], v[118:121]
	v_mfma_f32_16x16x32_bf16 v[110:113], v[158:161], v[166:169], v[110:113]
	v_mfma_f32_16x16x32_bf16 v[98:101], v[150:153], v[174:177], v[98:101]
	v_mfma_f32_16x16x32_bf16 v[90:93], v[158:161], v[174:177], v[90:93]
	v_mfma_f32_16x16x32_bf16 v[82:85], v[150:153], v[182:185], v[82:85]
	v_mfma_f32_16x16x32_bf16 v[74:77], v[158:161], v[182:185], v[74:77]
	v_mfma_f32_16x16x32_bf16 v[70:73], v[150:153], v[190:193], v[70:73]
	v_mfma_f32_16x16x32_bf16 v[66:69], v[158:161], v[190:193], v[66:69]
	s_setprio 0
	s_barrier
	v_add_u32_e32 v130, s82, v227
	v_add_u32_e32 v142, s83, v227
	ds_read_b128 v[146:149], v130
	ds_read_b128 v[150:153], v130 offset:1024
	ds_read_b128 v[154:157], v130 offset:2048
	ds_read_b128 v[158:161], v130 offset:3072
	ds_read_b128 v[130:133], v142
	ds_read_b128 v[134:137], v142 offset:1024
	ds_read_b128 v[138:141], v142 offset:2048
	ds_read_b128 v[142:145], v142 offset:3072
	s_mov_b32 m0, s53
	v_lshl_add_u64 v[238:239], s[58:59], 0, v[194:195]
	ds_read_b128 v[162:165], v231 offset:32768
	ds_read_b128 v[166:169], v231 offset:33792
	ds_read_b128 v[170:173], v231 offset:34816
	ds_read_b128 v[174:177], v231 offset:35840
	ds_read_b128 v[178:181], v231 offset:36864
	ds_read_b128 v[182:185], v231 offset:37888
	ds_read_b128 v[186:189], v231 offset:38912
	ds_read_b128 v[190:193], v231 offset:39936
	global_load_lds_dwordx4 v[238:239], off
	v_lshl_add_u64 v[238:239], s[58:59], 0, v[198:199]
	s_mov_b32 m0, s74
	s_nop 0
	global_load_lds_dwordx4 v[238:239], off
	s_waitcnt vmcnt(8)
	s_waitcnt lgkmcnt(0)
	s_barrier
	s_setprio 1
	s_waitcnt lgkmcnt(0)
	v_mfma_f32_16x16x32_bf16 v[62:65], v[146:149], v[162:165], v[62:65]
	v_mfma_f32_16x16x32_bf16 v[58:61], v[154:157], v[162:165], v[58:61]
	v_mfma_f32_16x16x32_bf16 v[54:57], v[146:149], v[170:173], v[54:57]
	v_mfma_f32_16x16x32_bf16 v[50:53], v[154:157], v[170:173], v[50:53]
	v_mfma_f32_16x16x32_bf16 v[46:49], v[146:149], v[178:181], v[46:49]
	v_mfma_f32_16x16x32_bf16 v[42:45], v[154:157], v[178:181], v[42:45]
	v_mfma_f32_16x16x32_bf16 v[38:41], v[146:149], v[186:189], v[38:41]
	v_mfma_f32_16x16x32_bf16 v[34:37], v[154:157], v[186:189], v[34:37]
	v_mfma_f32_16x16x32_bf16 v[62:65], v[150:153], v[166:169], v[62:65]
	v_mfma_f32_16x16x32_bf16 v[58:61], v[158:161], v[166:169], v[58:61]
	v_mfma_f32_16x16x32_bf16 v[54:57], v[150:153], v[174:177], v[54:57]
	v_mfma_f32_16x16x32_bf16 v[50:53], v[158:161], v[174:177], v[50:53]
	v_mfma_f32_16x16x32_bf16 v[46:49], v[150:153], v[182:185], v[46:49]
	v_mfma_f32_16x16x32_bf16 v[42:45], v[158:161], v[182:185], v[42:45]
	v_mfma_f32_16x16x32_bf16 v[38:41], v[150:153], v[190:193], v[38:41]
	v_mfma_f32_16x16x32_bf16 v[34:37], v[158:161], v[190:193], v[34:37]
	s_setprio 0
	s_setprio 1
	v_mfma_f32_16x16x32_bf16 v[30:33], v[130:133], v[162:165], v[30:33]
	v_mfma_f32_16x16x32_bf16 v[26:29], v[138:141], v[162:165], v[26:29]
	v_mfma_f32_16x16x32_bf16 v[22:25], v[130:133], v[170:173], v[22:25]
	v_mfma_f32_16x16x32_bf16 v[18:21], v[138:141], v[170:173], v[18:21]
	v_mfma_f32_16x16x32_bf16 v[14:17], v[130:133], v[178:181], v[14:17]
	v_mfma_f32_16x16x32_bf16 v[10:13], v[138:141], v[178:181], v[10:13]
	v_mfma_f32_16x16x32_bf16 v[6:9], v[130:133], v[186:189], v[6:9]
	v_mfma_f32_16x16x32_bf16 v[2:5], v[138:141], v[186:189], v[2:5]
	v_mfma_f32_16x16x32_bf16 v[30:33], v[134:137], v[166:169], v[30:33]
	v_mfma_f32_16x16x32_bf16 v[26:29], v[142:145], v[166:169], v[26:29]
	v_mfma_f32_16x16x32_bf16 v[22:25], v[134:137], v[174:177], v[22:25]
	v_mfma_f32_16x16x32_bf16 v[18:21], v[142:145], v[174:177], v[18:21]
	v_mfma_f32_16x16x32_bf16 v[14:17], v[134:137], v[182:185], v[14:17]
	v_mfma_f32_16x16x32_bf16 v[10:13], v[142:145], v[182:185], v[10:13]
	v_mfma_f32_16x16x32_bf16 v[6:9], v[134:137], v[190:193], v[6:9]
	v_mfma_f32_16x16x32_bf16 v[2:5], v[142:145], v[190:193], v[2:5]
	s_setprio 0
	s_barrier
	s_mov_b32 m0, s8
	v_lshl_add_u64 v[224:225], v[224:225], 0, s[18:19]
	ds_read_b128 v[186:189], v231 offset:49152
	ds_read_b128 v[190:193], v231 offset:50176
	ds_read_b128 v[178:181], v231 offset:51200
	ds_read_b128 v[182:185], v231 offset:52224
	ds_read_b128 v[170:173], v231 offset:53248
	ds_read_b128 v[174:177], v231 offset:54272
	ds_read_b128 v[162:165], v231 offset:55296
	ds_read_b128 v[166:169], v231 offset:56320
	global_load_lds_dwordx4 v[224:225], off
	v_lshl_add_u64 v[224:225], v[232:233], 0, s[18:19]
	s_mov_b32 m0, s2
	s_nop 0
	global_load_lds_dwordx4 v[224:225], off
	v_lshl_add_u64 v[224:225], s[54:55], 0, v[196:197]
	s_mov_b32 m0, s12
	s_nop 0
	global_load_lds_dwordx4 v[224:225], off
	v_lshl_add_u64 v[224:225], s[54:55], 0, v[200:201]
	s_mov_b32 m0, s9
	s_nop 0
	global_load_lds_dwordx4 v[224:225], off
	v_lshl_add_u64 v[224:225], v[234:235], 0, s[18:19]
	s_mov_b32 m0, s78
	s_nop 0
	global_load_lds_dwordx4 v[224:225], off
	v_lshl_add_u64 v[224:225], v[236:237], 0, s[18:19]
	s_mov_b32 m0, s79
	s_nop 0
	global_load_lds_dwordx4 v[224:225], off
	s_waitcnt vmcnt(8)
	s_waitcnt lgkmcnt(0)
	s_barrier
	s_cbranch_scc1 .LBB0_1293
	v_mov_b32_e32 v202, v1
	v_mov_b32_e32 v224, v209
	s_mov_b64 s[54:55], -1
	v_add_u32_e32 v202, s69, v202
	v_lshlrev_b32_e32 v224, 3, v224
	s_and_b64 vcc, exec, s[38:39]
	v_add_u32_e32 v234, 16, v202
	v_add_u32_e32 v233, 32, v202
	v_add_u32_e32 v232, 48, v202
	s_cbranch_vccz .LBB0_1297
	v_add_u32_e32 v236, s70, v224
	v_ashrrev_i32_e32 v237, 31, v236
	v_mov_b64_e32 v[240:241], s[14:15]
	v_mad_i64_i32 v[238:239], s[8:9], v202, s88, v[240:241]
	v_lshlrev_b64 v[244:245], 1, v[236:237]
	v_lshl_add_u64 v[246:247], v[238:239], 0, v[244:245]
	v_cvt_pk_bf16_f32 v236, v62, v63
	v_cvt_pk_bf16_f32 v237, v64, v65
	v_cvt_pk_bf16_f32 v238, v58, v59
	v_cvt_pk_bf16_f32 v239, v60, v61
	global_store_dwordx4 v[246:247], v[236:239], off sc1
	s_mov_b64 s[54:55], 0
	s_nop 0
	v_cvt_pk_bf16_f32 v236, v30, v31
	v_cvt_pk_bf16_f32 v237, v32, v33
	v_cvt_pk_bf16_f32 v238, v26, v27
	v_cvt_pk_bf16_f32 v239, v28, v29
	global_store_dwordx4 v[246:247], v[236:239], off offset:256 sc1
	s_nop 1
	v_mad_i64_i32 v[236:237], s[8:9], v234, s88, v[240:241]
	v_lshl_add_u64 v[246:247], v[236:237], 0, v[244:245]
	v_cvt_pk_bf16_f32 v236, v54, v55
	v_cvt_pk_bf16_f32 v237, v56, v57
	v_cvt_pk_bf16_f32 v238, v50, v51
	v_cvt_pk_bf16_f32 v239, v52, v53
	global_store_dwordx4 v[246:247], v[236:239], off sc1
	s_nop 1
	v_cvt_pk_bf16_f32 v236, v22, v23
	v_cvt_pk_bf16_f32 v237, v24, v25
	v_cvt_pk_bf16_f32 v238, v18, v19
	v_cvt_pk_bf16_f32 v239, v20, v21
	global_store_dwordx4 v[246:247], v[236:239], off offset:256 sc1
	s_nop 1
	v_mad_i64_i32 v[236:237], s[8:9], v233, s88, v[240:241]
	v_lshl_add_u64 v[246:247], v[236:237], 0, v[244:245]
	v_cvt_pk_bf16_f32 v236, v46, v47
	v_cvt_pk_bf16_f32 v237, v48, v49
	v_cvt_pk_bf16_f32 v238, v42, v43
	v_cvt_pk_bf16_f32 v239, v44, v45
	global_store_dwordx4 v[246:247], v[236:239], off sc1
	s_nop 1
	v_cvt_pk_bf16_f32 v236, v14, v15
	v_cvt_pk_bf16_f32 v237, v16, v17
	v_cvt_pk_bf16_f32 v238, v10, v11
	v_cvt_pk_bf16_f32 v239, v12, v13
	global_store_dwordx4 v[246:247], v[236:239], off offset:256 sc1
	s_nop 1
	v_mad_i64_i32 v[236:237], s[8:9], v232, s88, v[240:241]
	v_lshl_add_u64 v[240:241], v[236:237], 0, v[244:245]
	v_cvt_pk_bf16_f32 v236, v38, v39
	v_cvt_pk_bf16_f32 v237, v40, v41
	v_cvt_pk_bf16_f32 v238, v34, v35
	v_cvt_pk_bf16_f32 v239, v36, v37
	global_store_dwordx4 v[240:241], v[236:239], off sc1
	s_nop 1
	v_cvt_pk_bf16_f32 v236, v6, v7
	v_cvt_pk_bf16_f32 v237, v8, v9
	v_cvt_pk_bf16_f32 v238, v2, v3
	v_cvt_pk_bf16_f32 v239, v4, v5
	global_store_dwordx4 v[240:241], v[236:239], off offset:256 sc1

.LBB0_1301:
	v_add_u32_e32 v3, s29, v226
	s_mov_b64 s[36:37], -1
	s_and_b64 vcc, exec, s[38:39]
	v_add_u32_e32 v2, 0x80, v3
	s_cbranch_vccz .LBB0_1303
	v_or_b32_e32 v4, s27, v228
	v_ashrrev_i32_e32 v5, 31, v4
	v_mov_b64_e32 v[8:9], s[14:15]
	v_mad_i64_i32 v[6:7], s[8:9], v2, s88, v[8:9]
	v_lshlrev_b64 v[10:11], 1, v[4:5]
	v_lshl_add_u64 v[12:13], v[6:7], 0, v[10:11]
	v_cvt_pk_bf16_f32 v4, v126, v127
	v_cvt_pk_bf16_f32 v5, v128, v129
	v_cvt_pk_bf16_f32 v6, v122, v123
	v_cvt_pk_bf16_f32 v7, v124, v125
	global_store_dwordx4 v[12:13], v[4:7], off sc1
	s_mov_b64 s[36:37], 0
	s_nop 0
	v_cvt_pk_bf16_f32 v4, v118, v119
	v_cvt_pk_bf16_f32 v5, v120, v121
	v_cvt_pk_bf16_f32 v6, v110, v111
	v_cvt_pk_bf16_f32 v7, v112, v113
	global_store_dwordx4 v[12:13], v[4:7], off offset:256 sc1
	s_nop 1
	v_add_u32_e32 v4, 0x90, v3
	v_mad_i64_i32 v[4:5], s[8:9], v4, s88, v[8:9]
	v_lshl_add_u64 v[12:13], v[4:5], 0, v[10:11]
	v_cvt_pk_bf16_f32 v4, v114, v115
	v_cvt_pk_bf16_f32 v5, v116, v117
	v_cvt_pk_bf16_f32 v6, v106, v107
	v_cvt_pk_bf16_f32 v7, v108, v109
	global_store_dwordx4 v[12:13], v[4:7], off sc1
	s_nop 1
	v_cvt_pk_bf16_f32 v4, v98, v99
	v_cvt_pk_bf16_f32 v5, v100, v101
	v_cvt_pk_bf16_f32 v6, v90, v91
	v_cvt_pk_bf16_f32 v7, v92, v93
	global_store_dwordx4 v[12:13], v[4:7], off offset:256 sc1
	s_nop 1
	v_add_u32_e32 v4, 0xa0, v3
	v_mad_i64_i32 v[4:5], s[8:9], v4, s88, v[8:9]
	v_lshl_add_u64 v[12:13], v[4:5], 0, v[10:11]
	v_cvt_pk_bf16_f32 v4, v102, v103
	v_cvt_pk_bf16_f32 v5, v104, v105
	v_cvt_pk_bf16_f32 v6, v94, v95
	v_cvt_pk_bf16_f32 v7, v96, v97
	global_store_dwordx4 v[12:13], v[4:7], off sc1
	v_add_u32_e32 v3, 0xb0, v3
	s_nop 0
	v_cvt_pk_bf16_f32 v4, v82, v83
	v_cvt_pk_bf16_f32 v5, v84, v85
	v_cvt_pk_bf16_f32 v6, v74, v75
	v_cvt_pk_bf16_f32 v7, v76, v77
	global_store_dwordx4 v[12:13], v[4:7], off offset:256 sc1
	s_nop 1
	v_mad_i64_i32 v[4:5], s[8:9], v3, s88, v[8:9]
	v_lshl_add_u64 v[8:9], v[4:5], 0, v[10:11]
	v_cvt_pk_bf16_f32 v4, v86, v87
	v_cvt_pk_bf16_f32 v5, v88, v89
	v_cvt_pk_bf16_f32 v6, v78, v79
	v_cvt_pk_bf16_f32 v7, v80, v81
	global_store_dwordx4 v[8:9], v[4:7], off sc1
	s_nop 1
	v_cvt_pk_bf16_f32 v4, v70, v71
	v_cvt_pk_bf16_f32 v5, v72, v73
	v_cvt_pk_bf16_f32 v6, v66, v67
	v_cvt_pk_bf16_f32 v7, v68, v69
	global_store_dwordx4 v[8:9], v[4:7], off offset:256 sc1

.LBB0_1323:
	s_mov_b32 s55, s11
	s_lshl_b64 s[54:55], s[54:55], 1
	s_add_u32 s54, s56, s54
	v_lshl_add_u64 v[174:175], s[58:59], 0, v[210:211]
	s_addc_u32 s55, s57, s55
	v_lshlrev_b32_e32 v202, 1, v208
	v_lshl_add_u64 v[176:177], s[54:55], 0, v[202:203]
	v_mul_lo_u32 v163, v175, s40
	v_mad_u64_u32 v[166:167], s[54:55], v174, s40, 0
	v_add_u32_e32 v167, v167, v163
	s_waitcnt vmcnt(0)
	v_mul_f32_e32 v2, v2, v79
	v_lshl_add_u64 v[178:179], v[166:167], 1, v[176:177]
	v_mul_f32_e32 v6, v6, v78
	v_cvt_pk_bf16_f32 v166, v6, v2
	v_mul_f32_e32 v2, v14, v80
	v_mul_f32_e32 v6, v10, v81
	v_cvt_pk_bf16_f32 v167, v2, v6
	v_mul_f32_e32 v2, v22, v74
	v_mul_f32_e32 v6, v18, v75
	v_cvt_pk_bf16_f32 v168, v2, v6
	v_mul_f32_e32 v2, v30, v76
	v_mul_f32_e32 v6, v26, v77
	v_cvt_pk_bf16_f32 v169, v2, v6
	v_mul_f32_e32 v2, v38, v70
	v_mul_f32_e32 v6, v34, v71
	v_cvt_pk_bf16_f32 v170, v2, v6
	v_mul_f32_e32 v2, v46, v72
	v_mul_f32_e32 v6, v42, v73
	v_cvt_pk_bf16_f32 v171, v2, v6
	v_mul_f32_e32 v2, v54, v66
	s_mov_b32 s41, s11
	v_mul_f32_e32 v6, v50, v67
	v_cvt_pk_bf16_f32 v172, v2, v6
	v_mul_f32_e32 v2, v62, v68
	v_mul_f32_e32 v6, v58, v69
	v_cvt_pk_bf16_f32 v173, v2, v6
	global_store_dwordx4 v[178:179], v[166:169], off sc1
	global_store_dwordx4 v[178:179], v[170:173], off offset:16 sc1
	v_mul_f32_e32 v2, v7, v78
	v_mov_b64_e32 v[166:167], s[40:41]
	v_mul_f32_e32 v3, v3, v79
	v_mad_u64_u32 v[174:175], s[54:55], v174, s40, v[166:167]
	v_cvt_pk_bf16_f32 v166, v2, v3
	v_mul_f32_e32 v2, v15, v80
	v_mul_f32_e32 v3, v11, v81
	v_cvt_pk_bf16_f32 v167, v2, v3
	v_mul_f32_e32 v2, v23, v74
	v_mul_f32_e32 v3, v19, v75
	v_cvt_pk_bf16_f32 v168, v2, v3
	v_mul_f32_e32 v2, v31, v76
	v_mul_f32_e32 v3, v27, v77
	v_cvt_pk_bf16_f32 v169, v2, v3
	v_mul_f32_e32 v2, v39, v70
	v_mul_f32_e32 v3, v35, v71
	v_add_u32_e32 v175, v163, v175
	v_cvt_pk_bf16_f32 v170, v2, v3
	v_mul_f32_e32 v2, v47, v72
	v_mul_f32_e32 v3, v43, v73
	v_lshl_add_u64 v[178:179], v[174:175], 1, v[176:177]
	v_cvt_pk_bf16_f32 v171, v2, v3
	v_mul_f32_e32 v2, v55, v66
	v_mul_f32_e32 v3, v51, v67
	v_mul_f32_e32 v4, v4, v79
	v_cvt_pk_bf16_f32 v172, v2, v3
	v_mul_f32_e32 v2, v63, v68
	v_mul_f32_e32 v3, v59, v69
	v_cvt_pk_bf16_f32 v173, v2, v3
	global_store_dwordx4 v[178:179], v[166:169], off sc1
	global_store_dwordx4 v[178:179], v[170:173], off offset:16 sc1
	v_mul_f32_e32 v8, v8, v78
	v_cvt_pk_bf16_f32 v166, v8, v4
	v_mul_f32_e32 v4, v16, v80
	v_mul_f32_e32 v8, v12, v81
	v_cvt_pk_bf16_f32 v167, v4, v8
	v_mul_f32_e32 v4, v24, v74
	v_mul_f32_e32 v8, v20, v75
	v_cvt_pk_bf16_f32 v168, v4, v8
	v_mul_f32_e32 v4, v32, v76
	v_mul_f32_e32 v8, v28, v77
	v_cvt_pk_bf16_f32 v169, v4, v8
	v_mul_f32_e32 v4, v40, v70
	v_lshl_add_u64 v[2:3], v[174:175], 0, s[40:41]
	v_mul_f32_e32 v8, v36, v71
	v_cvt_pk_bf16_f32 v170, v4, v8
	v_mul_f32_e32 v4, v48, v72
	v_lshl_add_u64 v[6:7], v[2:3], 1, v[176:177]
	v_mul_f32_e32 v8, v44, v73
	v_cvt_pk_bf16_f32 v171, v4, v8
	v_mul_f32_e32 v4, v56, v66
	v_lshl_add_u64 v[2:3], v[2:3], 0, s[40:41]
	v_mul_f32_e32 v8, v52, v67
	v_cvt_pk_bf16_f32 v172, v4, v8
	v_mul_f32_e32 v4, v64, v68
	v_lshl_add_u64 v[10:11], v[2:3], 1, v[176:177]
	v_mul_f32_e32 v2, v9, v78
	v_mul_f32_e32 v3, v5, v79
	v_mul_f32_e32 v8, v60, v69
	v_cvt_pk_bf16_f32 v173, v4, v8
	global_store_dwordx4 v[6:7], v[166:169], off sc1
	global_store_dwordx4 v[6:7], v[170:173], off offset:16 sc1
	v_cvt_pk_bf16_f32 v2, v2, v3
	v_mul_f32_e32 v3, v17, v80
	v_mul_f32_e32 v4, v13, v81
	v_cvt_pk_bf16_f32 v3, v3, v4
	v_mul_f32_e32 v4, v25, v74
	v_mul_f32_e32 v5, v21, v75
	v_cvt_pk_bf16_f32 v4, v4, v5
	v_mul_f32_e32 v5, v33, v76
	v_mul_f32_e32 v6, v29, v77
	v_cvt_pk_bf16_f32 v5, v5, v6
	v_mul_f32_e32 v6, v41, v70
	v_mul_f32_e32 v7, v37, v71
	v_cvt_pk_bf16_f32 v6, v6, v7
	v_mul_f32_e32 v7, v49, v72
	v_mul_f32_e32 v8, v45, v73
	v_cvt_pk_bf16_f32 v7, v7, v8
	v_mul_f32_e32 v8, v57, v66
	v_mul_f32_e32 v9, v53, v67
	v_cvt_pk_bf16_f32 v8, v8, v9
	v_mul_f32_e32 v9, v65, v68
	v_mul_f32_e32 v12, v61, v69
	v_cvt_pk_bf16_f32 v9, v9, v12
	global_store_dwordx4 v[10:11], v[2:5], off sc1
	global_store_dwordx4 v[10:11], v[6:9], off offset:16 sc1
	v_mov_b64_e32 v[58:59], v[142:143]
	v_mov_b64_e32 v[62:63], v[138:139]
	v_mov_b64_e32 v[50:51], v[134:135]
	v_mov_b64_e32 v[54:55], v[130:131]
	v_mov_b64_e32 v[42:43], v[126:127]
	v_mov_b64_e32 v[46:47], v[122:123]
	v_mov_b64_e32 v[34:35], v[118:119]
	v_mov_b64_e32 v[38:39], v[114:115]
	v_mov_b64_e32 v[26:27], v[110:111]
	v_mov_b64_e32 v[30:31], v[106:107]
	v_mov_b64_e32 v[18:19], v[102:103]
	v_mov_b64_e32 v[22:23], v[98:99]
	v_mov_b64_e32 v[10:11], v[94:95]
	v_mov_b64_e32 v[14:15], v[90:91]
	v_mov_b64_e32 v[2:3], v[86:87]
	v_mov_b64_e32 v[6:7], v[82:83]
	s_add_i32 s23, s23, s9
	s_add_i32 s24, s24, s25
	s_add_i32 s83, s83, s84
	s_andn2_b64 vcc, exec, s[64:65]
	v_mov_b64_e32 v[60:61], v[144:145]
	v_mov_b64_e32 v[64:65], v[140:141]
	v_mov_b64_e32 v[52:53], v[136:137]
	v_mov_b64_e32 v[56:57], v[132:133]
	v_mov_b64_e32 v[44:45], v[128:129]
	v_mov_b64_e32 v[48:49], v[124:125]
	v_mov_b64_e32 v[36:37], v[120:121]
	v_mov_b64_e32 v[40:41], v[116:117]
	v_mov_b64_e32 v[28:29], v[112:113]
	v_mov_b64_e32 v[32:33], v[108:109]
	v_mov_b64_e32 v[20:21], v[104:105]
	v_mov_b64_e32 v[24:25], v[100:101]
	v_mov_b64_e32 v[12:13], v[96:97]
	v_mov_b64_e32 v[16:17], v[92:93]
	v_mov_b64_e32 v[4:5], v[88:89]
	v_mov_b64_e32 v[8:9], v[84:85]
	s_mov_b64 s[58:59], s[62:63]
	s_mov_b32 s54, s66
	s_mov_b32 s40, s2
	s_mov_b64 s[56:57], s[60:61]
	v_mov_b32_e32 v66, v146
	v_mov_b32_e32 v67, v147
	v_mov_b32_e32 v68, v148
	v_mov_b32_e32 v69, v149
	v_mov_b32_e32 v70, v150
	v_mov_b32_e32 v71, v151
	v_mov_b32_e32 v72, v152
	v_mov_b32_e32 v73, v153
	v_mov_b32_e32 v74, v154
	v_mov_b32_e32 v75, v155
	v_mov_b32_e32 v76, v156
	v_mov_b32_e32 v77, v157
	v_mov_b32_e32 v78, v158
	v_mov_b32_e32 v79, v159
	v_mov_b32_e32 v80, v160
	v_mov_b32_e32 v81, v161
	s_cbranch_vccz .LBB0_1311

.LBB0_1550:
	v_lshl_or_b32 v170, s12, 8, v185
	v_lshl_add_u32 v174, s14, 8, v1
	v_ashrrev_i32_e32 v171, 31, v170
	v_lshlrev_b64 v[202:203], 1, v[170:171]
	v_ashrrev_i32_e32 v175, 31, v174
	v_lshl_add_u64 v[172:173], s[18:19], 0, v[202:203]
	v_lshlrev_b64 v[204:205], 12, v[174:175]
	v_lshl_add_u64 v[130:131], v[172:173], 0, v[204:205]
	global_load_dwordx4 v[194:197], v[130:131], off
	global_load_dwordx4 v[198:201], v[130:131], off offset:256
	v_lshl_add_u64 v[176:177], v[174:175], 2, s[24:25]
	global_load_dword v206, v[176:177], off
	v_or_b32_e32 v186, 16, v174
	v_or_b32_e32 v182, 32, v174
	v_or_b32_e32 v178, 48, v174
	v_ashrrev_i32_e32 v187, 31, v186
	v_ashrrev_i32_e32 v183, 31, v182
	v_ashrrev_i32_e32 v179, 31, v178
	v_lshlrev_b64 v[132:133], 12, v[186:187]
	v_lshlrev_b64 v[136:137], 12, v[182:183]
	v_lshl_add_u64 v[130:131], v[186:187], 2, s[24:25]
	v_lshl_add_u64 v[134:135], v[182:183], 2, s[24:25]
	v_lshlrev_b64 v[138:139], 12, v[178:179]
	v_lshl_add_u64 v[132:133], v[172:173], 0, v[132:133]
	v_lshl_add_u64 v[136:137], v[172:173], 0, v[136:137]
	v_lshl_add_u64 v[208:209], v[178:179], 2, s[24:25]
	v_lshl_add_u64 v[210:211], v[172:173], 0, v[138:139]
	global_load_dword v188, v[130:131], off
	global_load_dwordx4 v[150:153], v[132:133], off
	global_load_dwordx4 v[146:149], v[132:133], off offset:256
	global_load_dword v184, v[134:135], off
	global_load_dwordx4 v[142:145], v[136:137], off
	global_load_dwordx4 v[138:141], v[136:137], off offset:256
	global_load_dword v180, v[208:209], off
	s_nop 0
	global_load_dwordx4 v[134:137], v[210:211], off
	global_load_dwordx4 v[130:133], v[210:211], off offset:256
	v_and_b32_e32 v207, 64, v192
	v_add_u32_e32 v207, 64, v207
	v_xor_b32_e32 v193, 16, v192
	v_cmp_lt_i32_e32 vcc, v193, v207
	s_waitcnt vmcnt(0)
	v_lshlrev_b32_e32 v208, 16, v194
	v_and_b32_e32 v209, 0xffff0000, v194
	v_lshlrev_b32_e32 v194, 16, v195
	v_and_b32_e32 v195, 0xffff0000, v195
	v_lshlrev_b32_e32 v212, 16, v198
	v_and_b32_e32 v213, 0xffff0000, v198
	v_lshlrev_b32_e32 v198, 16, v199
	v_and_b32_e32 v199, 0xffff0000, v199
	v_lshlrev_b32_e32 v210, 16, v196
	v_and_b32_e32 v211, 0xffff0000, v196
	v_lshlrev_b32_e32 v196, 16, v197
	v_and_b32_e32 v197, 0xffff0000, v197
	v_lshlrev_b32_e32 v214, 16, v200
	v_and_b32_e32 v215, 0xffff0000, v200
	v_lshlrev_b32_e32 v200, 16, v201
	v_and_b32_e32 v201, 0xffff0000, v201
	v_pk_fma_f32 v[128:129], v[206:207], v[194:195], v[128:129] op_sel_hi:[0,1,1]
	v_pk_fma_f32 v[126:127], v[206:207], v[208:209], v[126:127] op_sel_hi:[0,1,1]
	v_pk_fma_f32 v[120:121], v[206:207], v[198:199], v[120:121] op_sel_hi:[0,1,1]
	v_pk_fma_f32 v[194:195], v[206:207], v[212:213], v[118:119] op_sel_hi:[0,1,1]
	v_pk_fma_f32 v[124:125], v[206:207], v[196:197], v[124:125] op_sel_hi:[0,1,1]
	v_pk_fma_f32 v[122:123], v[206:207], v[210:211], v[122:123] op_sel_hi:[0,1,1]
	v_pk_fma_f32 v[196:197], v[206:207], v[200:201], v[116:117] op_sel_hi:[0,1,1]
	v_pk_fma_f32 v[198:199], v[206:207], v[214:215], v[114:115] op_sel_hi:[0,1,1]
	v_cvt_pk_bf16_f32 v116, v126, v127
	v_cvt_pk_bf16_f32 v117, v128, v129
	v_mul_f32_e32 v114, v127, v127
	v_mul_f32_e32 v115, v129, v129
	v_mul_f32_e32 v127, v195, v195
	v_mul_f32_e32 v129, v121, v121
	v_cvt_pk_bf16_f32 v118, v122, v123
	v_mul_f32_e32 v123, v123, v123
	v_mul_f32_e32 v200, v199, v199
	v_fmac_f32_e32 v114, v126, v126
	v_fmac_f32_e32 v115, v128, v128
	v_fmac_f32_e32 v127, v194, v194
	v_fmac_f32_e32 v129, v120, v120
	v_cvt_pk_bf16_f32 v119, v124, v125
	v_mul_f32_e32 v125, v125, v125
	v_mul_f32_e32 v201, v197, v197
	v_fmac_f32_e32 v123, v122, v122
	v_fmac_f32_e32 v200, v198, v198
	v_add_f32_e32 v114, v114, v115
	v_add_f32_e32 v115, v127, v129
	v_fmac_f32_e32 v125, v124, v124
	v_fmac_f32_e32 v201, v196, v196
	v_add_f32_e32 v114, v123, v114
	v_add_f32_e32 v115, v200, v115
	v_cndmask_b32_e32 v193, v192, v193, vcc
	v_add_f32_e32 v114, v125, v114
	v_add_f32_e32 v115, v201, v115
	v_add_f32_e32 v115, v114, v115
	v_lshlrev_b32_e32 v114, 2, v193
	ds_bpermute_b32 v124, v114, v115
	v_lshl_add_u64 v[122:123], s[20:21], 0, v[204:205]
	v_lshl_add_u64 v[122:123], v[122:123], 0, v[202:203]
	global_store_dwordx4 v[122:123], v[116:119], off sc1
	s_waitcnt lgkmcnt(0)
	s_nop 0
	v_add_f32_e32 v116, v115, v124
	v_xor_b32_e32 v115, 32, v192
	v_cmp_lt_i32_e32 vcc, v115, v207
	v_cvt_pk_bf16_f32 v118, v194, v195
	v_cvt_pk_bf16_f32 v119, v120, v121
	v_cvt_pk_bf16_f32 v120, v198, v199
	v_cvt_pk_bf16_f32 v121, v196, v197
	global_store_dwordx4 v[122:123], v[118:121], off offset:256 sc1
	s_nop 0
	v_cndmask_b32_e32 v115, v192, v115, vcc
	v_lshlrev_b32_e32 v115, 2, v115
	ds_bpermute_b32 v117, v115, v116
	s_and_saveexec_b64 s[40:41], s[6:7]
	s_cbranch_execz .LBB0_1552
	s_waitcnt lgkmcnt(0)
	v_add_f32_e32 v118, v116, v117
	s_lshl_b32 s54, s12, 2
	v_lshlrev_b64 v[116:117], 7, v[174:175]
	s_ashr_i32 s55, s54, 31
	v_lshl_add_u64 v[116:117], s[22:23], 0, v[116:117]
	v_lshl_add_u64 v[116:117], s[54:55], 2, v[116:117]
	s_lshl_b32 s14, s50, 2
	v_lshl_add_u64 v[116:117], v[116:117], 0, s[14:15]
	global_store_dword v[116:117], v118, off
.LBB0_1552:
	s_or_b64 exec, exec, s[40:41]
	v_lshlrev_b32_e32 v118, 16, v150
	v_and_b32_e32 v119, 0xffff0000, v150
	v_lshlrev_b32_e32 v120, 16, v151
	v_and_b32_e32 v121, 0xffff0000, v151
	v_lshlrev_b32_e32 v122, 16, v152
	v_and_b32_e32 v123, 0xffff0000, v152
	v_pk_fma_f32 v[110:111], v[188:189], v[118:119], v[110:111] op_sel_hi:[0,1,1]
	v_pk_fma_f32 v[112:113], v[188:189], v[120:121], v[112:113] op_sel_hi:[0,1,1]
	v_pk_fma_f32 v[120:121], v[188:189], v[122:123], v[106:107] op_sel_hi:[0,1,1]
	v_cvt_pk_bf16_f32 v106, v110, v111
	v_mul_f32_e32 v111, v111, v111
	v_fmac_f32_e32 v111, v110, v110
	v_mul_f32_e32 v110, v113, v113
	v_lshlrev_b32_e32 v126, 16, v146
	v_and_b32_e32 v127, 0xffff0000, v146
	v_lshlrev_b32_e32 v128, 16, v147
	v_and_b32_e32 v129, 0xffff0000, v147
	v_fmac_f32_e32 v110, v112, v112
	v_lshlrev_b32_e32 v124, 16, v153
	v_and_b32_e32 v125, 0xffff0000, v153
	v_lshlrev_b32_e32 v146, 16, v148
	v_and_b32_e32 v147, 0xffff0000, v148
	v_add_f32_e32 v110, v111, v110
	v_mul_f32_e32 v111, v121, v121
	v_pk_fma_f32 v[104:105], v[188:189], v[128:129], v[104:105] op_sel_hi:[0,1,1]
	v_pk_fma_f32 v[102:103], v[188:189], v[126:127], v[102:103] op_sel_hi:[0,1,1]
	v_pk_fma_f32 v[118:119], v[188:189], v[124:125], v[108:109] op_sel_hi:[0,1,1]
	v_cvt_pk_bf16_f32 v107, v112, v113
	v_fmac_f32_e32 v111, v120, v120
	v_pk_fma_f32 v[112:113], v[188:189], v[146:147], v[98:99] op_sel_hi:[0,1,1]
	v_mul_f32_e32 v98, v103, v103
	v_mul_f32_e32 v99, v105, v105
	v_add_f32_e32 v110, v111, v110
	v_mul_f32_e32 v111, v119, v119
	v_fmac_f32_e32 v98, v102, v102
	v_fmac_f32_e32 v99, v104, v104
	v_lshlrev_b32_e32 v148, 16, v149
	v_and_b32_e32 v149, 0xffff0000, v149
	v_fmac_f32_e32 v111, v118, v118
	v_add_f32_e32 v98, v98, v99
	v_mul_f32_e32 v99, v113, v113
	v_cvt_pk_bf16_f32 v108, v120, v121
	v_cvt_pk_bf16_f32 v109, v118, v119
	v_add_f32_e32 v118, v111, v110
	v_pk_fma_f32 v[110:111], v[188:189], v[148:149], v[100:101] op_sel_hi:[0,1,1]
	v_fmac_f32_e32 v99, v112, v112
	v_add_f32_e32 v98, v99, v98
	v_mul_f32_e32 v99, v111, v111
	v_fmac_f32_e32 v99, v110, v110
	v_add_f32_e32 v98, v99, v98
	v_add_f32_e32 v101, v118, v98
	ds_bpermute_b32 v118, v114, v101
	s_waitcnt lgkmcnt(1)
	v_lshlrev_b64 v[116:117], 11, v[186:187]
	v_lshl_add_u64 v[98:99], v[116:117], 1, s[20:21]
	v_lshl_add_u64 v[116:117], v[170:171], 1, v[98:99]
	global_store_dwordx4 v[116:117], v[106:109], off sc1
	s_waitcnt lgkmcnt(0)
	v_add_f32_e32 v98, v101, v118
	ds_bpermute_b32 v99, v115, v98
	v_cvt_pk_bf16_f32 v100, v102, v103
	v_cvt_pk_bf16_f32 v101, v104, v105
	v_cvt_pk_bf16_f32 v102, v112, v113
	v_cvt_pk_bf16_f32 v103, v110, v111
	global_store_dwordx4 v[116:117], v[100:103], off offset:256 sc1
	s_and_saveexec_b64 s[40:41], s[6:7]
	s_cbranch_execz .LBB0_1554
	s_waitcnt lgkmcnt(0)
	v_add_f32_e32 v100, v98, v99
	s_lshl_b32 s54, s12, 2
	v_lshlrev_b64 v[98:99], 7, v[186:187]
	s_ashr_i32 s55, s54, 31
	v_lshl_add_u64 v[98:99], s[22:23], 0, v[98:99]
	v_lshl_add_u64 v[98:99], s[54:55], 2, v[98:99]
	s_lshl_b32 s14, s50, 2
	v_lshl_add_u64 v[98:99], v[98:99], 0, s[14:15]
	global_store_dword v[98:99], v100, off
.LBB0_1554:
	s_or_b64 exec, exec, s[40:41]
	v_lshlrev_b32_e32 v100, 16, v142
	v_and_b32_e32 v101, 0xffff0000, v142
	v_lshlrev_b32_e32 v102, 16, v143
	v_and_b32_e32 v103, 0xffff0000, v143
	v_lshlrev_b32_e32 v104, 16, v144
	v_and_b32_e32 v105, 0xffff0000, v144
	v_pk_fma_f32 v[94:95], v[184:185], v[100:101], v[94:95] op_sel_hi:[0,1,1]
	v_pk_fma_f32 v[96:97], v[184:185], v[102:103], v[96:97] op_sel_hi:[0,1,1]
	v_pk_fma_f32 v[102:103], v[184:185], v[104:105], v[90:91] op_sel_hi:[0,1,1]
	v_cvt_pk_bf16_f32 v90, v94, v95
	v_mul_f32_e32 v95, v95, v95
	v_fmac_f32_e32 v95, v94, v94
	v_mul_f32_e32 v94, v97, v97
	v_lshlrev_b32_e32 v108, 16, v138
	v_and_b32_e32 v109, 0xffff0000, v138
	v_lshlrev_b32_e32 v110, 16, v139
	v_and_b32_e32 v111, 0xffff0000, v139
	v_fmac_f32_e32 v94, v96, v96
	v_lshlrev_b32_e32 v106, 16, v145
	v_and_b32_e32 v107, 0xffff0000, v145
	v_lshlrev_b32_e32 v112, 16, v140
	v_and_b32_e32 v113, 0xffff0000, v140
	v_add_f32_e32 v94, v95, v94
	v_mul_f32_e32 v95, v103, v103
	v_pk_fma_f32 v[88:89], v[184:185], v[110:111], v[88:89] op_sel_hi:[0,1,1]
	v_pk_fma_f32 v[86:87], v[184:185], v[108:109], v[86:87] op_sel_hi:[0,1,1]
	v_pk_fma_f32 v[100:101], v[184:185], v[106:107], v[92:93] op_sel_hi:[0,1,1]
	v_cvt_pk_bf16_f32 v91, v96, v97
	v_fmac_f32_e32 v95, v102, v102
	v_pk_fma_f32 v[96:97], v[184:185], v[112:113], v[82:83] op_sel_hi:[0,1,1]
	v_mul_f32_e32 v82, v87, v87
	v_mul_f32_e32 v83, v89, v89
	v_add_f32_e32 v94, v95, v94
	v_mul_f32_e32 v95, v101, v101
	v_fmac_f32_e32 v82, v86, v86
	v_fmac_f32_e32 v83, v88, v88
	v_lshlrev_b32_e32 v116, 16, v141
	v_and_b32_e32 v117, 0xffff0000, v141
	v_fmac_f32_e32 v95, v100, v100
	v_add_f32_e32 v82, v82, v83
	v_mul_f32_e32 v83, v97, v97
	v_cvt_pk_bf16_f32 v92, v102, v103
	v_cvt_pk_bf16_f32 v93, v100, v101
	v_add_f32_e32 v100, v95, v94
	v_pk_fma_f32 v[94:95], v[184:185], v[116:117], v[84:85] op_sel_hi:[0,1,1]
	v_fmac_f32_e32 v83, v96, v96
	v_add_f32_e32 v82, v83, v82
	v_mul_f32_e32 v83, v95, v95
	v_fmac_f32_e32 v83, v94, v94
	v_add_f32_e32 v82, v83, v82
	v_add_f32_e32 v85, v100, v82
	ds_bpermute_b32 v100, v114, v85
	s_waitcnt lgkmcnt(1)
	v_lshlrev_b64 v[98:99], 11, v[182:183]
	v_lshl_add_u64 v[82:83], v[98:99], 1, s[20:21]
	v_lshl_add_u64 v[98:99], v[170:171], 1, v[82:83]
	global_store_dwordx4 v[98:99], v[90:93], off sc1
	s_waitcnt lgkmcnt(0)
	v_add_f32_e32 v82, v85, v100
	ds_bpermute_b32 v83, v115, v82
	v_cvt_pk_bf16_f32 v84, v86, v87
	v_cvt_pk_bf16_f32 v85, v88, v89
	v_cvt_pk_bf16_f32 v86, v96, v97
	v_cvt_pk_bf16_f32 v87, v94, v95
	global_store_dwordx4 v[98:99], v[84:87], off offset:256 sc1
	s_and_saveexec_b64 s[40:41], s[6:7]
	s_cbranch_execz .LBB0_1556
	s_waitcnt lgkmcnt(0)
	v_add_f32_e32 v84, v82, v83
	s_lshl_b32 s54, s12, 2
	v_lshlrev_b64 v[82:83], 7, v[182:183]
	s_ashr_i32 s55, s54, 31
	v_lshl_add_u64 v[82:83], s[22:23], 0, v[82:83]
	v_lshl_add_u64 v[82:83], s[54:55], 2, v[82:83]
	s_lshl_b32 s14, s50, 2
	v_lshl_add_u64 v[82:83], v[82:83], 0, s[14:15]
	global_store_dword v[82:83], v84, off
.LBB0_1556:
	s_or_b64 exec, exec, s[40:41]
	v_lshlrev_b32_e32 v84, 16, v134
	v_and_b32_e32 v85, 0xffff0000, v134
	v_lshlrev_b32_e32 v86, 16, v135
	v_and_b32_e32 v87, 0xffff0000, v135
	v_lshlrev_b32_e32 v88, 16, v136
	v_and_b32_e32 v89, 0xffff0000, v136
	v_pk_fma_f32 v[78:79], v[180:181], v[84:85], v[78:79] op_sel_hi:[0,1,1]
	v_pk_fma_f32 v[80:81], v[180:181], v[86:87], v[80:81] op_sel_hi:[0,1,1]
	v_pk_fma_f32 v[86:87], v[180:181], v[88:89], v[74:75] op_sel_hi:[0,1,1]
	v_cvt_pk_bf16_f32 v74, v78, v79
	v_mul_f32_e32 v79, v79, v79
	v_fmac_f32_e32 v79, v78, v78
	v_mul_f32_e32 v78, v81, v81
	v_lshlrev_b32_e32 v92, 16, v130
	v_and_b32_e32 v93, 0xffff0000, v130
	v_lshlrev_b32_e32 v94, 16, v131
	v_and_b32_e32 v95, 0xffff0000, v131
	v_fmac_f32_e32 v78, v80, v80
	v_lshlrev_b32_e32 v90, 16, v137
	v_and_b32_e32 v91, 0xffff0000, v137
	v_lshlrev_b32_e32 v96, 16, v132
	v_and_b32_e32 v97, 0xffff0000, v132
	v_add_f32_e32 v78, v79, v78
	v_mul_f32_e32 v79, v87, v87
	v_pk_fma_f32 v[72:73], v[180:181], v[94:95], v[72:73] op_sel_hi:[0,1,1]
	v_pk_fma_f32 v[70:71], v[180:181], v[92:93], v[70:71] op_sel_hi:[0,1,1]
	v_pk_fma_f32 v[84:85], v[180:181], v[90:91], v[76:77] op_sel_hi:[0,1,1]
	v_cvt_pk_bf16_f32 v75, v80, v81
	v_fmac_f32_e32 v79, v86, v86
	v_pk_fma_f32 v[80:81], v[180:181], v[96:97], v[66:67] op_sel_hi:[0,1,1]
	v_mul_f32_e32 v66, v71, v71
	v_mul_f32_e32 v67, v73, v73
	v_add_f32_e32 v78, v79, v78
	v_mul_f32_e32 v79, v85, v85
	v_fmac_f32_e32 v66, v70, v70
	v_fmac_f32_e32 v67, v72, v72
	v_lshlrev_b32_e32 v98, 16, v133
	v_and_b32_e32 v99, 0xffff0000, v133
	v_fmac_f32_e32 v79, v84, v84
	v_add_f32_e32 v66, v66, v67
	v_mul_f32_e32 v67, v81, v81
	v_cvt_pk_bf16_f32 v76, v86, v87
	v_cvt_pk_bf16_f32 v77, v84, v85
	v_add_f32_e32 v84, v79, v78
	v_pk_fma_f32 v[78:79], v[180:181], v[98:99], v[68:69] op_sel_hi:[0,1,1]
	v_fmac_f32_e32 v67, v80, v80
	v_add_f32_e32 v66, v67, v66
	v_mul_f32_e32 v67, v79, v79
	v_fmac_f32_e32 v67, v78, v78
	v_add_f32_e32 v66, v67, v66
	v_add_f32_e32 v69, v84, v66
	ds_bpermute_b32 v84, v114, v69
	s_waitcnt lgkmcnt(1)
	v_lshlrev_b64 v[82:83], 11, v[178:179]
	v_lshl_add_u64 v[66:67], v[82:83], 1, s[20:21]
	v_lshl_add_u64 v[82:83], v[170:171], 1, v[66:67]
	global_store_dwordx4 v[82:83], v[74:77], off sc1
	s_waitcnt lgkmcnt(0)
	v_add_f32_e32 v66, v69, v84
	ds_bpermute_b32 v67, v115, v66
	v_cvt_pk_bf16_f32 v68, v70, v71
	v_cvt_pk_bf16_f32 v69, v72, v73
	v_cvt_pk_bf16_f32 v70, v80, v81
	v_cvt_pk_bf16_f32 v71, v78, v79
	global_store_dwordx4 v[82:83], v[68:71], off offset:256 sc1
	s_and_saveexec_b64 s[40:41], s[6:7]
	s_cbranch_execz .LBB0_1558
	s_waitcnt lgkmcnt(0)
	v_add_f32_e32 v68, v66, v67
	s_lshl_b32 s54, s12, 2
	v_lshlrev_b64 v[66:67], 7, v[178:179]
	s_ashr_i32 s55, s54, 31
	v_lshl_add_u64 v[66:67], s[22:23], 0, v[66:67]
	v_lshl_add_u64 v[66:67], s[54:55], 2, v[66:67]
	s_lshl_b32 s14, s50, 2
	v_lshl_add_u64 v[66:67], v[66:67], 0, s[14:15]
	global_store_dword v[66:67], v68, off
.LBB0_1558:
	s_or_b64 exec, exec, s[40:41]
	v_add_u32_e32 v102, 0x80, v174
	v_ashrrev_i32_e32 v103, 31, v102
	v_lshlrev_b64 v[112:113], 12, v[102:103]
	s_waitcnt lgkmcnt(0)
	v_lshl_add_u64 v[66:67], v[172:173], 0, v[112:113]
	global_load_dwordx4 v[104:107], v[66:67], off
	global_load_dwordx4 v[108:111], v[66:67], off offset:256
	global_load_dword v116, v[176:177], off offset:512
	v_add_u32_e32 v98, 0x90, v174
	v_add_u32_e32 v94, 0xa0, v174
	v_add_u32_e32 v90, 0xb0, v174
	v_ashrrev_i32_e32 v99, 31, v98
	v_ashrrev_i32_e32 v95, 31, v94
	v_ashrrev_i32_e32 v91, 31, v90
	v_lshlrev_b64 v[66:67], 12, v[98:99]
	v_lshlrev_b64 v[68:69], 12, v[94:95]
	v_lshlrev_b64 v[70:71], 12, v[90:91]
	v_lshl_add_u64 v[66:67], v[172:173], 0, v[66:67]
	v_lshl_add_u64 v[68:69], v[172:173], 0, v[68:69]
	global_load_dword v100, v[176:177], off offset:576
	global_load_dword v96, v[176:177], off offset:640
	global_load_dword v92, v[176:177], off offset:704
	v_lshl_add_u64 v[118:119], v[172:173], 0, v[70:71]
	global_load_dwordx4 v[86:89], v[66:67], off
	global_load_dwordx4 v[82:85], v[66:67], off offset:256
	global_load_dwordx4 v[78:81], v[68:69], off
	global_load_dwordx4 v[74:77], v[68:69], off offset:256
	global_load_dwordx4 v[70:73], v[118:119], off
	s_nop 0
	global_load_dwordx4 v[66:69], v[118:119], off offset:256
	s_waitcnt vmcnt(11)
	v_lshlrev_b32_e32 v118, 16, v104
	v_and_b32_e32 v119, 0xffff0000, v104
	v_lshlrev_b32_e32 v104, 16, v105
	v_and_b32_e32 v105, 0xffff0000, v105
	s_waitcnt vmcnt(10)
	v_lshlrev_b32_e32 v122, 16, v108
	v_and_b32_e32 v123, 0xffff0000, v108
	v_lshlrev_b32_e32 v108, 16, v109
	v_and_b32_e32 v109, 0xffff0000, v109
	v_lshlrev_b32_e32 v120, 16, v106
	v_and_b32_e32 v121, 0xffff0000, v106
	v_lshlrev_b32_e32 v106, 16, v107
	v_and_b32_e32 v107, 0xffff0000, v107
	v_lshlrev_b32_e32 v124, 16, v110
	v_and_b32_e32 v125, 0xffff0000, v110
	s_waitcnt vmcnt(9)
	v_pk_fma_f32 v[64:65], v[116:117], v[104:105], v[64:65] op_sel_hi:[0,1,1]
	v_pk_fma_f32 v[62:63], v[116:117], v[118:119], v[62:63] op_sel_hi:[0,1,1]
	v_pk_fma_f32 v[56:57], v[116:117], v[108:109], v[56:57] op_sel_hi:[0,1,1]
	v_pk_fma_f32 v[54:55], v[116:117], v[122:123], v[54:55] op_sel_hi:[0,1,1]
	v_lshlrev_b32_e32 v110, 16, v111
	v_and_b32_e32 v111, 0xffff0000, v111
	v_pk_fma_f32 v[60:61], v[116:117], v[106:107], v[60:61] op_sel_hi:[0,1,1]
	v_pk_fma_f32 v[58:59], v[116:117], v[120:121], v[58:59] op_sel_hi:[0,1,1]
	v_pk_fma_f32 v[106:107], v[116:117], v[124:125], v[50:51] op_sel_hi:[0,1,1]
	v_cvt_pk_bf16_f32 v50, v62, v63
	v_cvt_pk_bf16_f32 v51, v64, v65
	v_mul_f32_e32 v63, v63, v63
	v_mul_f32_e32 v65, v65, v65
	v_mul_f32_e32 v93, v55, v55
	v_mul_f32_e32 v97, v57, v57
	v_pk_fma_f32 v[104:105], v[116:117], v[110:111], v[52:53] op_sel_hi:[0,1,1]
	v_cvt_pk_bf16_f32 v52, v58, v59
	v_cvt_pk_bf16_f32 v53, v60, v61
	v_mul_f32_e32 v59, v59, v59
	v_mul_f32_e32 v61, v61, v61
	v_mul_f32_e32 v101, v107, v107
	v_fmac_f32_e32 v63, v62, v62
	v_fmac_f32_e32 v65, v64, v64
	v_fmac_f32_e32 v93, v54, v54
	v_fmac_f32_e32 v97, v56, v56
	v_mul_f32_e32 v108, v105, v105
	v_fmac_f32_e32 v59, v58, v58
	v_fmac_f32_e32 v61, v60, v60
	v_fmac_f32_e32 v101, v106, v106
	v_add_f32_e32 v58, v63, v65
	v_add_f32_e32 v60, v93, v97
	v_fmac_f32_e32 v108, v104, v104
	v_add_f32_e32 v58, v59, v58
	v_add_f32_e32 v59, v101, v60
	v_add_f32_e32 v58, v61, v58
	v_add_f32_e32 v59, v108, v59
	v_add_f32_e32 v60, v58, v59
	ds_bpermute_b32 v61, v114, v60
	v_lshl_add_u64 v[58:59], s[20:21], 0, v[112:113]
	v_lshl_add_u64 v[58:59], v[170:171], 1, v[58:59]
	global_store_dwordx4 v[58:59], v[50:53], off sc1
	s_waitcnt lgkmcnt(0)
	s_nop 0
	v_add_f32_e32 v50, v60, v61
	ds_bpermute_b32 v51, v115, v50
	v_cvt_pk_bf16_f32 v52, v54, v55
	v_cvt_pk_bf16_f32 v53, v56, v57
	v_cvt_pk_bf16_f32 v54, v106, v107
	v_cvt_pk_bf16_f32 v55, v104, v105
	global_store_dwordx4 v[58:59], v[52:55], off offset:256 sc1
	s_and_saveexec_b64 s[40:41], s[6:7]
	s_cbranch_execz .LBB0_1560
	s_waitcnt lgkmcnt(0)
	v_add_f32_e32 v52, v50, v51
	s_lshl_b32 s54, s12, 2
	v_lshlrev_b64 v[50:51], 7, v[102:103]
	s_ashr_i32 s55, s54, 31
	v_lshl_add_u64 v[50:51], s[22:23], 0, v[50:51]
	v_lshl_add_u64 v[50:51], s[54:55], 2, v[50:51]
	s_lshl_b32 s14, s50, 2
	v_lshl_add_u64 v[50:51], v[50:51], 0, s[14:15]
	global_store_dword v[50:51], v52, off
.LBB0_1560:
	s_or_b64 exec, exec, s[40:41]
	s_waitcnt vmcnt(7)
	v_lshlrev_b32_e32 v52, 16, v86
	v_and_b32_e32 v53, 0xffff0000, v86
	v_lshlrev_b32_e32 v54, 16, v87
	v_and_b32_e32 v55, 0xffff0000, v87
	v_lshlrev_b32_e32 v56, 16, v88
	v_and_b32_e32 v57, 0xffff0000, v88
	v_pk_fma_f32 v[46:47], v[100:101], v[52:53], v[46:47] op_sel_hi:[0,1,1]
	v_pk_fma_f32 v[48:49], v[100:101], v[54:55], v[48:49] op_sel_hi:[0,1,1]
	v_pk_fma_f32 v[54:55], v[100:101], v[56:57], v[42:43] op_sel_hi:[0,1,1]
	v_cvt_pk_bf16_f32 v42, v46, v47
	v_mul_f32_e32 v47, v47, v47
	v_fmac_f32_e32 v47, v46, v46
	v_mul_f32_e32 v46, v49, v49
	s_waitcnt vmcnt(6)
	v_lshlrev_b32_e32 v60, 16, v82
	v_and_b32_e32 v61, 0xffff0000, v82
	v_lshlrev_b32_e32 v62, 16, v83
	v_and_b32_e32 v63, 0xffff0000, v83
	v_fmac_f32_e32 v46, v48, v48
	v_lshlrev_b32_e32 v58, 16, v89
	v_and_b32_e32 v59, 0xffff0000, v89
	v_lshlrev_b32_e32 v64, 16, v84
	v_and_b32_e32 v65, 0xffff0000, v84
	v_add_f32_e32 v46, v47, v46
	v_mul_f32_e32 v47, v55, v55
	v_pk_fma_f32 v[40:41], v[100:101], v[62:63], v[40:41] op_sel_hi:[0,1,1]
	v_pk_fma_f32 v[38:39], v[100:101], v[60:61], v[38:39] op_sel_hi:[0,1,1]
	v_pk_fma_f32 v[52:53], v[100:101], v[58:59], v[44:45] op_sel_hi:[0,1,1]
	v_cvt_pk_bf16_f32 v43, v48, v49
	v_fmac_f32_e32 v47, v54, v54
	v_pk_fma_f32 v[48:49], v[100:101], v[64:65], v[34:35] op_sel_hi:[0,1,1]
	v_mul_f32_e32 v34, v39, v39
	v_mul_f32_e32 v35, v41, v41
	v_add_f32_e32 v46, v47, v46
	v_mul_f32_e32 v47, v53, v53
	v_fmac_f32_e32 v34, v38, v38
	v_fmac_f32_e32 v35, v40, v40
	v_lshlrev_b32_e32 v82, 16, v85
	v_and_b32_e32 v83, 0xffff0000, v85
	v_fmac_f32_e32 v47, v52, v52
	v_add_f32_e32 v34, v34, v35
	v_mul_f32_e32 v35, v49, v49
	v_cvt_pk_bf16_f32 v44, v54, v55
	v_cvt_pk_bf16_f32 v45, v52, v53
	v_add_f32_e32 v52, v47, v46
	v_pk_fma_f32 v[46:47], v[100:101], v[82:83], v[36:37] op_sel_hi:[0,1,1]
	v_fmac_f32_e32 v35, v48, v48
	v_add_f32_e32 v34, v35, v34
	v_mul_f32_e32 v35, v47, v47
	v_fmac_f32_e32 v35, v46, v46
	v_add_f32_e32 v34, v35, v34
	v_add_f32_e32 v37, v52, v34
	ds_bpermute_b32 v52, v114, v37
	s_waitcnt lgkmcnt(1)
	v_lshlrev_b64 v[50:51], 11, v[98:99]
	v_lshl_add_u64 v[34:35], v[50:51], 1, s[20:21]
	v_lshl_add_u64 v[50:51], v[170:171], 1, v[34:35]
	global_store_dwordx4 v[50:51], v[42:45], off sc1
	s_waitcnt lgkmcnt(0)
	v_add_f32_e32 v34, v37, v52
	ds_bpermute_b32 v35, v115, v34
	v_cvt_pk_bf16_f32 v36, v38, v39
	v_cvt_pk_bf16_f32 v37, v40, v41
	v_cvt_pk_bf16_f32 v38, v48, v49
	v_cvt_pk_bf16_f32 v39, v46, v47
	global_store_dwordx4 v[50:51], v[36:39], off offset:256 sc1
	s_and_saveexec_b64 s[40:41], s[6:7]
	s_cbranch_execz .LBB0_1562
	s_waitcnt lgkmcnt(0)
	v_add_f32_e32 v36, v34, v35
	s_lshl_b32 s54, s12, 2
	v_lshlrev_b64 v[34:35], 7, v[98:99]
	s_ashr_i32 s55, s54, 31
	v_lshl_add_u64 v[34:35], s[22:23], 0, v[34:35]
	v_lshl_add_u64 v[34:35], s[54:55], 2, v[34:35]
	s_lshl_b32 s14, s50, 2
	v_lshl_add_u64 v[34:35], v[34:35], 0, s[14:15]
	global_store_dword v[34:35], v36, off
.LBB0_1562:
	s_or_b64 exec, exec, s[40:41]
	s_waitcnt vmcnt(7)
	v_lshlrev_b32_e32 v36, 16, v78
	v_and_b32_e32 v37, 0xffff0000, v78
	v_lshlrev_b32_e32 v38, 16, v79
	v_and_b32_e32 v39, 0xffff0000, v79
	v_lshlrev_b32_e32 v40, 16, v80
	v_and_b32_e32 v41, 0xffff0000, v80
	v_pk_fma_f32 v[30:31], v[96:97], v[36:37], v[30:31] op_sel_hi:[0,1,1]
	v_pk_fma_f32 v[32:33], v[96:97], v[38:39], v[32:33] op_sel_hi:[0,1,1]
	v_pk_fma_f32 v[38:39], v[96:97], v[40:41], v[26:27] op_sel_hi:[0,1,1]
	v_cvt_pk_bf16_f32 v26, v30, v31
	v_mul_f32_e32 v31, v31, v31
	v_fmac_f32_e32 v31, v30, v30
	v_mul_f32_e32 v30, v33, v33
	s_waitcnt vmcnt(6)
	v_lshlrev_b32_e32 v44, 16, v74
	v_and_b32_e32 v45, 0xffff0000, v74
	v_lshlrev_b32_e32 v46, 16, v75
	v_and_b32_e32 v47, 0xffff0000, v75
	v_fmac_f32_e32 v30, v32, v32
	v_lshlrev_b32_e32 v42, 16, v81
	v_and_b32_e32 v43, 0xffff0000, v81
	v_lshlrev_b32_e32 v48, 16, v76
	v_and_b32_e32 v49, 0xffff0000, v76
	v_add_f32_e32 v30, v31, v30
	v_mul_f32_e32 v31, v39, v39
	v_pk_fma_f32 v[24:25], v[96:97], v[46:47], v[24:25] op_sel_hi:[0,1,1]
	v_pk_fma_f32 v[22:23], v[96:97], v[44:45], v[22:23] op_sel_hi:[0,1,1]
	v_pk_fma_f32 v[36:37], v[96:97], v[42:43], v[28:29] op_sel_hi:[0,1,1]
	v_cvt_pk_bf16_f32 v27, v32, v33
	v_fmac_f32_e32 v31, v38, v38
	v_pk_fma_f32 v[32:33], v[96:97], v[48:49], v[18:19] op_sel_hi:[0,1,1]
	v_mul_f32_e32 v18, v23, v23
	v_mul_f32_e32 v19, v25, v25
	v_add_f32_e32 v30, v31, v30
	v_mul_f32_e32 v31, v37, v37
	v_fmac_f32_e32 v18, v22, v22
	v_fmac_f32_e32 v19, v24, v24
	v_lshlrev_b32_e32 v50, 16, v77
	v_and_b32_e32 v51, 0xffff0000, v77
	v_fmac_f32_e32 v31, v36, v36
	v_add_f32_e32 v18, v18, v19
	v_mul_f32_e32 v19, v33, v33
	v_cvt_pk_bf16_f32 v28, v38, v39
	v_cvt_pk_bf16_f32 v29, v36, v37
	v_add_f32_e32 v36, v31, v30
	v_pk_fma_f32 v[30:31], v[96:97], v[50:51], v[20:21] op_sel_hi:[0,1,1]
	v_fmac_f32_e32 v19, v32, v32
	v_add_f32_e32 v18, v19, v18
	v_mul_f32_e32 v19, v31, v31
	v_fmac_f32_e32 v19, v30, v30
	v_add_f32_e32 v18, v19, v18
	v_add_f32_e32 v21, v36, v18
	ds_bpermute_b32 v36, v114, v21
	s_waitcnt lgkmcnt(1)
	v_lshlrev_b64 v[34:35], 11, v[94:95]
	v_lshl_add_u64 v[18:19], v[34:35], 1, s[20:21]
	v_lshl_add_u64 v[34:35], v[170:171], 1, v[18:19]
	global_store_dwordx4 v[34:35], v[26:29], off sc1
	s_waitcnt lgkmcnt(0)
	v_add_f32_e32 v18, v21, v36
	ds_bpermute_b32 v19, v115, v18
	v_cvt_pk_bf16_f32 v20, v22, v23
	v_cvt_pk_bf16_f32 v21, v24, v25
	v_cvt_pk_bf16_f32 v22, v32, v33
	v_cvt_pk_bf16_f32 v23, v30, v31
	global_store_dwordx4 v[34:35], v[20:23], off offset:256 sc1
	s_and_saveexec_b64 s[40:41], s[6:7]
	s_cbranch_execz .LBB0_1564
	s_waitcnt lgkmcnt(0)
	v_add_f32_e32 v20, v18, v19
	s_lshl_b32 s54, s12, 2
	v_lshlrev_b64 v[18:19], 7, v[94:95]
	s_ashr_i32 s55, s54, 31
	v_lshl_add_u64 v[18:19], s[22:23], 0, v[18:19]
	v_lshl_add_u64 v[18:19], s[54:55], 2, v[18:19]
	s_lshl_b32 s14, s50, 2
	v_lshl_add_u64 v[18:19], v[18:19], 0, s[14:15]
	global_store_dword v[18:19], v20, off
.LBB0_1564:
	s_or_b64 exec, exec, s[40:41]
	s_waitcnt vmcnt(7)
	v_lshlrev_b32_e32 v20, 16, v70
	v_and_b32_e32 v21, 0xffff0000, v70
	v_lshlrev_b32_e32 v22, 16, v71
	v_and_b32_e32 v23, 0xffff0000, v71
	v_lshlrev_b32_e32 v24, 16, v72
	v_and_b32_e32 v25, 0xffff0000, v72
	v_pk_fma_f32 v[14:15], v[92:93], v[20:21], v[14:15] op_sel_hi:[0,1,1]
	v_pk_fma_f32 v[16:17], v[92:93], v[22:23], v[16:17] op_sel_hi:[0,1,1]
	v_pk_fma_f32 v[22:23], v[92:93], v[24:25], v[10:11] op_sel_hi:[0,1,1]
	v_cvt_pk_bf16_f32 v10, v14, v15
	v_mul_f32_e32 v15, v15, v15
	v_fmac_f32_e32 v15, v14, v14
	v_mul_f32_e32 v14, v17, v17
	s_waitcnt vmcnt(6)
	v_lshlrev_b32_e32 v28, 16, v66
	v_and_b32_e32 v29, 0xffff0000, v66
	v_lshlrev_b32_e32 v30, 16, v67
	v_and_b32_e32 v31, 0xffff0000, v67
	v_fmac_f32_e32 v14, v16, v16
	v_lshlrev_b32_e32 v26, 16, v73
	v_and_b32_e32 v27, 0xffff0000, v73
	v_lshlrev_b32_e32 v32, 16, v68
	v_and_b32_e32 v33, 0xffff0000, v68
	v_add_f32_e32 v14, v15, v14
	v_mul_f32_e32 v15, v23, v23
	v_pk_fma_f32 v[8:9], v[92:93], v[30:31], v[8:9] op_sel_hi:[0,1,1]
	v_pk_fma_f32 v[6:7], v[92:93], v[28:29], v[6:7] op_sel_hi:[0,1,1]
	v_pk_fma_f32 v[20:21], v[92:93], v[26:27], v[12:13] op_sel_hi:[0,1,1]
	v_cvt_pk_bf16_f32 v11, v16, v17
	v_fmac_f32_e32 v15, v22, v22
	v_pk_fma_f32 v[16:17], v[92:93], v[32:33], v[2:3] op_sel_hi:[0,1,1]
	v_mul_f32_e32 v2, v7, v7
	v_mul_f32_e32 v3, v9, v9
	v_add_f32_e32 v14, v15, v14
	v_mul_f32_e32 v15, v21, v21
	v_fmac_f32_e32 v2, v6, v6
	v_fmac_f32_e32 v3, v8, v8
	v_lshlrev_b32_e32 v34, 16, v69
	v_and_b32_e32 v35, 0xffff0000, v69
	v_fmac_f32_e32 v15, v20, v20
	v_add_f32_e32 v2, v2, v3
	v_mul_f32_e32 v3, v17, v17
	v_cvt_pk_bf16_f32 v12, v22, v23
	v_cvt_pk_bf16_f32 v13, v20, v21
	v_add_f32_e32 v20, v15, v14
	v_pk_fma_f32 v[14:15], v[92:93], v[34:35], v[4:5] op_sel_hi:[0,1,1]
	v_fmac_f32_e32 v3, v16, v16
	v_add_f32_e32 v2, v3, v2
	v_mul_f32_e32 v3, v15, v15
	v_fmac_f32_e32 v3, v14, v14
	v_add_f32_e32 v2, v3, v2
	v_add_f32_e32 v5, v20, v2
	ds_bpermute_b32 v20, v114, v5
	s_waitcnt lgkmcnt(1)
	v_lshlrev_b64 v[18:19], 11, v[90:91]
	v_lshl_add_u64 v[2:3], v[18:19], 1, s[20:21]
	v_lshl_add_u64 v[18:19], v[170:171], 1, v[2:3]
	global_store_dwordx4 v[18:19], v[10:13], off sc1
	s_waitcnt lgkmcnt(0)
	v_add_f32_e32 v2, v5, v20
	ds_bpermute_b32 v3, v115, v2
	v_cvt_pk_bf16_f32 v4, v6, v7
	v_cvt_pk_bf16_f32 v5, v8, v9
	v_cvt_pk_bf16_f32 v6, v16, v17
	v_cvt_pk_bf16_f32 v7, v14, v15
	global_store_dwordx4 v[18:19], v[4:7], off offset:256 sc1
	s_and_saveexec_b64 s[40:41], s[6:7]
	s_cbranch_execz .LBB0_1566
	s_waitcnt lgkmcnt(0)
	v_add_f32_e32 v4, v2, v3
	s_lshl_b32 s54, s12, 2
	v_lshlrev_b64 v[2:3], 7, v[90:91]
	s_ashr_i32 s55, s54, 31
	v_lshl_add_u64 v[2:3], s[22:23], 0, v[2:3]
	v_lshl_add_u64 v[2:3], s[54:55], 2, v[2:3]
	s_lshl_b32 s14, s50, 2
	v_lshl_add_u64 v[2:3], v[2:3], 0, s[14:15]
	global_store_dword v[2:3], v4, off

.LBB0_2051:
	s_add_u32 s8, s16, s0
	v_lshl_add_u64 v[10:11], s[16:17], 0, v[6:7]
	s_addc_u32 s9, s17, s1
	v_add_co_u32_e32 v10, vcc, s11, v10
	v_mov_b32_e32 v9, v1
	s_nop 0
	v_addc_co_u32_e32 v11, vcc, 0, v11, vcc
	global_load_dword v0, v12, s[8:9]
	global_load_dword v8, v13, s[8:9]
	global_load_dword v17, v14, s[8:9]
	global_load_dword v34, v15, s[8:9]
	global_load_dwordx2 v[18:19], v[10:11], off
	global_load_dwordx2 v[20:21], v[10:11], off offset:512
	global_load_dwordx2 v[22:23], v[10:11], off offset:1024
	global_load_dwordx2 v[24:25], v[10:11], off offset:1536
	global_load_dwordx2 v[26:27], v[10:11], off offset:2048
	global_load_dwordx2 v[28:29], v[10:11], off offset:2560
	global_load_dwordx2 v[30:31], v[10:11], off offset:3072
	global_load_dwordx2 v[32:33], v[10:11], off offset:3584
	s_add_i32 s94, s94, s92
	s_add_u32 s0, s0, s2
	s_addc_u32 s1, s1, s3
	v_lshl_add_u64 v[6:7], v[6:7], 0, s[6:7]
	s_cmp_lt_i32 s94, 0x8000
	s_waitcnt vmcnt(11)
	v_lshlrev_b32_sdwa v11, v16, v0 dst_sel:DWORD dst_unused:UNUSED_PAD src0_sel:DWORD src1_sel:BYTE_3
	s_waitcnt vmcnt(10)
	v_lshlrev_b32_sdwa v35, v16, v8 dst_sel:DWORD dst_unused:UNUSED_PAD src0_sel:DWORD src1_sel:BYTE_3
	s_waitcnt vmcnt(9)
	v_mul_f32_e32 v10, 0x3d000000, v17
	v_add_u32_e32 v11, s10, v11
	v_add_u32_e32 v17, s10, v35
	ds_read_b32 v11, v11
	ds_read_b32 v17, v17
	v_and_b32_e32 v0, 0xffffff, v0
	v_and_b32_e32 v8, 0xffffff, v8
	s_waitcnt vmcnt(8)
	v_mul_f32_e32 v44, 0x3d000000, v34
	s_waitcnt lgkmcnt(1)
	v_add_u32_e32 v0, v11, v0
	s_waitcnt lgkmcnt(0)
	v_add_u32_e32 v8, v17, v8
	v_lshlrev_b64 v[68:69], 11, v[0:1]
	v_lshlrev_b64 v[8:9], 11, v[8:9]
	v_lshl_add_u64 v[68:69], v[2:3], 0, v[68:69]
	v_lshl_add_u64 v[8:9], v[2:3], 0, v[8:9]
	global_load_dword v0, v[68:69], off
	global_load_dword v11, v[8:9], off
	global_load_dword v17, v[68:69], off offset:256
	global_load_dword v35, v[8:9], off offset:256
	global_load_dword v36, v[68:69], off offset:512
	global_load_dword v39, v[8:9], off offset:512
	global_load_dword v40, v[68:69], off offset:768
	global_load_dword v43, v[8:9], off offset:768
	global_load_dword v45, v[68:69], off offset:1024
	global_load_dword v46, v[8:9], off offset:1024
	global_load_dword v49, v[68:69], off offset:1280
	global_load_dword v50, v[8:9], off offset:1280
	global_load_dword v53, v[68:69], off offset:1536
	global_load_dword v54, v[8:9], off offset:1536
	global_load_dword v57, v[68:69], off offset:1792
	global_load_dword v58, v[8:9], off offset:1792
	s_waitcnt vmcnt(23)
	v_lshlrev_b32_e32 v34, 16, v18
	v_and_b32_e32 v37, 0xffff0000, v18
	v_lshlrev_b32_e32 v18, 16, v19
	v_and_b32_e32 v19, 0xffff0000, v19
	s_waitcnt vmcnt(22)
	v_lshlrev_b32_e32 v38, 16, v20
	v_and_b32_e32 v41, 0xffff0000, v20
	v_lshlrev_b32_e32 v20, 16, v21
	v_and_b32_e32 v21, 0xffff0000, v21
	s_waitcnt vmcnt(21)
	v_lshlrev_b32_e32 v42, 16, v22
	v_and_b32_e32 v47, 0xffff0000, v22
	v_lshlrev_b32_e32 v22, 16, v23
	v_and_b32_e32 v23, 0xffff0000, v23
	s_waitcnt vmcnt(20)
	v_lshlrev_b32_e32 v48, 16, v24
	v_and_b32_e32 v51, 0xffff0000, v24
	v_lshlrev_b32_e32 v24, 16, v25
	v_and_b32_e32 v25, 0xffff0000, v25
	s_waitcnt vmcnt(19)
	v_lshlrev_b32_e32 v52, 16, v26
	v_and_b32_e32 v55, 0xffff0000, v26
	v_lshlrev_b32_e32 v26, 16, v27
	v_and_b32_e32 v27, 0xffff0000, v27
	s_waitcnt vmcnt(18)
	v_lshlrev_b32_e32 v56, 16, v28
	v_and_b32_e32 v59, 0xffff0000, v28
	v_lshlrev_b32_e32 v28, 16, v29
	v_and_b32_e32 v29, 0xffff0000, v29
	s_waitcnt vmcnt(17)
	v_lshlrev_b32_e32 v60, 16, v30
	v_and_b32_e32 v63, 0xffff0000, v30
	v_lshlrev_b32_e32 v30, 16, v31
	v_and_b32_e32 v31, 0xffff0000, v31
	s_waitcnt vmcnt(16)
	v_lshlrev_b32_e32 v64, 16, v32
	v_and_b32_e32 v67, 0xffff0000, v32
	v_lshlrev_b32_e32 v32, 16, v33
	v_and_b32_e32 v33, 0xffff0000, v33
	s_waitcnt vmcnt(15)
	v_cvt_f32_fp8_e32 v61, v0
	s_waitcnt vmcnt(14)
	v_cvt_f32_fp8_e32 v62, v11
	v_cvt_f32_fp8_sdwa v65, v0 src0_sel:BYTE_1
	v_cvt_f32_fp8_sdwa v66, v11 src0_sel:BYTE_1
	v_cvt_f32_fp8_sdwa v8, v0 src0_sel:BYTE_2
	v_cvt_f32_fp8_sdwa v68, v11 src0_sel:BYTE_2
	v_cvt_f32_fp8_sdwa v9, v0 src0_sel:BYTE_3
	v_cvt_f32_fp8_sdwa v69, v11 src0_sel:BYTE_3
	s_waitcnt vmcnt(12)
	v_cvt_f32_fp8_e32 v11, v35
	v_cvt_f32_fp8_e32 v0, v17
	v_cvt_f32_fp8_sdwa v98, v17 src0_sel:BYTE_1
	v_cvt_f32_fp8_sdwa v99, v35 src0_sel:BYTE_1
	v_cvt_f32_fp8_sdwa v70, v17 src0_sel:BYTE_2
	v_cvt_f32_fp8_sdwa v71, v17 src0_sel:BYTE_3
	s_waitcnt vmcnt(11)
	v_cvt_f32_fp8_e32 v17, v36
	s_waitcnt vmcnt(10)
	v_cvt_f32_fp8_e32 v100, v39
	v_cvt_f32_fp8_sdwa v101, v36 src0_sel:BYTE_1
	v_cvt_f32_fp8_sdwa v102, v39 src0_sel:BYTE_1
	v_cvt_f32_fp8_sdwa v74, v36 src0_sel:BYTE_2
	v_cvt_f32_fp8_sdwa v75, v36 src0_sel:BYTE_3
	s_waitcnt vmcnt(9)
	v_cvt_f32_fp8_e32 v103, v40
	s_waitcnt vmcnt(8)
	v_cvt_f32_fp8_e32 v104, v43
	v_cvt_f32_fp8_sdwa v105, v40 src0_sel:BYTE_1
	v_cvt_f32_fp8_sdwa v106, v43 src0_sel:BYTE_1
	v_cvt_f32_fp8_sdwa v78, v40 src0_sel:BYTE_2
	v_cvt_f32_fp8_sdwa v79, v40 src0_sel:BYTE_3
	s_waitcnt vmcnt(7)
	v_cvt_f32_fp8_e32 v107, v45
	s_waitcnt vmcnt(6)
	v_cvt_f32_fp8_e32 v108, v46
	v_cvt_f32_fp8_sdwa v109, v45 src0_sel:BYTE_1
	v_cvt_f32_fp8_sdwa v110, v46 src0_sel:BYTE_1
	v_cvt_f32_fp8_sdwa v82, v45 src0_sel:BYTE_2
	v_cvt_f32_fp8_sdwa v83, v45 src0_sel:BYTE_3
	s_waitcnt vmcnt(5)
	v_cvt_f32_fp8_e32 v45, v49
	s_waitcnt vmcnt(4)
	v_cvt_f32_fp8_e32 v111, v50
	v_cvt_f32_fp8_sdwa v112, v49 src0_sel:BYTE_1
	v_cvt_f32_fp8_sdwa v113, v50 src0_sel:BYTE_1
	v_cvt_f32_fp8_sdwa v86, v49 src0_sel:BYTE_2
	v_cvt_f32_fp8_sdwa v87, v49 src0_sel:BYTE_3
	s_waitcnt vmcnt(3)
	v_cvt_f32_fp8_e32 v114, v53
	s_waitcnt vmcnt(2)
	v_cvt_f32_fp8_e32 v115, v54
	v_cvt_f32_fp8_sdwa v116, v53 src0_sel:BYTE_1
	v_cvt_f32_fp8_sdwa v117, v54 src0_sel:BYTE_1
	v_cvt_f32_fp8_sdwa v90, v53 src0_sel:BYTE_2
	v_cvt_f32_fp8_sdwa v91, v53 src0_sel:BYTE_3
	s_waitcnt vmcnt(1)
	v_cvt_f32_fp8_e32 v118, v57
	s_waitcnt vmcnt(0)
	v_cvt_f32_fp8_e32 v119, v58
	v_cvt_f32_fp8_sdwa v120, v57 src0_sel:BYTE_1
	v_cvt_f32_fp8_sdwa v121, v58 src0_sel:BYTE_1
	v_cvt_f32_fp8_sdwa v94, v57 src0_sel:BYTE_2
	v_cvt_f32_fp8_sdwa v95, v57 src0_sel:BYTE_3
	v_cvt_f32_fp8_sdwa v72, v35 src0_sel:BYTE_2
	v_cvt_f32_fp8_sdwa v73, v35 src0_sel:BYTE_3
	v_cvt_f32_fp8_sdwa v76, v39 src0_sel:BYTE_2
	v_cvt_f32_fp8_sdwa v77, v39 src0_sel:BYTE_3
	v_cvt_f32_fp8_sdwa v80, v43 src0_sel:BYTE_2
	v_cvt_f32_fp8_sdwa v81, v43 src0_sel:BYTE_3
	v_cvt_f32_fp8_sdwa v84, v46 src0_sel:BYTE_2
	v_cvt_f32_fp8_sdwa v85, v46 src0_sel:BYTE_3
	v_cvt_f32_fp8_sdwa v88, v50 src0_sel:BYTE_2
	v_cvt_f32_fp8_sdwa v89, v50 src0_sel:BYTE_3
	v_cvt_f32_fp8_sdwa v92, v54 src0_sel:BYTE_2
	v_cvt_f32_fp8_sdwa v93, v54 src0_sel:BYTE_3
	v_cvt_f32_fp8_sdwa v96, v58 src0_sel:BYTE_2
	v_cvt_f32_fp8_sdwa v97, v58 src0_sel:BYTE_3
	v_fmac_f32_e32 v34, v10, v61
	v_mul_f32_e32 v36, v44, v62
	v_fmac_f32_e32 v37, v10, v65
	v_mul_f32_e32 v35, v44, v66
	v_pk_fma_f32 v[18:19], v[10:11], v[8:9], v[18:19] op_sel_hi:[0,1,1]
	v_fmac_f32_e32 v38, v10, v0
	v_mul_f32_e32 v40, v44, v11
	v_fmac_f32_e32 v41, v10, v98
	v_mul_f32_e32 v39, v44, v99
	v_pk_fma_f32 v[20:21], v[10:11], v[70:71], v[20:21] op_sel_hi:[0,1,1]
	v_fmac_f32_e32 v42, v10, v17
	v_mul_f32_e32 v46, v44, v100
	v_fmac_f32_e32 v47, v10, v101
	v_mul_f32_e32 v43, v44, v102
	v_pk_fma_f32 v[70:71], v[10:11], v[74:75], v[22:23] op_sel_hi:[0,1,1]
	v_fmac_f32_e32 v48, v10, v103
	v_mul_f32_e32 v50, v44, v104
	v_fmac_f32_e32 v51, v10, v105
	v_mul_f32_e32 v49, v44, v106
	v_pk_fma_f32 v[74:75], v[10:11], v[78:79], v[24:25] op_sel_hi:[0,1,1]
	v_fmac_f32_e32 v52, v10, v107
	v_mul_f32_e32 v54, v44, v108
	v_fmac_f32_e32 v55, v10, v109
	v_mul_f32_e32 v53, v44, v110
	v_pk_fma_f32 v[78:79], v[10:11], v[82:83], v[26:27] op_sel_hi:[0,1,1]
	v_fmac_f32_e32 v56, v10, v45
	v_mul_f32_e32 v58, v44, v111
	v_fmac_f32_e32 v59, v10, v112
	v_mul_f32_e32 v57, v44, v113
	v_pk_fma_f32 v[82:83], v[10:11], v[86:87], v[28:29] op_sel_hi:[0,1,1]
	v_fmac_f32_e32 v60, v10, v114
	v_mul_f32_e32 v62, v44, v115
	v_fmac_f32_e32 v63, v10, v116
	v_mul_f32_e32 v61, v44, v117
	v_pk_fma_f32 v[86:87], v[10:11], v[90:91], v[30:31] op_sel_hi:[0,1,1]
	v_fmac_f32_e32 v64, v10, v118
	v_mul_f32_e32 v66, v44, v119
	v_fmac_f32_e32 v67, v10, v120
	v_mul_f32_e32 v65, v44, v121
	v_pk_fma_f32 v[90:91], v[10:11], v[94:95], v[32:33] op_sel_hi:[0,1,1]
	v_pk_add_f32 v[8:9], v[36:37], v[34:35]
	v_pk_fma_f32 v[10:11], v[44:45], v[68:69], v[18:19] op_sel_hi:[0,1,1]
	v_pk_add_f32 v[18:19], v[40:41], v[38:39]
	v_pk_fma_f32 v[20:21], v[44:45], v[72:73], v[20:21] op_sel_hi:[0,1,1]
	v_pk_add_f32 v[22:23], v[46:47], v[42:43]
	v_pk_fma_f32 v[24:25], v[44:45], v[76:77], v[70:71] op_sel_hi:[0,1,1]
	v_pk_add_f32 v[26:27], v[50:51], v[48:49]
	v_pk_fma_f32 v[28:29], v[44:45], v[80:81], v[74:75] op_sel_hi:[0,1,1]
	v_pk_add_f32 v[30:31], v[54:55], v[52:53]
	v_pk_fma_f32 v[32:33], v[44:45], v[84:85], v[78:79] op_sel_hi:[0,1,1]
	v_pk_add_f32 v[34:35], v[58:59], v[56:57]
	v_pk_fma_f32 v[36:37], v[44:45], v[88:89], v[82:83] op_sel_hi:[0,1,1]
	v_pk_add_f32 v[38:39], v[62:63], v[60:61]
	v_pk_fma_f32 v[40:41], v[44:45], v[92:93], v[86:87] op_sel_hi:[0,1,1]
	v_pk_add_f32 v[42:43], v[66:67], v[64:65]
	v_pk_fma_f32 v[44:45], v[44:45], v[96:97], v[90:91] op_sel_hi:[0,1,1]
	global_store_dwordx4 v[4:5], v[8:11], off offset:-4096 sc1
	global_store_dwordx4 v[4:5], v[18:21], off offset:-3072 sc1
	global_store_dwordx4 v[4:5], v[22:25], off offset:-2048 sc1
	global_store_dwordx4 v[4:5], v[26:29], off offset:-1024 sc1
	global_store_dwordx4 v[4:5], v[30:33], off sc1
	global_store_dwordx4 v[4:5], v[34:37], off offset:1024 sc1
	global_store_dwordx4 v[4:5], v[38:41], off offset:2048 sc1
	global_store_dwordx4 v[4:5], v[42:45], off offset:3072 sc1
	v_lshl_add_u64 v[4:5], v[4:5], 0, s[4:5]
	s_cbranch_scc1 .LBB0_2051
